# P0 prologue: W_pa items and adaLN mod GEMV request all their rows up front (straight-line bodies, same f32 op order) instead of one memory round trip per 4-8 rows
# baseline (speedup 1.0000x reference)
; __device__ __forceinline__ float sigmoidf_(float x) { return frcp_(1.0f + fexp_(-x)); }
; __device__ __forceinline__ void p0_prologue(const Args& a, const Frame& F) {
;     ...
;         for (int i = F.tid; i < 9 * 1024; i += 512) { const int r = i >> 10, k = i & 1023; const float v = (r < 8) ? a.in[IN_C][r * 1024 + k] : a.in[IN_CCTX][k]; sc[i] = v * sigmoidf_(v); }
;         __syncthreads();
;         const int col = 64 * item + F.lane, k0 = F.wave * 128; const float* W = a.in[IN_WADA] + col;
;         float acc[9];
; #pragma unroll
;         for (int q = 0; q < 9; ++q) acc[q] = 0.f;
;         for (int kk = 0; kk < 128; kk += 8) {
;             float wv[8];
; #pragma unroll
;             for (int u = 0; u < 8; ++u) wv[u] = W[(size_t)(k0 + kk + u) * 6144];
.LBB0_12:
	v_and_b32_e32 v2, 0x3ff, v10
	v_lshlrev_b32_e32 v2, 2, v2
	v_lshl_add_u64 v[12:13], s[42:43], 0, v[2:3]
	v_cmp_gt_u32_e32 vcc, s35, v10
	v_add_u32_e32 v11, 0x200, v10
	s_nop 0
	v_cndmask_b32_e32 v13, v13, v9, vcc
	v_cndmask_b32_e32 v12, v12, v8, vcc
	global_load_dword v2, v[12:13], off
	v_cmp_lt_u32_e32 vcc, s44, v10
	s_or_b64 s[14:15], vcc, s[14:15]
	v_lshl_add_u64 v[8:9], v[8:9], 0, s[10:11]
	s_waitcnt vmcnt(0)
	v_mul_f32_e32 v12, 0xbfb8aa3b, v2
	v_exp_f32_e32 v12, v12
	s_nop 0
	v_add_f32_e32 v10, 1.0, v12
	v_rcp_f32_e32 v12, v10
	v_mov_b32_e32 v10, v11
	v_mul_f32_e32 v2, v2, v12
	ds_write_b32 v7, v2
	v_add_u32_e32 v7, 0x800, v7
	s_andn2_b64 exec, exec, s[14:15]
	s_cbranch_execnz .LBB0_12
	s_or_b64 exec, exec, s[14:15]
	v_ashrrev_i32_e32 v7, 31, v6
	v_mov_b32_e32 v10, 0
	v_lshl_add_u64 v[8:9], v[6:7], 2, s[8:9]
	v_mov_b64_e32 v[248:249], v[8:9]
	s_mov_b64 s[98:99], 0x6000
	global_load_dword v120, v[248:249], off
	v_lshl_add_u64 v[248:249], v[248:249], 0, s[98:99]
	global_load_dword v121, v[248:249], off
	v_lshl_add_u64 v[248:249], v[248:249], 0, s[98:99]
	global_load_dword v122, v[248:249], off
	v_lshl_add_u64 v[248:249], v[248:249], 0, s[98:99]
	global_load_dword v123, v[248:249], off
	v_lshl_add_u64 v[248:249], v[248:249], 0, s[98:99]
	global_load_dword v124, v[248:249], off
	v_lshl_add_u64 v[248:249], v[248:249], 0, s[98:99]
	global_load_dword v125, v[248:249], off
	v_lshl_add_u64 v[248:249], v[248:249], 0, s[98:99]
	global_load_dword v126, v[248:249], off
	v_lshl_add_u64 v[248:249], v[248:249], 0, s[98:99]
	global_load_dword v127, v[248:249], off
	v_lshl_add_u64 v[248:249], v[248:249], 0, s[98:99]
	global_load_dword v128, v[248:249], off
	v_lshl_add_u64 v[248:249], v[248:249], 0, s[98:99]
	global_load_dword v129, v[248:249], off
	v_lshl_add_u64 v[248:249], v[248:249], 0, s[98:99]
	global_load_dword v130, v[248:249], off
	v_lshl_add_u64 v[248:249], v[248:249], 0, s[98:99]
	global_load_dword v131, v[248:249], off
	v_lshl_add_u64 v[248:249], v[248:249], 0, s[98:99]
	global_load_dword v132, v[248:249], off
	v_lshl_add_u64 v[248:249], v[248:249], 0, s[98:99]
	global_load_dword v133, v[248:249], off
	v_lshl_add_u64 v[248:249], v[248:249], 0, s[98:99]
	global_load_dword v134, v[248:249], off
	v_lshl_add_u64 v[248:249], v[248:249], 0, s[98:99]
	global_load_dword v135, v[248:249], off
	v_lshl_add_u64 v[248:249], v[248:249], 0, s[98:99]
	global_load_dword v136, v[248:249], off
	v_lshl_add_u64 v[248:249], v[248:249], 0, s[98:99]
	global_load_dword v137, v[248:249], off
	v_lshl_add_u64 v[248:249], v[248:249], 0, s[98:99]
	global_load_dword v138, v[248:249], off
	v_lshl_add_u64 v[248:249], v[248:249], 0, s[98:99]
	global_load_dword v139, v[248:249], off
	v_lshl_add_u64 v[248:249], v[248:249], 0, s[98:99]
	global_load_dword v140, v[248:249], off
	v_lshl_add_u64 v[248:249], v[248:249], 0, s[98:99]
	global_load_dword v141, v[248:249], off
	v_lshl_add_u64 v[248:249], v[248:249], 0, s[98:99]
	global_load_dword v142, v[248:249], off
	v_lshl_add_u64 v[248:249], v[248:249], 0, s[98:99]
	global_load_dword v143, v[248:249], off
	v_lshl_add_u64 v[248:249], v[248:249], 0, s[98:99]
	global_load_dword v144, v[248:249], off
	v_lshl_add_u64 v[248:249], v[248:249], 0, s[98:99]
	global_load_dword v145, v[248:249], off
	v_lshl_add_u64 v[248:249], v[248:249], 0, s[98:99]
	global_load_dword v146, v[248:249], off
	v_lshl_add_u64 v[248:249], v[248:249], 0, s[98:99]
	global_load_dword v147, v[248:249], off
	v_lshl_add_u64 v[248:249], v[248:249], 0, s[98:99]
	global_load_dword v148, v[248:249], off
	v_lshl_add_u64 v[248:249], v[248:249], 0, s[98:99]
	global_load_dword v149, v[248:249], off
	v_lshl_add_u64 v[248:249], v[248:249], 0, s[98:99]
	global_load_dword v150, v[248:249], off
	v_lshl_add_u64 v[248:249], v[248:249], 0, s[98:99]
	global_load_dword v151, v[248:249], off
	v_lshl_add_u64 v[248:249], v[248:249], 0, s[98:99]
	global_load_dword v152, v[248:249], off
	v_lshl_add_u64 v[248:249], v[248:249], 0, s[98:99]
	global_load_dword v153, v[248:249], off
	v_lshl_add_u64 v[248:249], v[248:249], 0, s[98:99]
	global_load_dword v154, v[248:249], off
	v_lshl_add_u64 v[248:249], v[248:249], 0, s[98:99]
	global_load_dword v155, v[248:249], off
	v_lshl_add_u64 v[248:249], v[248:249], 0, s[98:99]
	global_load_dword v156, v[248:249], off
	v_lshl_add_u64 v[248:249], v[248:249], 0, s[98:99]
	global_load_dword v157, v[248:249], off
	v_lshl_add_u64 v[248:249], v[248:249], 0, s[98:99]
	global_load_dword v158, v[248:249], off
	v_lshl_add_u64 v[248:249], v[248:249], 0, s[98:99]
	global_load_dword v159, v[248:249], off
	v_lshl_add_u64 v[248:249], v[248:249], 0, s[98:99]
	global_load_dword v160, v[248:249], off
	v_lshl_add_u64 v[248:249], v[248:249], 0, s[98:99]
	global_load_dword v161, v[248:249], off
	v_lshl_add_u64 v[248:249], v[248:249], 0, s[98:99]
	global_load_dword v162, v[248:249], off
	v_lshl_add_u64 v[248:249], v[248:249], 0, s[98:99]
	global_load_dword v163, v[248:249], off
	v_lshl_add_u64 v[248:249], v[248:249], 0, s[98:99]
	global_load_dword v164, v[248:249], off
	v_lshl_add_u64 v[248:249], v[248:249], 0, s[98:99]
	global_load_dword v165, v[248:249], off
	v_lshl_add_u64 v[248:249], v[248:249], 0, s[98:99]
	global_load_dword v166, v[248:249], off
	v_lshl_add_u64 v[248:249], v[248:249], 0, s[98:99]
	global_load_dword v167, v[248:249], off
	v_lshl_add_u64 v[248:249], v[248:249], 0, s[98:99]
	global_load_dword v168, v[248:249], off
	v_lshl_add_u64 v[248:249], v[248:249], 0, s[98:99]
	global_load_dword v169, v[248:249], off
	v_lshl_add_u64 v[248:249], v[248:249], 0, s[98:99]
	global_load_dword v170, v[248:249], off
	v_lshl_add_u64 v[248:249], v[248:249], 0, s[98:99]
; __device__ __forceinline__ void p0_prologue(const Args& a, const Frame& F) {
;     ...
;         for (int kk = 0; kk < 128; kk += 8) {
;             float wv[8];
; #pragma unroll
;             for (int u = 0; u < 8; ++u) wv[u] = W[(size_t)(k0 + kk + u) * 6144];
	global_load_dword v171, v[248:249], off
	v_lshl_add_u64 v[248:249], v[248:249], 0, s[98:99]
	global_load_dword v172, v[248:249], off
	v_lshl_add_u64 v[248:249], v[248:249], 0, s[98:99]
	global_load_dword v173, v[248:249], off
	v_lshl_add_u64 v[248:249], v[248:249], 0, s[98:99]
	global_load_dword v174, v[248:249], off
	v_lshl_add_u64 v[248:249], v[248:249], 0, s[98:99]
	global_load_dword v175, v[248:249], off
	v_lshl_add_u64 v[248:249], v[248:249], 0, s[98:99]
	global_load_dword v176, v[248:249], off
	v_lshl_add_u64 v[248:249], v[248:249], 0, s[98:99]
	global_load_dword v177, v[248:249], off
	v_lshl_add_u64 v[248:249], v[248:249], 0, s[98:99]
	global_load_dword v178, v[248:249], off
	v_lshl_add_u64 v[248:249], v[248:249], 0, s[98:99]
	global_load_dword v179, v[248:249], off
	v_lshl_add_u64 v[248:249], v[248:249], 0, s[98:99]
	global_load_dword v180, v[248:249], off
	v_lshl_add_u64 v[248:249], v[248:249], 0, s[98:99]
	global_load_dword v181, v[248:249], off
	v_lshl_add_u64 v[248:249], v[248:249], 0, s[98:99]
	global_load_dword v182, v[248:249], off
	v_lshl_add_u64 v[248:249], v[248:249], 0, s[98:99]
	global_load_dword v183, v[248:249], off
	v_lshl_add_u64 v[248:249], v[248:249], 0, s[98:99]
	global_load_dword v184, v[248:249], off
	v_lshl_add_u64 v[248:249], v[248:249], 0, s[98:99]
	global_load_dword v185, v[248:249], off
	v_lshl_add_u64 v[248:249], v[248:249], 0, s[98:99]
	global_load_dword v186, v[248:249], off
	v_lshl_add_u64 v[248:249], v[248:249], 0, s[98:99]
	global_load_dword v187, v[248:249], off
	v_lshl_add_u64 v[248:249], v[248:249], 0, s[98:99]
	global_load_dword v188, v[248:249], off
	v_lshl_add_u64 v[248:249], v[248:249], 0, s[98:99]
	global_load_dword v189, v[248:249], off
	v_lshl_add_u64 v[248:249], v[248:249], 0, s[98:99]
	global_load_dword v190, v[248:249], off
	v_lshl_add_u64 v[248:249], v[248:249], 0, s[98:99]
	global_load_dword v191, v[248:249], off
	v_lshl_add_u64 v[248:249], v[248:249], 0, s[98:99]
	global_load_dword v192, v[248:249], off
	v_lshl_add_u64 v[248:249], v[248:249], 0, s[98:99]
	global_load_dword v193, v[248:249], off
	v_lshl_add_u64 v[248:249], v[248:249], 0, s[98:99]
	global_load_dword v194, v[248:249], off
	v_lshl_add_u64 v[248:249], v[248:249], 0, s[98:99]
	global_load_dword v195, v[248:249], off
	v_lshl_add_u64 v[248:249], v[248:249], 0, s[98:99]
	global_load_dword v196, v[248:249], off
	v_lshl_add_u64 v[248:249], v[248:249], 0, s[98:99]
	global_load_dword v197, v[248:249], off
	v_lshl_add_u64 v[248:249], v[248:249], 0, s[98:99]
	global_load_dword v198, v[248:249], off
	v_lshl_add_u64 v[248:249], v[248:249], 0, s[98:99]
	global_load_dword v199, v[248:249], off
	v_lshl_add_u64 v[248:249], v[248:249], 0, s[98:99]
	global_load_dword v200, v[248:249], off
	v_lshl_add_u64 v[248:249], v[248:249], 0, s[98:99]
	global_load_dword v201, v[248:249], off
	v_lshl_add_u64 v[248:249], v[248:249], 0, s[98:99]
	global_load_dword v202, v[248:249], off
	v_lshl_add_u64 v[248:249], v[248:249], 0, s[98:99]
	global_load_dword v203, v[248:249], off
	v_lshl_add_u64 v[248:249], v[248:249], 0, s[98:99]
	global_load_dword v204, v[248:249], off
	v_lshl_add_u64 v[248:249], v[248:249], 0, s[98:99]
	global_load_dword v205, v[248:249], off
	v_lshl_add_u64 v[248:249], v[248:249], 0, s[98:99]
	global_load_dword v206, v[248:249], off
	v_lshl_add_u64 v[248:249], v[248:249], 0, s[98:99]
	global_load_dword v207, v[248:249], off
	v_lshl_add_u64 v[248:249], v[248:249], 0, s[98:99]
	global_load_dword v208, v[248:249], off
	v_lshl_add_u64 v[248:249], v[248:249], 0, s[98:99]
	global_load_dword v209, v[248:249], off
	v_lshl_add_u64 v[248:249], v[248:249], 0, s[98:99]
	global_load_dword v210, v[248:249], off
	v_lshl_add_u64 v[248:249], v[248:249], 0, s[98:99]
	global_load_dword v211, v[248:249], off
	v_lshl_add_u64 v[248:249], v[248:249], 0, s[98:99]
	global_load_dword v212, v[248:249], off
	v_lshl_add_u64 v[248:249], v[248:249], 0, s[98:99]
	global_load_dword v213, v[248:249], off
	v_lshl_add_u64 v[248:249], v[248:249], 0, s[98:99]
	global_load_dword v214, v[248:249], off
	v_lshl_add_u64 v[248:249], v[248:249], 0, s[98:99]
	global_load_dword v215, v[248:249], off
	v_lshl_add_u64 v[248:249], v[248:249], 0, s[98:99]
	global_load_dword v216, v[248:249], off
	v_lshl_add_u64 v[248:249], v[248:249], 0, s[98:99]
	global_load_dword v217, v[248:249], off
	v_lshl_add_u64 v[248:249], v[248:249], 0, s[98:99]
	global_load_dword v218, v[248:249], off
	v_lshl_add_u64 v[248:249], v[248:249], 0, s[98:99]
	global_load_dword v219, v[248:249], off
	v_lshl_add_u64 v[248:249], v[248:249], 0, s[98:99]
	global_load_dword v220, v[248:249], off
	v_lshl_add_u64 v[248:249], v[248:249], 0, s[98:99]
	global_load_dword v221, v[248:249], off
	v_lshl_add_u64 v[248:249], v[248:249], 0, s[98:99]
	global_load_dword v222, v[248:249], off
	v_lshl_add_u64 v[248:249], v[248:249], 0, s[98:99]
	global_load_dword v223, v[248:249], off
	v_lshl_add_u64 v[248:249], v[248:249], 0, s[98:99]
	global_load_dword v224, v[248:249], off
	v_lshl_add_u64 v[248:249], v[248:249], 0, s[98:99]
	global_load_dword v225, v[248:249], off
	v_lshl_add_u64 v[248:249], v[248:249], 0, s[98:99]
	global_load_dword v226, v[248:249], off
	v_lshl_add_u64 v[248:249], v[248:249], 0, s[98:99]
	global_load_dword v227, v[248:249], off
	v_lshl_add_u64 v[248:249], v[248:249], 0, s[98:99]
	global_load_dword v228, v[248:249], off
	v_lshl_add_u64 v[248:249], v[248:249], 0, s[98:99]
	global_load_dword v229, v[248:249], off
	v_lshl_add_u64 v[248:249], v[248:249], 0, s[98:99]
	global_load_dword v230, v[248:249], off
	v_lshl_add_u64 v[248:249], v[248:249], 0, s[98:99]
	global_load_dword v231, v[248:249], off
; #define LAS __attribute__((address_space(3)))
; __device__ __forceinline__ void p0_prologue(const Args& a, const Frame& F) {
;     ...
;         float acc[9];
; #pragma unroll
;         for (int q = 0; q < 9; ++q) acc[q] = 0.f;
;         for (int kk = 0; kk < 128; kk += 8) {
;             float wv[8];
; #pragma unroll
;             for (int u = 0; u < 8; ++u) wv[u] = W[(size_t)(k0 + kk + u) * 6144];
; #pragma unroll
;             for (int q = 0; q < 9; ++q) { const f32x4 s0 = *(const LAS f32x4*)(sc + q * 1024 + k0 + kk), s1 = *(const LAS f32x4*)(sc + q * 1024 + k0 + kk + 4);
;                 acc[q] += (s0.x * wv[0] + s0.y * wv[1]) + (s0.z * wv[2] + s0.w * wv[3]) + (s1.x * wv[4] + s1.y * wv[5]) + (s1.z * wv[6] + s1.w * wv[7]); }
;         }
	v_lshl_add_u64 v[248:249], v[248:249], 0, s[98:99]
	global_load_dword v232, v[248:249], off
	v_lshl_add_u64 v[248:249], v[248:249], 0, s[98:99]
	global_load_dword v233, v[248:249], off
	v_lshl_add_u64 v[248:249], v[248:249], 0, s[98:99]
	global_load_dword v234, v[248:249], off
	v_lshl_add_u64 v[248:249], v[248:249], 0, s[98:99]
	global_load_dword v235, v[248:249], off
	v_lshl_add_u64 v[248:249], v[248:249], 0, s[98:99]
	global_load_dword v236, v[248:249], off
	v_lshl_add_u64 v[248:249], v[248:249], 0, s[98:99]
	global_load_dword v237, v[248:249], off
	v_lshl_add_u64 v[248:249], v[248:249], 0, s[98:99]
	global_load_dword v238, v[248:249], off
	v_lshl_add_u64 v[248:249], v[248:249], 0, s[98:99]
	global_load_dword v239, v[248:249], off
	v_lshl_add_u64 v[248:249], v[248:249], 0, s[98:99]
	global_load_dword v240, v[248:249], off
	v_lshl_add_u64 v[248:249], v[248:249], 0, s[98:99]
	global_load_dword v241, v[248:249], off
	v_lshl_add_u64 v[248:249], v[248:249], 0, s[98:99]
	global_load_dword v242, v[248:249], off
	v_lshl_add_u64 v[248:249], v[248:249], 0, s[98:99]
	global_load_dword v243, v[248:249], off
	v_lshl_add_u64 v[248:249], v[248:249], 0, s[98:99]
	global_load_dword v244, v[248:249], off
	v_lshl_add_u64 v[248:249], v[248:249], 0, s[98:99]
	global_load_dword v245, v[248:249], off
	v_lshl_add_u64 v[248:249], v[248:249], 0, s[98:99]
	global_load_dword v246, v[248:249], off
	v_lshl_add_u64 v[248:249], v[248:249], 0, s[98:99]
	global_load_dword v247, v[248:249], off
	s_mov_b32 s14, -8
	s_mov_b32 s15, s33
	v_mov_b32_e32 v11, v10
	v_mov_b32_e32 v12, v10
	v_mov_b32_e32 v13, v10
	v_mov_b32_e32 v14, v10
	v_mov_b32_e32 v15, v10
	v_mov_b32_e32 v16, v10
	v_mov_b32_e32 v17, v10
	v_mov_b32_e32 v2, v10
	s_waitcnt lgkmcnt(0)
	s_barrier
	s_waitcnt vmcnt(63)
	v_add_co_u32_e32 v94, vcc, 0x6000, v8
	v_mov_b32_e32 v7, s15
	s_nop 0
	v_addc_co_u32_e32 v95, vcc, 0, v9, vcc
	v_add_co_u32_e32 v98, vcc, 0xc000, v8
	v_mov_b32_e32 v96, v120
	s_nop 0
	v_addc_co_u32_e32 v99, vcc, 0, v9, vcc
	v_add_co_u32_e32 v100, vcc, 0x12000, v8
	ds_read_b128 v[22:25], v7
	ds_read_b128 v[26:29], v7 offset:16
	ds_read_b128 v[30:33], v7 offset:4096
	ds_read_b128 v[34:37], v7 offset:4112
	ds_read_b128 v[38:41], v7 offset:8192
	ds_read_b128 v[42:45], v7 offset:8208
	ds_read_b128 v[46:49], v7 offset:12288
	ds_read_b128 v[50:53], v7 offset:12304
	ds_read_b128 v[54:57], v7 offset:16384
	ds_read_b128 v[58:61], v7 offset:16400
	ds_read_b128 v[62:65], v7 offset:20480
	ds_read_b128 v[66:69], v7 offset:20496
	ds_read_b128 v[70:73], v7 offset:24576
	ds_read_b128 v[74:77], v7 offset:24592
	ds_read_b128 v[78:81], v7 offset:28672
	ds_read_b128 v[82:85], v7 offset:28688
	v_addc_co_u32_e32 v101, vcc, 0, v9, vcc
	v_add_co_u32_e32 v102, vcc, 0x18000, v8
	ds_read_b128 v[86:89], v7 offset:32768
	ds_read_b128 v[90:93], v7 offset:32784
	v_addc_co_u32_e32 v103, vcc, 0, v9, vcc
	v_mov_b32_e32 v94, v121
	v_add_co_u32_e32 v104, vcc, 0x1e000, v8
	v_mov_b32_e32 v98, v122
	s_nop 0
	v_mov_b32_e32 v100, v123
	v_addc_co_u32_e32 v105, vcc, 0, v9, vcc
	v_add_co_u32_e32 v106, vcc, 0x24000, v8
	v_mov_b32_e32 v102, v124
	s_waitcnt lgkmcnt(14)
	v_mov_b32_e32 v108, v22
	v_mov_b32_e32 v22, v24
	v_mov_b32_e32 v24, v26
	v_mov_b32_e32 v26, v28
	s_waitcnt lgkmcnt(13)
	v_mov_b32_e32 v28, v38
	v_mov_b32_e32 v38, v40
	s_waitcnt lgkmcnt(12)
	v_mov_b32_e32 v40, v42
	v_mov_b32_e32 v42, v44
	s_waitcnt lgkmcnt(9)
	v_mov_b32_e32 v44, v54
	v_mov_b32_e32 v54, v56
	v_mov_b32_e32 v56, v125
	v_addc_co_u32_e32 v107, vcc, 0, v9, vcc
	v_add_co_u32_e32 v104, vcc, 0x2a000, v8
	v_mov_b32_e32 v109, v30
	s_nop 0
	v_addc_co_u32_e32 v105, vcc, 0, v9, vcc
	v_mov_b32_e32 v106, v126
	s_nop 0
	v_mov_b32_e32 v104, v127
	v_mov_b32_e32 v30, v23
	v_mov_b32_e32 v23, v32
	v_mov_b32_e32 v32, v25
	v_mov_b32_e32 v25, v34
	v_mov_b32_e32 v34, v27
	v_mov_b32_e32 v27, v36
	v_mov_b32_e32 v36, v29
	v_mov_b32_e32 v29, v46
	v_mov_b32_e32 v46, v39
	s_waitcnt lgkmcnt(6)
	v_mov_b32_e32 v111, v66
	v_mov_b32_e32 v66, v59
	v_mov_b32_e32 v59, v68
	v_mov_b32_e32 v68, v61
	s_waitcnt lgkmcnt(3)
	v_mov_b32_e32 v61, v78
	v_mov_b32_e32 v78, v71
	v_mov_b32_e32 v39, v48
	v_mov_b32_e32 v48, v41
	v_mov_b32_e32 v41, v50
	v_mov_b32_e32 v50, v43
	v_mov_b32_e32 v43, v52
	v_mov_b32_e32 v52, v45
	v_mov_b32_e32 v45, v62
	v_mov_b32_e32 v62, v55
	v_mov_b32_e32 v55, v64
	v_mov_b32_e32 v64, v57
	v_mov_b32_e32 v110, v58
	v_mov_b32_e32 v58, v60
	v_mov_b32_e32 v60, v70
	v_mov_b32_e32 v71, v80
	v_mov_b32_e32 v80, v73
	v_mov_b32_e32 v70, v72
	v_mov_b32_e32 v72, v74
	s_waitcnt lgkmcnt(2)
	v_mov_b32_e32 v73, v82
	v_mov_b32_e32 v82, v75
	v_mov_b32_e32 v74, v76
	v_mov_b32_e32 v75, v84
	v_mov_b32_e32 v84, v77
	s_waitcnt lgkmcnt(1)
	v_mov_b32_e32 v76, v87
	v_mov_b32_e32 v87, v89
	v_mov_b32_e32 v77, v88
	s_waitcnt lgkmcnt(0)
; #define LAS __attribute__((address_space(3)))
; __device__ __forceinline__ void p0_prologue(const Args& a, const Frame& F) {
;     ...
;         for (int kk = 0; kk < 128; kk += 8) {
;             float wv[8];
; #pragma unroll
;             for (int u = 0; u < 8; ++u) wv[u] = W[(size_t)(k0 + kk + u) * 6144];
; #pragma unroll
;             for (int q = 0; q < 9; ++q) { const f32x4 s0 = *(const LAS f32x4*)(sc + q * 1024 + k0 + kk), s1 = *(const LAS f32x4*)(sc + q * 1024 + k0 + kk + 4);
;                 acc[q] += (s0.x * wv[0] + s0.y * wv[1]) + (s0.z * wv[2] + s0.w * wv[3]) + (s1.x * wv[4] + s1.y * wv[5]) + (s1.z * wv[6] + s1.w * wv[7]); }
;         }
	v_mov_b32_e32 v89, v90
	v_mov_b32_e32 v90, v93
	v_mov_b32_e32 v88, v92
	s_add_i32 s14, s14, 8
	s_add_i32 s15, s15, 32
	s_cmpk_gt_u32 s14, 0x77
	v_lshl_add_u64 v[8:9], v[8:9], 0, s[12:13]
	v_pk_mul_f32 v[46:47], v[94:95], v[46:47] op_sel_hi:[0,1]
	v_pk_mul_f32 v[78:79], v[94:95], v[78:79] op_sel_hi:[0,1]
	v_pk_mul_f32 v[30:31], v[94:95], v[30:31] op_sel_hi:[0,1]
	v_pk_mul_f32 v[62:63], v[94:95], v[62:63] op_sel_hi:[0,1]
	v_pk_fma_f32 v[28:29], v[96:97], v[28:29], v[46:47] op_sel_hi:[0,1,1]
	v_pk_fma_f32 v[46:47], v[96:97], v[60:61], v[78:79] op_sel_hi:[0,1,1]
	v_pk_mul_f32 v[32:33], v[100:101], v[32:33] op_sel_hi:[0,1]
	v_pk_mul_f32 v[48:49], v[100:101], v[48:49] op_sel_hi:[0,1]
	v_pk_mul_f32 v[60:61], v[100:101], v[64:65] op_sel_hi:[0,1]
	v_pk_fma_f32 v[30:31], v[96:97], v[108:109], v[30:31] op_sel_hi:[0,1,1]
	v_pk_fma_f32 v[44:45], v[96:97], v[44:45], v[62:63] op_sel_hi:[0,1,1]
	v_pk_fma_f32 v[22:23], v[98:99], v[22:23], v[32:33] op_sel_hi:[0,1,1]
	v_pk_fma_f32 v[32:33], v[98:99], v[38:39], v[48:49] op_sel_hi:[0,1,1]
	v_pk_fma_f32 v[38:39], v[98:99], v[54:55], v[60:61] op_sel_hi:[0,1,1]
	v_pk_add_f32 v[22:23], v[30:31], v[22:23]
	v_pk_add_f32 v[30:31], v[44:45], v[38:39]
	v_pk_mul_f32 v[62:63], v[100:101], v[80:81] op_sel_hi:[0,1]
	v_mov_b32_e32 v97, v100
	v_pk_add_f32 v[28:29], v[28:29], v[32:33]
	v_pk_mul_f32 v[34:35], v[56:57], v[34:35] op_sel_hi:[0,1]
	v_pk_mul_f32 v[38:39], v[56:57], v[50:51] op_sel_hi:[0,1]
	v_pk_mul_f32 v[44:45], v[56:57], v[66:67] op_sel_hi:[0,1]
	v_pk_fma_f32 v[24:25], v[102:103], v[24:25], v[34:35] op_sel_hi:[0,1,1]
	v_pk_fma_f32 v[34:35], v[102:103], v[40:41], v[38:39] op_sel_hi:[0,1,1]
	v_pk_fma_f32 v[38:39], v[102:103], v[110:111], v[44:45] op_sel_hi:[0,1,1]
	v_mov_b32_e32 v95, v98
	v_pk_mul_f32 v[64:65], v[96:97], v[86:87]
	v_pk_fma_f32 v[48:49], v[98:99], v[70:71], v[62:63] op_sel_hi:[0,1,1]
	v_pk_add_f32 v[22:23], v[22:23], v[24:25]
	v_pk_mul_f32 v[24:25], v[104:105], v[36:37] op_sel_hi:[0,1]
	v_pk_add_f32 v[28:29], v[28:29], v[34:35]
	v_pk_mul_f32 v[34:35], v[104:105], v[52:53] op_sel_hi:[0,1]
	v_pk_add_f32 v[30:31], v[30:31], v[38:39]
	v_pk_mul_f32 v[36:37], v[104:105], v[68:69] op_sel_hi:[0,1]
	v_pk_mul_f32 v[38:39], v[104:105], v[84:85] op_sel_hi:[0,1]
	v_mov_b32_e32 v105, v56
	v_pk_fma_f32 v[54:55], v[94:95], v[76:77], v[64:65]
	v_pk_add_f32 v[32:33], v[46:47], v[48:49]
	v_pk_mul_f32 v[46:47], v[56:57], v[82:83] op_sel_hi:[0,1]
	v_pk_fma_f32 v[24:25], v[106:107], v[26:27], v[24:25] op_sel_hi:[0,1,1]
	v_pk_fma_f32 v[26:27], v[106:107], v[42:43], v[34:35] op_sel_hi:[0,1,1]
	v_pk_fma_f32 v[34:35], v[106:107], v[58:59], v[36:37] op_sel_hi:[0,1,1]
	v_pk_fma_f32 v[36:37], v[106:107], v[74:75], v[38:39] op_sel_hi:[0,1,1]
	v_mov_b32_e32 v107, v102
	v_pk_mul_f32 v[38:39], v[104:105], v[90:91]
	v_pk_fma_f32 v[40:41], v[102:103], v[72:73], v[46:47] op_sel_hi:[0,1,1]
	v_add_f32_e32 v7, v54, v55
	v_pk_add_f32 v[22:23], v[24:25], v[22:23]
	v_pk_add_f32 v[24:25], v[26:27], v[28:29]
	v_pk_add_f32 v[26:27], v[34:35], v[30:31]
	v_pk_fma_f32 v[30:31], v[106:107], v[88:89], v[38:39]
	v_pk_add_f32 v[32:33], v[32:33], v[40:41]
	v_add_f32_e32 v7, v7, v31
	v_pk_add_f32 v[28:29], v[36:37], v[32:33]
	v_add_f32_e32 v7, v30, v7
	v_pk_add_f32 v[10:11], v[10:11], v[22:23]
	v_pk_add_f32 v[12:13], v[12:13], v[24:25]
	v_pk_add_f32 v[14:15], v[14:15], v[26:27]
	v_pk_add_f32 v[16:17], v[16:17], v[28:29]
	v_add_f32_e32 v2, v2, v7
	s_waitcnt vmcnt(63)
	v_add_co_u32_e32 v94, vcc, 0x6000, v8
	v_mov_b32_e32 v7, s15
	s_nop 0
	v_addc_co_u32_e32 v95, vcc, 0, v9, vcc
	v_add_co_u32_e32 v98, vcc, 0xc000, v8
	v_mov_b32_e32 v96, v128
	s_nop 0
	v_addc_co_u32_e32 v99, vcc, 0, v9, vcc
	v_add_co_u32_e32 v100, vcc, 0x12000, v8
	ds_read_b128 v[22:25], v7
	ds_read_b128 v[26:29], v7 offset:16
	ds_read_b128 v[30:33], v7 offset:4096
	ds_read_b128 v[34:37], v7 offset:4112
	ds_read_b128 v[38:41], v7 offset:8192
	ds_read_b128 v[42:45], v7 offset:8208
	ds_read_b128 v[46:49], v7 offset:12288
	ds_read_b128 v[50:53], v7 offset:12304
	ds_read_b128 v[54:57], v7 offset:16384
	ds_read_b128 v[58:61], v7 offset:16400
	ds_read_b128 v[62:65], v7 offset:20480
	ds_read_b128 v[66:69], v7 offset:20496
	ds_read_b128 v[70:73], v7 offset:24576
	ds_read_b128 v[74:77], v7 offset:24592
	ds_read_b128 v[78:81], v7 offset:28672
	ds_read_b128 v[82:85], v7 offset:28688
	v_addc_co_u32_e32 v101, vcc, 0, v9, vcc
	v_add_co_u32_e32 v102, vcc, 0x18000, v8
	ds_read_b128 v[86:89], v7 offset:32768
	ds_read_b128 v[90:93], v7 offset:32784
	v_addc_co_u32_e32 v103, vcc, 0, v9, vcc
	v_mov_b32_e32 v94, v129
	v_add_co_u32_e32 v104, vcc, 0x1e000, v8
	v_mov_b32_e32 v98, v130
	s_nop 0
	v_mov_b32_e32 v100, v131
	v_addc_co_u32_e32 v105, vcc, 0, v9, vcc
	v_add_co_u32_e32 v106, vcc, 0x24000, v8
	v_mov_b32_e32 v102, v132
	s_waitcnt lgkmcnt(14)
	v_mov_b32_e32 v108, v22
	v_mov_b32_e32 v22, v24
	v_mov_b32_e32 v24, v26
	v_mov_b32_e32 v26, v28
	s_waitcnt lgkmcnt(13)
	v_mov_b32_e32 v28, v38
	v_mov_b32_e32 v38, v40
	s_waitcnt lgkmcnt(12)
	v_mov_b32_e32 v40, v42
	v_mov_b32_e32 v42, v44
	s_waitcnt lgkmcnt(9)
	v_mov_b32_e32 v44, v54
	v_mov_b32_e32 v54, v56
	v_mov_b32_e32 v56, v133
	v_addc_co_u32_e32 v107, vcc, 0, v9, vcc
	v_add_co_u32_e32 v104, vcc, 0x2a000, v8
	v_mov_b32_e32 v109, v30
	s_nop 0
	v_addc_co_u32_e32 v105, vcc, 0, v9, vcc
	v_mov_b32_e32 v106, v134
	s_nop 0
	v_mov_b32_e32 v104, v135
	v_mov_b32_e32 v30, v23
	v_mov_b32_e32 v23, v32
	v_mov_b32_e32 v32, v25
	v_mov_b32_e32 v25, v34
	v_mov_b32_e32 v34, v27
	v_mov_b32_e32 v27, v36
	v_mov_b32_e32 v36, v29
	v_mov_b32_e32 v29, v46
	v_mov_b32_e32 v46, v39
	s_waitcnt lgkmcnt(6)
	v_mov_b32_e32 v111, v66
	v_mov_b32_e32 v66, v59
	v_mov_b32_e32 v59, v68
	v_mov_b32_e32 v68, v61
	s_waitcnt lgkmcnt(3)
; #define LAS __attribute__((address_space(3)))
; __device__ __forceinline__ void p0_prologue(const Args& a, const Frame& F) {
;     ...
;         for (int kk = 0; kk < 128; kk += 8) {
;             float wv[8];
; #pragma unroll
;             for (int u = 0; u < 8; ++u) wv[u] = W[(size_t)(k0 + kk + u) * 6144];
; #pragma unroll
;             for (int q = 0; q < 9; ++q) { const f32x4 s0 = *(const LAS f32x4*)(sc + q * 1024 + k0 + kk), s1 = *(const LAS f32x4*)(sc + q * 1024 + k0 + kk + 4);
;                 acc[q] += (s0.x * wv[0] + s0.y * wv[1]) + (s0.z * wv[2] + s0.w * wv[3]) + (s1.x * wv[4] + s1.y * wv[5]) + (s1.z * wv[6] + s1.w * wv[7]); }
;         }
	v_mov_b32_e32 v61, v78
	v_mov_b32_e32 v78, v71
	v_mov_b32_e32 v39, v48
	v_mov_b32_e32 v48, v41
	v_mov_b32_e32 v41, v50
	v_mov_b32_e32 v50, v43
	v_mov_b32_e32 v43, v52
	v_mov_b32_e32 v52, v45
	v_mov_b32_e32 v45, v62
	v_mov_b32_e32 v62, v55
	v_mov_b32_e32 v55, v64
	v_mov_b32_e32 v64, v57
	v_mov_b32_e32 v110, v58
	v_mov_b32_e32 v58, v60
	v_mov_b32_e32 v60, v70
	v_mov_b32_e32 v71, v80
	v_mov_b32_e32 v80, v73
	v_mov_b32_e32 v70, v72
	v_mov_b32_e32 v72, v74
	s_waitcnt lgkmcnt(2)
	v_mov_b32_e32 v73, v82
	v_mov_b32_e32 v82, v75
	v_mov_b32_e32 v74, v76
	v_mov_b32_e32 v75, v84
	v_mov_b32_e32 v84, v77
	s_waitcnt lgkmcnt(1)
	v_mov_b32_e32 v76, v87
	v_mov_b32_e32 v87, v89
	v_mov_b32_e32 v77, v88
	s_waitcnt lgkmcnt(0)
	v_mov_b32_e32 v89, v90
	v_mov_b32_e32 v90, v93
	v_mov_b32_e32 v88, v92
	s_add_i32 s14, s14, 8
	s_add_i32 s15, s15, 32
	s_cmpk_gt_u32 s14, 0x77
	v_lshl_add_u64 v[8:9], v[8:9], 0, s[12:13]
	v_pk_mul_f32 v[46:47], v[94:95], v[46:47] op_sel_hi:[0,1]
	v_pk_mul_f32 v[78:79], v[94:95], v[78:79] op_sel_hi:[0,1]
	v_pk_mul_f32 v[30:31], v[94:95], v[30:31] op_sel_hi:[0,1]
	v_pk_mul_f32 v[62:63], v[94:95], v[62:63] op_sel_hi:[0,1]
	v_pk_fma_f32 v[28:29], v[96:97], v[28:29], v[46:47] op_sel_hi:[0,1,1]
	v_pk_fma_f32 v[46:47], v[96:97], v[60:61], v[78:79] op_sel_hi:[0,1,1]
	v_pk_mul_f32 v[32:33], v[100:101], v[32:33] op_sel_hi:[0,1]
	v_pk_mul_f32 v[48:49], v[100:101], v[48:49] op_sel_hi:[0,1]
	v_pk_mul_f32 v[60:61], v[100:101], v[64:65] op_sel_hi:[0,1]
	v_pk_fma_f32 v[30:31], v[96:97], v[108:109], v[30:31] op_sel_hi:[0,1,1]
	v_pk_fma_f32 v[44:45], v[96:97], v[44:45], v[62:63] op_sel_hi:[0,1,1]
	v_pk_fma_f32 v[22:23], v[98:99], v[22:23], v[32:33] op_sel_hi:[0,1,1]
	v_pk_fma_f32 v[32:33], v[98:99], v[38:39], v[48:49] op_sel_hi:[0,1,1]
	v_pk_fma_f32 v[38:39], v[98:99], v[54:55], v[60:61] op_sel_hi:[0,1,1]
	v_pk_add_f32 v[22:23], v[30:31], v[22:23]
	v_pk_add_f32 v[30:31], v[44:45], v[38:39]
	v_pk_mul_f32 v[62:63], v[100:101], v[80:81] op_sel_hi:[0,1]
	v_mov_b32_e32 v97, v100
	v_pk_add_f32 v[28:29], v[28:29], v[32:33]
	v_pk_mul_f32 v[34:35], v[56:57], v[34:35] op_sel_hi:[0,1]
	v_pk_mul_f32 v[38:39], v[56:57], v[50:51] op_sel_hi:[0,1]
	v_pk_mul_f32 v[44:45], v[56:57], v[66:67] op_sel_hi:[0,1]
	v_pk_fma_f32 v[24:25], v[102:103], v[24:25], v[34:35] op_sel_hi:[0,1,1]
	v_pk_fma_f32 v[34:35], v[102:103], v[40:41], v[38:39] op_sel_hi:[0,1,1]
	v_pk_fma_f32 v[38:39], v[102:103], v[110:111], v[44:45] op_sel_hi:[0,1,1]
	v_mov_b32_e32 v95, v98
	v_pk_mul_f32 v[64:65], v[96:97], v[86:87]
	v_pk_fma_f32 v[48:49], v[98:99], v[70:71], v[62:63] op_sel_hi:[0,1,1]
	v_pk_add_f32 v[22:23], v[22:23], v[24:25]
	v_pk_mul_f32 v[24:25], v[104:105], v[36:37] op_sel_hi:[0,1]
	v_pk_add_f32 v[28:29], v[28:29], v[34:35]
	v_pk_mul_f32 v[34:35], v[104:105], v[52:53] op_sel_hi:[0,1]
	v_pk_add_f32 v[30:31], v[30:31], v[38:39]
	v_pk_mul_f32 v[36:37], v[104:105], v[68:69] op_sel_hi:[0,1]
	v_pk_mul_f32 v[38:39], v[104:105], v[84:85] op_sel_hi:[0,1]
	v_mov_b32_e32 v105, v56
	v_pk_fma_f32 v[54:55], v[94:95], v[76:77], v[64:65]
	v_pk_add_f32 v[32:33], v[46:47], v[48:49]
	v_pk_mul_f32 v[46:47], v[56:57], v[82:83] op_sel_hi:[0,1]
	v_pk_fma_f32 v[24:25], v[106:107], v[26:27], v[24:25] op_sel_hi:[0,1,1]
	v_pk_fma_f32 v[26:27], v[106:107], v[42:43], v[34:35] op_sel_hi:[0,1,1]
	v_pk_fma_f32 v[34:35], v[106:107], v[58:59], v[36:37] op_sel_hi:[0,1,1]
	v_pk_fma_f32 v[36:37], v[106:107], v[74:75], v[38:39] op_sel_hi:[0,1,1]
	v_mov_b32_e32 v107, v102
	v_pk_mul_f32 v[38:39], v[104:105], v[90:91]
	v_pk_fma_f32 v[40:41], v[102:103], v[72:73], v[46:47] op_sel_hi:[0,1,1]
	v_add_f32_e32 v7, v54, v55
	v_pk_add_f32 v[22:23], v[24:25], v[22:23]
	v_pk_add_f32 v[24:25], v[26:27], v[28:29]
	v_pk_add_f32 v[26:27], v[34:35], v[30:31]
	v_pk_fma_f32 v[30:31], v[106:107], v[88:89], v[38:39]
	v_pk_add_f32 v[32:33], v[32:33], v[40:41]
	v_add_f32_e32 v7, v7, v31
	v_pk_add_f32 v[28:29], v[36:37], v[32:33]
	v_add_f32_e32 v7, v30, v7
	v_pk_add_f32 v[10:11], v[10:11], v[22:23]
	v_pk_add_f32 v[12:13], v[12:13], v[24:25]
	v_pk_add_f32 v[14:15], v[14:15], v[26:27]
	v_pk_add_f32 v[16:17], v[16:17], v[28:29]
	v_add_f32_e32 v2, v2, v7
	s_waitcnt vmcnt(63)
	v_add_co_u32_e32 v94, vcc, 0x6000, v8
	v_mov_b32_e32 v7, s15
	s_nop 0
	v_addc_co_u32_e32 v95, vcc, 0, v9, vcc
	v_add_co_u32_e32 v98, vcc, 0xc000, v8
	v_mov_b32_e32 v96, v136
	s_nop 0
	v_addc_co_u32_e32 v99, vcc, 0, v9, vcc
	v_add_co_u32_e32 v100, vcc, 0x12000, v8
	ds_read_b128 v[22:25], v7
	ds_read_b128 v[26:29], v7 offset:16
	ds_read_b128 v[30:33], v7 offset:4096
	ds_read_b128 v[34:37], v7 offset:4112
	ds_read_b128 v[38:41], v7 offset:8192
	ds_read_b128 v[42:45], v7 offset:8208
	ds_read_b128 v[46:49], v7 offset:12288
	ds_read_b128 v[50:53], v7 offset:12304
	ds_read_b128 v[54:57], v7 offset:16384
	ds_read_b128 v[58:61], v7 offset:16400
	ds_read_b128 v[62:65], v7 offset:20480
	ds_read_b128 v[66:69], v7 offset:20496
	ds_read_b128 v[70:73], v7 offset:24576
	ds_read_b128 v[74:77], v7 offset:24592
	ds_read_b128 v[78:81], v7 offset:28672
	ds_read_b128 v[82:85], v7 offset:28688
	v_addc_co_u32_e32 v101, vcc, 0, v9, vcc
	v_add_co_u32_e32 v102, vcc, 0x18000, v8
	ds_read_b128 v[86:89], v7 offset:32768
	ds_read_b128 v[90:93], v7 offset:32784
	v_addc_co_u32_e32 v103, vcc, 0, v9, vcc
	v_mov_b32_e32 v94, v137
	v_add_co_u32_e32 v104, vcc, 0x1e000, v8
	v_mov_b32_e32 v98, v138
	s_nop 0
	v_mov_b32_e32 v100, v139
	v_addc_co_u32_e32 v105, vcc, 0, v9, vcc
	v_add_co_u32_e32 v106, vcc, 0x24000, v8
	v_mov_b32_e32 v102, v140
	s_waitcnt lgkmcnt(14)
	v_mov_b32_e32 v108, v22
	v_mov_b32_e32 v22, v24
	v_mov_b32_e32 v24, v26
	v_mov_b32_e32 v26, v28
	s_waitcnt lgkmcnt(13)
	v_mov_b32_e32 v28, v38
	v_mov_b32_e32 v38, v40
	s_waitcnt lgkmcnt(12)
; #define LAS __attribute__((address_space(3)))
; __device__ __forceinline__ void p0_prologue(const Args& a, const Frame& F) {
;     ...
;         for (int kk = 0; kk < 128; kk += 8) {
;             float wv[8];
; #pragma unroll
;             for (int u = 0; u < 8; ++u) wv[u] = W[(size_t)(k0 + kk + u) * 6144];
; #pragma unroll
;             for (int q = 0; q < 9; ++q) { const f32x4 s0 = *(const LAS f32x4*)(sc + q * 1024 + k0 + kk), s1 = *(const LAS f32x4*)(sc + q * 1024 + k0 + kk + 4);
;                 acc[q] += (s0.x * wv[0] + s0.y * wv[1]) + (s0.z * wv[2] + s0.w * wv[3]) + (s1.x * wv[4] + s1.y * wv[5]) + (s1.z * wv[6] + s1.w * wv[7]); }
;         }
	v_mov_b32_e32 v40, v42
	v_mov_b32_e32 v42, v44
	s_waitcnt lgkmcnt(9)
	v_mov_b32_e32 v44, v54
	v_mov_b32_e32 v54, v56
	v_mov_b32_e32 v56, v141
	v_addc_co_u32_e32 v107, vcc, 0, v9, vcc
	v_add_co_u32_e32 v104, vcc, 0x2a000, v8
	v_mov_b32_e32 v109, v30
	s_nop 0
	v_addc_co_u32_e32 v105, vcc, 0, v9, vcc
	v_mov_b32_e32 v106, v142
	s_nop 0
	v_mov_b32_e32 v104, v143
	v_mov_b32_e32 v30, v23
	v_mov_b32_e32 v23, v32
	v_mov_b32_e32 v32, v25
	v_mov_b32_e32 v25, v34
	v_mov_b32_e32 v34, v27
	v_mov_b32_e32 v27, v36
	v_mov_b32_e32 v36, v29
	v_mov_b32_e32 v29, v46
	v_mov_b32_e32 v46, v39
	s_waitcnt lgkmcnt(6)
	v_mov_b32_e32 v111, v66
	v_mov_b32_e32 v66, v59
	v_mov_b32_e32 v59, v68
	v_mov_b32_e32 v68, v61
	s_waitcnt lgkmcnt(3)
	v_mov_b32_e32 v61, v78
	v_mov_b32_e32 v78, v71
	v_mov_b32_e32 v39, v48
	v_mov_b32_e32 v48, v41
	v_mov_b32_e32 v41, v50
	v_mov_b32_e32 v50, v43
	v_mov_b32_e32 v43, v52
	v_mov_b32_e32 v52, v45
	v_mov_b32_e32 v45, v62
	v_mov_b32_e32 v62, v55
	v_mov_b32_e32 v55, v64
	v_mov_b32_e32 v64, v57
	v_mov_b32_e32 v110, v58
	v_mov_b32_e32 v58, v60
	v_mov_b32_e32 v60, v70
	v_mov_b32_e32 v71, v80
	v_mov_b32_e32 v80, v73
	v_mov_b32_e32 v70, v72
	v_mov_b32_e32 v72, v74
	s_waitcnt lgkmcnt(2)
	v_mov_b32_e32 v73, v82
	v_mov_b32_e32 v82, v75
	v_mov_b32_e32 v74, v76
	v_mov_b32_e32 v75, v84
	v_mov_b32_e32 v84, v77
	s_waitcnt lgkmcnt(1)
	v_mov_b32_e32 v76, v87
	v_mov_b32_e32 v87, v89
	v_mov_b32_e32 v77, v88
	s_waitcnt lgkmcnt(0)
	v_mov_b32_e32 v89, v90
	v_mov_b32_e32 v90, v93
	v_mov_b32_e32 v88, v92
	s_add_i32 s14, s14, 8
	s_add_i32 s15, s15, 32
	s_cmpk_gt_u32 s14, 0x77
	v_lshl_add_u64 v[8:9], v[8:9], 0, s[12:13]
	v_pk_mul_f32 v[46:47], v[94:95], v[46:47] op_sel_hi:[0,1]
	v_pk_mul_f32 v[78:79], v[94:95], v[78:79] op_sel_hi:[0,1]
	v_pk_mul_f32 v[30:31], v[94:95], v[30:31] op_sel_hi:[0,1]
	v_pk_mul_f32 v[62:63], v[94:95], v[62:63] op_sel_hi:[0,1]
	v_pk_fma_f32 v[28:29], v[96:97], v[28:29], v[46:47] op_sel_hi:[0,1,1]
	v_pk_fma_f32 v[46:47], v[96:97], v[60:61], v[78:79] op_sel_hi:[0,1,1]
	v_pk_mul_f32 v[32:33], v[100:101], v[32:33] op_sel_hi:[0,1]
	v_pk_mul_f32 v[48:49], v[100:101], v[48:49] op_sel_hi:[0,1]
	v_pk_mul_f32 v[60:61], v[100:101], v[64:65] op_sel_hi:[0,1]
	v_pk_fma_f32 v[30:31], v[96:97], v[108:109], v[30:31] op_sel_hi:[0,1,1]
	v_pk_fma_f32 v[44:45], v[96:97], v[44:45], v[62:63] op_sel_hi:[0,1,1]
	v_pk_fma_f32 v[22:23], v[98:99], v[22:23], v[32:33] op_sel_hi:[0,1,1]
	v_pk_fma_f32 v[32:33], v[98:99], v[38:39], v[48:49] op_sel_hi:[0,1,1]
	v_pk_fma_f32 v[38:39], v[98:99], v[54:55], v[60:61] op_sel_hi:[0,1,1]
	v_pk_add_f32 v[22:23], v[30:31], v[22:23]
	v_pk_add_f32 v[30:31], v[44:45], v[38:39]
	v_pk_mul_f32 v[62:63], v[100:101], v[80:81] op_sel_hi:[0,1]
	v_mov_b32_e32 v97, v100
	v_pk_add_f32 v[28:29], v[28:29], v[32:33]
	v_pk_mul_f32 v[34:35], v[56:57], v[34:35] op_sel_hi:[0,1]
	v_pk_mul_f32 v[38:39], v[56:57], v[50:51] op_sel_hi:[0,1]
	v_pk_mul_f32 v[44:45], v[56:57], v[66:67] op_sel_hi:[0,1]
	v_pk_fma_f32 v[24:25], v[102:103], v[24:25], v[34:35] op_sel_hi:[0,1,1]
	v_pk_fma_f32 v[34:35], v[102:103], v[40:41], v[38:39] op_sel_hi:[0,1,1]
	v_pk_fma_f32 v[38:39], v[102:103], v[110:111], v[44:45] op_sel_hi:[0,1,1]
	v_mov_b32_e32 v95, v98
	v_pk_mul_f32 v[64:65], v[96:97], v[86:87]
	v_pk_fma_f32 v[48:49], v[98:99], v[70:71], v[62:63] op_sel_hi:[0,1,1]
	v_pk_add_f32 v[22:23], v[22:23], v[24:25]
	v_pk_mul_f32 v[24:25], v[104:105], v[36:37] op_sel_hi:[0,1]
	v_pk_add_f32 v[28:29], v[28:29], v[34:35]
	v_pk_mul_f32 v[34:35], v[104:105], v[52:53] op_sel_hi:[0,1]
	v_pk_add_f32 v[30:31], v[30:31], v[38:39]
	v_pk_mul_f32 v[36:37], v[104:105], v[68:69] op_sel_hi:[0,1]
	v_pk_mul_f32 v[38:39], v[104:105], v[84:85] op_sel_hi:[0,1]
	v_mov_b32_e32 v105, v56
	v_pk_fma_f32 v[54:55], v[94:95], v[76:77], v[64:65]
	v_pk_add_f32 v[32:33], v[46:47], v[48:49]
	v_pk_mul_f32 v[46:47], v[56:57], v[82:83] op_sel_hi:[0,1]
	v_pk_fma_f32 v[24:25], v[106:107], v[26:27], v[24:25] op_sel_hi:[0,1,1]
	v_pk_fma_f32 v[26:27], v[106:107], v[42:43], v[34:35] op_sel_hi:[0,1,1]
	v_pk_fma_f32 v[34:35], v[106:107], v[58:59], v[36:37] op_sel_hi:[0,1,1]
	v_pk_fma_f32 v[36:37], v[106:107], v[74:75], v[38:39] op_sel_hi:[0,1,1]
	v_mov_b32_e32 v107, v102
	v_pk_mul_f32 v[38:39], v[104:105], v[90:91]
	v_pk_fma_f32 v[40:41], v[102:103], v[72:73], v[46:47] op_sel_hi:[0,1,1]
	v_add_f32_e32 v7, v54, v55
	v_pk_add_f32 v[22:23], v[24:25], v[22:23]
	v_pk_add_f32 v[24:25], v[26:27], v[28:29]
	v_pk_add_f32 v[26:27], v[34:35], v[30:31]
	v_pk_fma_f32 v[30:31], v[106:107], v[88:89], v[38:39]
	v_pk_add_f32 v[32:33], v[32:33], v[40:41]
	v_add_f32_e32 v7, v7, v31
	v_pk_add_f32 v[28:29], v[36:37], v[32:33]
	v_add_f32_e32 v7, v30, v7
	v_pk_add_f32 v[10:11], v[10:11], v[22:23]
	v_pk_add_f32 v[12:13], v[12:13], v[24:25]
	v_pk_add_f32 v[14:15], v[14:15], v[26:27]
	v_pk_add_f32 v[16:17], v[16:17], v[28:29]
	v_add_f32_e32 v2, v2, v7
	s_waitcnt vmcnt(63)
	v_add_co_u32_e32 v94, vcc, 0x6000, v8
	v_mov_b32_e32 v7, s15
	s_nop 0
	v_addc_co_u32_e32 v95, vcc, 0, v9, vcc
	v_add_co_u32_e32 v98, vcc, 0xc000, v8
	v_mov_b32_e32 v96, v144
	s_nop 0
	v_addc_co_u32_e32 v99, vcc, 0, v9, vcc
	v_add_co_u32_e32 v100, vcc, 0x12000, v8
	ds_read_b128 v[22:25], v7
	ds_read_b128 v[26:29], v7 offset:16
	ds_read_b128 v[30:33], v7 offset:4096
	ds_read_b128 v[34:37], v7 offset:4112
	ds_read_b128 v[38:41], v7 offset:8192
	ds_read_b128 v[42:45], v7 offset:8208
	ds_read_b128 v[46:49], v7 offset:12288
	ds_read_b128 v[50:53], v7 offset:12304
	ds_read_b128 v[54:57], v7 offset:16384
	ds_read_b128 v[58:61], v7 offset:16400
	ds_read_b128 v[62:65], v7 offset:20480
	ds_read_b128 v[66:69], v7 offset:20496
	ds_read_b128 v[70:73], v7 offset:24576
	ds_read_b128 v[74:77], v7 offset:24592
	ds_read_b128 v[78:81], v7 offset:28672
	ds_read_b128 v[82:85], v7 offset:28688
	v_addc_co_u32_e32 v101, vcc, 0, v9, vcc
	v_add_co_u32_e32 v102, vcc, 0x18000, v8
	ds_read_b128 v[86:89], v7 offset:32768
	ds_read_b128 v[90:93], v7 offset:32784
	v_addc_co_u32_e32 v103, vcc, 0, v9, vcc
	v_mov_b32_e32 v94, v145
	v_add_co_u32_e32 v104, vcc, 0x1e000, v8
	v_mov_b32_e32 v98, v146
	s_nop 0
	v_mov_b32_e32 v100, v147
	v_addc_co_u32_e32 v105, vcc, 0, v9, vcc
	v_add_co_u32_e32 v106, vcc, 0x24000, v8
	v_mov_b32_e32 v102, v148
	s_waitcnt lgkmcnt(14)
; #define LAS __attribute__((address_space(3)))
; __device__ __forceinline__ void p0_prologue(const Args& a, const Frame& F) {
;     ...
;         for (int kk = 0; kk < 128; kk += 8) {
;             float wv[8];
; #pragma unroll
;             for (int u = 0; u < 8; ++u) wv[u] = W[(size_t)(k0 + kk + u) * 6144];
; #pragma unroll
;             for (int q = 0; q < 9; ++q) { const f32x4 s0 = *(const LAS f32x4*)(sc + q * 1024 + k0 + kk), s1 = *(const LAS f32x4*)(sc + q * 1024 + k0 + kk + 4);
;                 acc[q] += (s0.x * wv[0] + s0.y * wv[1]) + (s0.z * wv[2] + s0.w * wv[3]) + (s1.x * wv[4] + s1.y * wv[5]) + (s1.z * wv[6] + s1.w * wv[7]); }
;         }
	v_mov_b32_e32 v108, v22
	v_mov_b32_e32 v22, v24
	v_mov_b32_e32 v24, v26
	v_mov_b32_e32 v26, v28
	s_waitcnt lgkmcnt(13)
	v_mov_b32_e32 v28, v38
	v_mov_b32_e32 v38, v40
	s_waitcnt lgkmcnt(12)
	v_mov_b32_e32 v40, v42
	v_mov_b32_e32 v42, v44
	s_waitcnt lgkmcnt(9)
	v_mov_b32_e32 v44, v54
	v_mov_b32_e32 v54, v56
	v_mov_b32_e32 v56, v149
	v_addc_co_u32_e32 v107, vcc, 0, v9, vcc
	v_add_co_u32_e32 v104, vcc, 0x2a000, v8
	v_mov_b32_e32 v109, v30
	s_nop 0
	v_addc_co_u32_e32 v105, vcc, 0, v9, vcc
	v_mov_b32_e32 v106, v150
	s_nop 0
	v_mov_b32_e32 v104, v151
	v_mov_b32_e32 v30, v23
	v_mov_b32_e32 v23, v32
	v_mov_b32_e32 v32, v25
	v_mov_b32_e32 v25, v34
	v_mov_b32_e32 v34, v27
	v_mov_b32_e32 v27, v36
	v_mov_b32_e32 v36, v29
	v_mov_b32_e32 v29, v46
	v_mov_b32_e32 v46, v39
	s_waitcnt lgkmcnt(6)
	v_mov_b32_e32 v111, v66
	v_mov_b32_e32 v66, v59
	v_mov_b32_e32 v59, v68
	v_mov_b32_e32 v68, v61
	s_waitcnt lgkmcnt(3)
	v_mov_b32_e32 v61, v78
	v_mov_b32_e32 v78, v71
	v_mov_b32_e32 v39, v48
	v_mov_b32_e32 v48, v41
	v_mov_b32_e32 v41, v50
	v_mov_b32_e32 v50, v43
	v_mov_b32_e32 v43, v52
	v_mov_b32_e32 v52, v45
	v_mov_b32_e32 v45, v62
	v_mov_b32_e32 v62, v55
	v_mov_b32_e32 v55, v64
	v_mov_b32_e32 v64, v57
	v_mov_b32_e32 v110, v58
	v_mov_b32_e32 v58, v60
	v_mov_b32_e32 v60, v70
	v_mov_b32_e32 v71, v80
	v_mov_b32_e32 v80, v73
	v_mov_b32_e32 v70, v72
	v_mov_b32_e32 v72, v74
	s_waitcnt lgkmcnt(2)
	v_mov_b32_e32 v73, v82
	v_mov_b32_e32 v82, v75
	v_mov_b32_e32 v74, v76
	v_mov_b32_e32 v75, v84
	v_mov_b32_e32 v84, v77
	s_waitcnt lgkmcnt(1)
	v_mov_b32_e32 v76, v87
	v_mov_b32_e32 v87, v89
	v_mov_b32_e32 v77, v88
	s_waitcnt lgkmcnt(0)
	v_mov_b32_e32 v89, v90
	v_mov_b32_e32 v90, v93
	v_mov_b32_e32 v88, v92
	s_add_i32 s14, s14, 8
	s_add_i32 s15, s15, 32
	s_cmpk_gt_u32 s14, 0x77
	v_lshl_add_u64 v[8:9], v[8:9], 0, s[12:13]
	v_pk_mul_f32 v[46:47], v[94:95], v[46:47] op_sel_hi:[0,1]
	v_pk_mul_f32 v[78:79], v[94:95], v[78:79] op_sel_hi:[0,1]
	v_pk_mul_f32 v[30:31], v[94:95], v[30:31] op_sel_hi:[0,1]
	v_pk_mul_f32 v[62:63], v[94:95], v[62:63] op_sel_hi:[0,1]
	v_pk_fma_f32 v[28:29], v[96:97], v[28:29], v[46:47] op_sel_hi:[0,1,1]
	v_pk_fma_f32 v[46:47], v[96:97], v[60:61], v[78:79] op_sel_hi:[0,1,1]
	v_pk_mul_f32 v[32:33], v[100:101], v[32:33] op_sel_hi:[0,1]
	v_pk_mul_f32 v[48:49], v[100:101], v[48:49] op_sel_hi:[0,1]
	v_pk_mul_f32 v[60:61], v[100:101], v[64:65] op_sel_hi:[0,1]
	v_pk_fma_f32 v[30:31], v[96:97], v[108:109], v[30:31] op_sel_hi:[0,1,1]
	v_pk_fma_f32 v[44:45], v[96:97], v[44:45], v[62:63] op_sel_hi:[0,1,1]
	v_pk_fma_f32 v[22:23], v[98:99], v[22:23], v[32:33] op_sel_hi:[0,1,1]
	v_pk_fma_f32 v[32:33], v[98:99], v[38:39], v[48:49] op_sel_hi:[0,1,1]
	v_pk_fma_f32 v[38:39], v[98:99], v[54:55], v[60:61] op_sel_hi:[0,1,1]
	v_pk_add_f32 v[22:23], v[30:31], v[22:23]
	v_pk_add_f32 v[30:31], v[44:45], v[38:39]
	v_pk_mul_f32 v[62:63], v[100:101], v[80:81] op_sel_hi:[0,1]
	v_mov_b32_e32 v97, v100
	v_pk_add_f32 v[28:29], v[28:29], v[32:33]
	v_pk_mul_f32 v[34:35], v[56:57], v[34:35] op_sel_hi:[0,1]
	v_pk_mul_f32 v[38:39], v[56:57], v[50:51] op_sel_hi:[0,1]
	v_pk_mul_f32 v[44:45], v[56:57], v[66:67] op_sel_hi:[0,1]
	v_pk_fma_f32 v[24:25], v[102:103], v[24:25], v[34:35] op_sel_hi:[0,1,1]
	v_pk_fma_f32 v[34:35], v[102:103], v[40:41], v[38:39] op_sel_hi:[0,1,1]
	v_pk_fma_f32 v[38:39], v[102:103], v[110:111], v[44:45] op_sel_hi:[0,1,1]
	v_mov_b32_e32 v95, v98
	v_pk_mul_f32 v[64:65], v[96:97], v[86:87]
	v_pk_fma_f32 v[48:49], v[98:99], v[70:71], v[62:63] op_sel_hi:[0,1,1]
	v_pk_add_f32 v[22:23], v[22:23], v[24:25]
	v_pk_mul_f32 v[24:25], v[104:105], v[36:37] op_sel_hi:[0,1]
	v_pk_add_f32 v[28:29], v[28:29], v[34:35]
	v_pk_mul_f32 v[34:35], v[104:105], v[52:53] op_sel_hi:[0,1]
	v_pk_add_f32 v[30:31], v[30:31], v[38:39]
	v_pk_mul_f32 v[36:37], v[104:105], v[68:69] op_sel_hi:[0,1]
	v_pk_mul_f32 v[38:39], v[104:105], v[84:85] op_sel_hi:[0,1]
	v_mov_b32_e32 v105, v56
	v_pk_fma_f32 v[54:55], v[94:95], v[76:77], v[64:65]
	v_pk_add_f32 v[32:33], v[46:47], v[48:49]
	v_pk_mul_f32 v[46:47], v[56:57], v[82:83] op_sel_hi:[0,1]
	v_pk_fma_f32 v[24:25], v[106:107], v[26:27], v[24:25] op_sel_hi:[0,1,1]
	v_pk_fma_f32 v[26:27], v[106:107], v[42:43], v[34:35] op_sel_hi:[0,1,1]
	v_pk_fma_f32 v[34:35], v[106:107], v[58:59], v[36:37] op_sel_hi:[0,1,1]
	v_pk_fma_f32 v[36:37], v[106:107], v[74:75], v[38:39] op_sel_hi:[0,1,1]
	v_mov_b32_e32 v107, v102
	v_pk_mul_f32 v[38:39], v[104:105], v[90:91]
	v_pk_fma_f32 v[40:41], v[102:103], v[72:73], v[46:47] op_sel_hi:[0,1,1]
	v_add_f32_e32 v7, v54, v55
	v_pk_add_f32 v[22:23], v[24:25], v[22:23]
	v_pk_add_f32 v[24:25], v[26:27], v[28:29]
	v_pk_add_f32 v[26:27], v[34:35], v[30:31]
	v_pk_fma_f32 v[30:31], v[106:107], v[88:89], v[38:39]
	v_pk_add_f32 v[32:33], v[32:33], v[40:41]
	v_add_f32_e32 v7, v7, v31
	v_pk_add_f32 v[28:29], v[36:37], v[32:33]
	v_add_f32_e32 v7, v30, v7
	v_pk_add_f32 v[10:11], v[10:11], v[22:23]
	v_pk_add_f32 v[12:13], v[12:13], v[24:25]
	v_pk_add_f32 v[14:15], v[14:15], v[26:27]
	v_pk_add_f32 v[16:17], v[16:17], v[28:29]
	v_add_f32_e32 v2, v2, v7
	s_waitcnt vmcnt(63)
; #define LAS __attribute__((address_space(3)))
; __device__ __forceinline__ void p0_prologue(const Args& a, const Frame& F) {
;     ...
;         for (int kk = 0; kk < 128; kk += 8) {
;             float wv[8];
; #pragma unroll
;             for (int u = 0; u < 8; ++u) wv[u] = W[(size_t)(k0 + kk + u) * 6144];
; #pragma unroll
;             for (int q = 0; q < 9; ++q) { const f32x4 s0 = *(const LAS f32x4*)(sc + q * 1024 + k0 + kk), s1 = *(const LAS f32x4*)(sc + q * 1024 + k0 + kk + 4);
;                 acc[q] += (s0.x * wv[0] + s0.y * wv[1]) + (s0.z * wv[2] + s0.w * wv[3]) + (s1.x * wv[4] + s1.y * wv[5]) + (s1.z * wv[6] + s1.w * wv[7]); }
;         }
	v_add_co_u32_e32 v94, vcc, 0x6000, v8
	v_mov_b32_e32 v7, s15
	s_nop 0
	v_addc_co_u32_e32 v95, vcc, 0, v9, vcc
	v_add_co_u32_e32 v98, vcc, 0xc000, v8
	v_mov_b32_e32 v96, v152
	s_nop 0
	v_addc_co_u32_e32 v99, vcc, 0, v9, vcc
	v_add_co_u32_e32 v100, vcc, 0x12000, v8
	ds_read_b128 v[22:25], v7
	ds_read_b128 v[26:29], v7 offset:16
	ds_read_b128 v[30:33], v7 offset:4096
	ds_read_b128 v[34:37], v7 offset:4112
	ds_read_b128 v[38:41], v7 offset:8192
	ds_read_b128 v[42:45], v7 offset:8208
	ds_read_b128 v[46:49], v7 offset:12288
	ds_read_b128 v[50:53], v7 offset:12304
	ds_read_b128 v[54:57], v7 offset:16384
	ds_read_b128 v[58:61], v7 offset:16400
	ds_read_b128 v[62:65], v7 offset:20480
	ds_read_b128 v[66:69], v7 offset:20496
	ds_read_b128 v[70:73], v7 offset:24576
	ds_read_b128 v[74:77], v7 offset:24592
	ds_read_b128 v[78:81], v7 offset:28672
	ds_read_b128 v[82:85], v7 offset:28688
	v_addc_co_u32_e32 v101, vcc, 0, v9, vcc
	v_add_co_u32_e32 v102, vcc, 0x18000, v8
	ds_read_b128 v[86:89], v7 offset:32768
	ds_read_b128 v[90:93], v7 offset:32784
	v_addc_co_u32_e32 v103, vcc, 0, v9, vcc
	v_mov_b32_e32 v94, v153
	v_add_co_u32_e32 v104, vcc, 0x1e000, v8
	v_mov_b32_e32 v98, v154
	s_nop 0
	v_mov_b32_e32 v100, v155
	v_addc_co_u32_e32 v105, vcc, 0, v9, vcc
	v_add_co_u32_e32 v106, vcc, 0x24000, v8
	v_mov_b32_e32 v102, v156
	s_waitcnt lgkmcnt(14)
	v_mov_b32_e32 v108, v22
	v_mov_b32_e32 v22, v24
	v_mov_b32_e32 v24, v26
	v_mov_b32_e32 v26, v28
	s_waitcnt lgkmcnt(13)
	v_mov_b32_e32 v28, v38
	v_mov_b32_e32 v38, v40
	s_waitcnt lgkmcnt(12)
	v_mov_b32_e32 v40, v42
	v_mov_b32_e32 v42, v44
	s_waitcnt lgkmcnt(9)
	v_mov_b32_e32 v44, v54
	v_mov_b32_e32 v54, v56
	v_mov_b32_e32 v56, v157
	v_addc_co_u32_e32 v107, vcc, 0, v9, vcc
	v_add_co_u32_e32 v104, vcc, 0x2a000, v8
	v_mov_b32_e32 v109, v30
	s_nop 0
	v_addc_co_u32_e32 v105, vcc, 0, v9, vcc
	v_mov_b32_e32 v106, v158
	s_nop 0
	v_mov_b32_e32 v104, v159
	v_mov_b32_e32 v30, v23
	v_mov_b32_e32 v23, v32
	v_mov_b32_e32 v32, v25
	v_mov_b32_e32 v25, v34
	v_mov_b32_e32 v34, v27
	v_mov_b32_e32 v27, v36
	v_mov_b32_e32 v36, v29
	v_mov_b32_e32 v29, v46
	v_mov_b32_e32 v46, v39
	s_waitcnt lgkmcnt(6)
	v_mov_b32_e32 v111, v66
	v_mov_b32_e32 v66, v59
	v_mov_b32_e32 v59, v68
	v_mov_b32_e32 v68, v61
	s_waitcnt lgkmcnt(3)
	v_mov_b32_e32 v61, v78
	v_mov_b32_e32 v78, v71
	v_mov_b32_e32 v39, v48
	v_mov_b32_e32 v48, v41
	v_mov_b32_e32 v41, v50
	v_mov_b32_e32 v50, v43
	v_mov_b32_e32 v43, v52
	v_mov_b32_e32 v52, v45
	v_mov_b32_e32 v45, v62
	v_mov_b32_e32 v62, v55
	v_mov_b32_e32 v55, v64
	v_mov_b32_e32 v64, v57
	v_mov_b32_e32 v110, v58
	v_mov_b32_e32 v58, v60
	v_mov_b32_e32 v60, v70
	v_mov_b32_e32 v71, v80
	v_mov_b32_e32 v80, v73
	v_mov_b32_e32 v70, v72
	v_mov_b32_e32 v72, v74
	s_waitcnt lgkmcnt(2)
	v_mov_b32_e32 v73, v82
	v_mov_b32_e32 v82, v75
	v_mov_b32_e32 v74, v76
	v_mov_b32_e32 v75, v84
	v_mov_b32_e32 v84, v77
	s_waitcnt lgkmcnt(1)
	v_mov_b32_e32 v76, v87
	v_mov_b32_e32 v87, v89
	v_mov_b32_e32 v77, v88
	s_waitcnt lgkmcnt(0)
	v_mov_b32_e32 v89, v90
	v_mov_b32_e32 v90, v93
	v_mov_b32_e32 v88, v92
	s_add_i32 s14, s14, 8
	s_add_i32 s15, s15, 32
	s_cmpk_gt_u32 s14, 0x77
	v_lshl_add_u64 v[8:9], v[8:9], 0, s[12:13]
	v_pk_mul_f32 v[46:47], v[94:95], v[46:47] op_sel_hi:[0,1]
	v_pk_mul_f32 v[78:79], v[94:95], v[78:79] op_sel_hi:[0,1]
	v_pk_mul_f32 v[30:31], v[94:95], v[30:31] op_sel_hi:[0,1]
	v_pk_mul_f32 v[62:63], v[94:95], v[62:63] op_sel_hi:[0,1]
	v_pk_fma_f32 v[28:29], v[96:97], v[28:29], v[46:47] op_sel_hi:[0,1,1]
	v_pk_fma_f32 v[46:47], v[96:97], v[60:61], v[78:79] op_sel_hi:[0,1,1]
	v_pk_mul_f32 v[32:33], v[100:101], v[32:33] op_sel_hi:[0,1]
	v_pk_mul_f32 v[48:49], v[100:101], v[48:49] op_sel_hi:[0,1]
	v_pk_mul_f32 v[60:61], v[100:101], v[64:65] op_sel_hi:[0,1]
	v_pk_fma_f32 v[30:31], v[96:97], v[108:109], v[30:31] op_sel_hi:[0,1,1]
	v_pk_fma_f32 v[44:45], v[96:97], v[44:45], v[62:63] op_sel_hi:[0,1,1]
	v_pk_fma_f32 v[22:23], v[98:99], v[22:23], v[32:33] op_sel_hi:[0,1,1]
	v_pk_fma_f32 v[32:33], v[98:99], v[38:39], v[48:49] op_sel_hi:[0,1,1]
	v_pk_fma_f32 v[38:39], v[98:99], v[54:55], v[60:61] op_sel_hi:[0,1,1]
	v_pk_add_f32 v[22:23], v[30:31], v[22:23]
	v_pk_add_f32 v[30:31], v[44:45], v[38:39]
	v_pk_mul_f32 v[62:63], v[100:101], v[80:81] op_sel_hi:[0,1]
	v_mov_b32_e32 v97, v100
	v_pk_add_f32 v[28:29], v[28:29], v[32:33]
	v_pk_mul_f32 v[34:35], v[56:57], v[34:35] op_sel_hi:[0,1]
	v_pk_mul_f32 v[38:39], v[56:57], v[50:51] op_sel_hi:[0,1]
	v_pk_mul_f32 v[44:45], v[56:57], v[66:67] op_sel_hi:[0,1]
	v_pk_fma_f32 v[24:25], v[102:103], v[24:25], v[34:35] op_sel_hi:[0,1,1]
	v_pk_fma_f32 v[34:35], v[102:103], v[40:41], v[38:39] op_sel_hi:[0,1,1]
	v_pk_fma_f32 v[38:39], v[102:103], v[110:111], v[44:45] op_sel_hi:[0,1,1]
	v_mov_b32_e32 v95, v98
	v_pk_mul_f32 v[64:65], v[96:97], v[86:87]
	v_pk_fma_f32 v[48:49], v[98:99], v[70:71], v[62:63] op_sel_hi:[0,1,1]
	v_pk_add_f32 v[22:23], v[22:23], v[24:25]
	v_pk_mul_f32 v[24:25], v[104:105], v[36:37] op_sel_hi:[0,1]
	v_pk_add_f32 v[28:29], v[28:29], v[34:35]
	v_pk_mul_f32 v[34:35], v[104:105], v[52:53] op_sel_hi:[0,1]
	v_pk_add_f32 v[30:31], v[30:31], v[38:39]
	v_pk_mul_f32 v[36:37], v[104:105], v[68:69] op_sel_hi:[0,1]
	v_pk_mul_f32 v[38:39], v[104:105], v[84:85] op_sel_hi:[0,1]
	v_mov_b32_e32 v105, v56
	v_pk_fma_f32 v[54:55], v[94:95], v[76:77], v[64:65]
	v_pk_add_f32 v[32:33], v[46:47], v[48:49]
	v_pk_mul_f32 v[46:47], v[56:57], v[82:83] op_sel_hi:[0,1]
	v_pk_fma_f32 v[24:25], v[106:107], v[26:27], v[24:25] op_sel_hi:[0,1,1]
	v_pk_fma_f32 v[26:27], v[106:107], v[42:43], v[34:35] op_sel_hi:[0,1,1]
	v_pk_fma_f32 v[34:35], v[106:107], v[58:59], v[36:37] op_sel_hi:[0,1,1]
	v_pk_fma_f32 v[36:37], v[106:107], v[74:75], v[38:39] op_sel_hi:[0,1,1]
	v_mov_b32_e32 v107, v102
	v_pk_mul_f32 v[38:39], v[104:105], v[90:91]
	v_pk_fma_f32 v[40:41], v[102:103], v[72:73], v[46:47] op_sel_hi:[0,1,1]
	v_add_f32_e32 v7, v54, v55
	v_pk_add_f32 v[22:23], v[24:25], v[22:23]
	v_pk_add_f32 v[24:25], v[26:27], v[28:29]
	v_pk_add_f32 v[26:27], v[34:35], v[30:31]
	v_pk_fma_f32 v[30:31], v[106:107], v[88:89], v[38:39]
	v_pk_add_f32 v[32:33], v[32:33], v[40:41]
	v_add_f32_e32 v7, v7, v31
	v_pk_add_f32 v[28:29], v[36:37], v[32:33]
	v_add_f32_e32 v7, v30, v7
	v_pk_add_f32 v[10:11], v[10:11], v[22:23]
	v_pk_add_f32 v[12:13], v[12:13], v[24:25]
	v_pk_add_f32 v[14:15], v[14:15], v[26:27]
	v_pk_add_f32 v[16:17], v[16:17], v[28:29]
	v_add_f32_e32 v2, v2, v7
	s_waitcnt vmcnt(63)
; #define LAS __attribute__((address_space(3)))
; __device__ __forceinline__ void p0_prologue(const Args& a, const Frame& F) {
;     ...
;         for (int kk = 0; kk < 128; kk += 8) {
;             float wv[8];
; #pragma unroll
;             for (int u = 0; u < 8; ++u) wv[u] = W[(size_t)(k0 + kk + u) * 6144];
; #pragma unroll
;             for (int q = 0; q < 9; ++q) { const f32x4 s0 = *(const LAS f32x4*)(sc + q * 1024 + k0 + kk), s1 = *(const LAS f32x4*)(sc + q * 1024 + k0 + kk + 4);
;                 acc[q] += (s0.x * wv[0] + s0.y * wv[1]) + (s0.z * wv[2] + s0.w * wv[3]) + (s1.x * wv[4] + s1.y * wv[5]) + (s1.z * wv[6] + s1.w * wv[7]); }
;         }
	v_add_co_u32_e32 v94, vcc, 0x6000, v8
	v_mov_b32_e32 v7, s15
	s_nop 0
	v_addc_co_u32_e32 v95, vcc, 0, v9, vcc
	v_add_co_u32_e32 v98, vcc, 0xc000, v8
	v_mov_b32_e32 v96, v160
	s_nop 0
	v_addc_co_u32_e32 v99, vcc, 0, v9, vcc
	v_add_co_u32_e32 v100, vcc, 0x12000, v8
	ds_read_b128 v[22:25], v7
	ds_read_b128 v[26:29], v7 offset:16
	ds_read_b128 v[30:33], v7 offset:4096
	ds_read_b128 v[34:37], v7 offset:4112
	ds_read_b128 v[38:41], v7 offset:8192
	ds_read_b128 v[42:45], v7 offset:8208
	ds_read_b128 v[46:49], v7 offset:12288
	ds_read_b128 v[50:53], v7 offset:12304
	ds_read_b128 v[54:57], v7 offset:16384
	ds_read_b128 v[58:61], v7 offset:16400
	ds_read_b128 v[62:65], v7 offset:20480
	ds_read_b128 v[66:69], v7 offset:20496
	ds_read_b128 v[70:73], v7 offset:24576
	ds_read_b128 v[74:77], v7 offset:24592
	ds_read_b128 v[78:81], v7 offset:28672
	ds_read_b128 v[82:85], v7 offset:28688
	v_addc_co_u32_e32 v101, vcc, 0, v9, vcc
	v_add_co_u32_e32 v102, vcc, 0x18000, v8
	ds_read_b128 v[86:89], v7 offset:32768
	ds_read_b128 v[90:93], v7 offset:32784
	v_addc_co_u32_e32 v103, vcc, 0, v9, vcc
	v_mov_b32_e32 v94, v161
	v_add_co_u32_e32 v104, vcc, 0x1e000, v8
	v_mov_b32_e32 v98, v162
	s_nop 0
	v_mov_b32_e32 v100, v163
	v_addc_co_u32_e32 v105, vcc, 0, v9, vcc
	v_add_co_u32_e32 v106, vcc, 0x24000, v8
	v_mov_b32_e32 v102, v164
	s_waitcnt lgkmcnt(14)
	v_mov_b32_e32 v108, v22
	v_mov_b32_e32 v22, v24
	v_mov_b32_e32 v24, v26
	v_mov_b32_e32 v26, v28
	s_waitcnt lgkmcnt(13)
	v_mov_b32_e32 v28, v38
	v_mov_b32_e32 v38, v40
	s_waitcnt lgkmcnt(12)
	v_mov_b32_e32 v40, v42
	v_mov_b32_e32 v42, v44
	s_waitcnt lgkmcnt(9)
	v_mov_b32_e32 v44, v54
	v_mov_b32_e32 v54, v56
	v_mov_b32_e32 v56, v165
	v_addc_co_u32_e32 v107, vcc, 0, v9, vcc
	v_add_co_u32_e32 v104, vcc, 0x2a000, v8
	v_mov_b32_e32 v109, v30
	s_nop 0
	v_addc_co_u32_e32 v105, vcc, 0, v9, vcc
	v_mov_b32_e32 v106, v166
	s_nop 0
	v_mov_b32_e32 v104, v167
	v_mov_b32_e32 v30, v23
	v_mov_b32_e32 v23, v32
	v_mov_b32_e32 v32, v25
	v_mov_b32_e32 v25, v34
	v_mov_b32_e32 v34, v27
	v_mov_b32_e32 v27, v36
	v_mov_b32_e32 v36, v29
	v_mov_b32_e32 v29, v46
	v_mov_b32_e32 v46, v39
	s_waitcnt lgkmcnt(6)
	v_mov_b32_e32 v111, v66
	v_mov_b32_e32 v66, v59
	v_mov_b32_e32 v59, v68
	v_mov_b32_e32 v68, v61
	s_waitcnt lgkmcnt(3)
	v_mov_b32_e32 v61, v78
	v_mov_b32_e32 v78, v71
	v_mov_b32_e32 v39, v48
	v_mov_b32_e32 v48, v41
	v_mov_b32_e32 v41, v50
	v_mov_b32_e32 v50, v43
	v_mov_b32_e32 v43, v52
	v_mov_b32_e32 v52, v45
	v_mov_b32_e32 v45, v62
	v_mov_b32_e32 v62, v55
	v_mov_b32_e32 v55, v64
	v_mov_b32_e32 v64, v57
	v_mov_b32_e32 v110, v58
	v_mov_b32_e32 v58, v60
	v_mov_b32_e32 v60, v70
	v_mov_b32_e32 v71, v80
	v_mov_b32_e32 v80, v73
	v_mov_b32_e32 v70, v72
	v_mov_b32_e32 v72, v74
	s_waitcnt lgkmcnt(2)
	v_mov_b32_e32 v73, v82
	v_mov_b32_e32 v82, v75
	v_mov_b32_e32 v74, v76
	v_mov_b32_e32 v75, v84
	v_mov_b32_e32 v84, v77
	s_waitcnt lgkmcnt(1)
	v_mov_b32_e32 v76, v87
	v_mov_b32_e32 v87, v89
	v_mov_b32_e32 v77, v88
	s_waitcnt lgkmcnt(0)
	v_mov_b32_e32 v89, v90
	v_mov_b32_e32 v90, v93
	v_mov_b32_e32 v88, v92
	s_add_i32 s14, s14, 8
	s_add_i32 s15, s15, 32
	s_cmpk_gt_u32 s14, 0x77
	v_lshl_add_u64 v[8:9], v[8:9], 0, s[12:13]
	v_pk_mul_f32 v[46:47], v[94:95], v[46:47] op_sel_hi:[0,1]
	v_pk_mul_f32 v[78:79], v[94:95], v[78:79] op_sel_hi:[0,1]
	v_pk_mul_f32 v[30:31], v[94:95], v[30:31] op_sel_hi:[0,1]
	v_pk_mul_f32 v[62:63], v[94:95], v[62:63] op_sel_hi:[0,1]
	v_pk_fma_f32 v[28:29], v[96:97], v[28:29], v[46:47] op_sel_hi:[0,1,1]
	v_pk_fma_f32 v[46:47], v[96:97], v[60:61], v[78:79] op_sel_hi:[0,1,1]
	v_pk_mul_f32 v[32:33], v[100:101], v[32:33] op_sel_hi:[0,1]
	v_pk_mul_f32 v[48:49], v[100:101], v[48:49] op_sel_hi:[0,1]
	v_pk_mul_f32 v[60:61], v[100:101], v[64:65] op_sel_hi:[0,1]
	v_pk_fma_f32 v[30:31], v[96:97], v[108:109], v[30:31] op_sel_hi:[0,1,1]
	v_pk_fma_f32 v[44:45], v[96:97], v[44:45], v[62:63] op_sel_hi:[0,1,1]
	v_pk_fma_f32 v[22:23], v[98:99], v[22:23], v[32:33] op_sel_hi:[0,1,1]
	v_pk_fma_f32 v[32:33], v[98:99], v[38:39], v[48:49] op_sel_hi:[0,1,1]
	v_pk_fma_f32 v[38:39], v[98:99], v[54:55], v[60:61] op_sel_hi:[0,1,1]
	v_pk_add_f32 v[22:23], v[30:31], v[22:23]
	v_pk_add_f32 v[30:31], v[44:45], v[38:39]
	v_pk_mul_f32 v[62:63], v[100:101], v[80:81] op_sel_hi:[0,1]
	v_mov_b32_e32 v97, v100
	v_pk_add_f32 v[28:29], v[28:29], v[32:33]
	v_pk_mul_f32 v[34:35], v[56:57], v[34:35] op_sel_hi:[0,1]
	v_pk_mul_f32 v[38:39], v[56:57], v[50:51] op_sel_hi:[0,1]
	v_pk_mul_f32 v[44:45], v[56:57], v[66:67] op_sel_hi:[0,1]
	v_pk_fma_f32 v[24:25], v[102:103], v[24:25], v[34:35] op_sel_hi:[0,1,1]
	v_pk_fma_f32 v[34:35], v[102:103], v[40:41], v[38:39] op_sel_hi:[0,1,1]
	v_pk_fma_f32 v[38:39], v[102:103], v[110:111], v[44:45] op_sel_hi:[0,1,1]
	v_mov_b32_e32 v95, v98
	v_pk_mul_f32 v[64:65], v[96:97], v[86:87]
	v_pk_fma_f32 v[48:49], v[98:99], v[70:71], v[62:63] op_sel_hi:[0,1,1]
	v_pk_add_f32 v[22:23], v[22:23], v[24:25]
	v_pk_mul_f32 v[24:25], v[104:105], v[36:37] op_sel_hi:[0,1]
	v_pk_add_f32 v[28:29], v[28:29], v[34:35]
	v_pk_mul_f32 v[34:35], v[104:105], v[52:53] op_sel_hi:[0,1]
	v_pk_add_f32 v[30:31], v[30:31], v[38:39]
	v_pk_mul_f32 v[36:37], v[104:105], v[68:69] op_sel_hi:[0,1]
	v_pk_mul_f32 v[38:39], v[104:105], v[84:85] op_sel_hi:[0,1]
	v_mov_b32_e32 v105, v56
	v_pk_fma_f32 v[54:55], v[94:95], v[76:77], v[64:65]
	v_pk_add_f32 v[32:33], v[46:47], v[48:49]
	v_pk_mul_f32 v[46:47], v[56:57], v[82:83] op_sel_hi:[0,1]
	v_pk_fma_f32 v[24:25], v[106:107], v[26:27], v[24:25] op_sel_hi:[0,1,1]
	v_pk_fma_f32 v[26:27], v[106:107], v[42:43], v[34:35] op_sel_hi:[0,1,1]
	v_pk_fma_f32 v[34:35], v[106:107], v[58:59], v[36:37] op_sel_hi:[0,1,1]
	v_pk_fma_f32 v[36:37], v[106:107], v[74:75], v[38:39] op_sel_hi:[0,1,1]
	v_mov_b32_e32 v107, v102
	v_pk_mul_f32 v[38:39], v[104:105], v[90:91]
	v_pk_fma_f32 v[40:41], v[102:103], v[72:73], v[46:47] op_sel_hi:[0,1,1]
	v_add_f32_e32 v7, v54, v55
	v_pk_add_f32 v[22:23], v[24:25], v[22:23]
	v_pk_add_f32 v[24:25], v[26:27], v[28:29]
	v_pk_add_f32 v[26:27], v[34:35], v[30:31]
	v_pk_fma_f32 v[30:31], v[106:107], v[88:89], v[38:39]
	v_pk_add_f32 v[32:33], v[32:33], v[40:41]
	v_add_f32_e32 v7, v7, v31
	v_pk_add_f32 v[28:29], v[36:37], v[32:33]
	v_add_f32_e32 v7, v30, v7
	v_pk_add_f32 v[10:11], v[10:11], v[22:23]
	v_pk_add_f32 v[12:13], v[12:13], v[24:25]
	v_pk_add_f32 v[14:15], v[14:15], v[26:27]
	v_pk_add_f32 v[16:17], v[16:17], v[28:29]
	v_add_f32_e32 v2, v2, v7
	s_waitcnt vmcnt(63)
; #define LAS __attribute__((address_space(3)))
; __device__ __forceinline__ void p0_prologue(const Args& a, const Frame& F) {
;     ...
;         for (int kk = 0; kk < 128; kk += 8) {
;             float wv[8];
; #pragma unroll
;             for (int u = 0; u < 8; ++u) wv[u] = W[(size_t)(k0 + kk + u) * 6144];
; #pragma unroll
;             for (int q = 0; q < 9; ++q) { const f32x4 s0 = *(const LAS f32x4*)(sc + q * 1024 + k0 + kk), s1 = *(const LAS f32x4*)(sc + q * 1024 + k0 + kk + 4);
;                 acc[q] += (s0.x * wv[0] + s0.y * wv[1]) + (s0.z * wv[2] + s0.w * wv[3]) + (s1.x * wv[4] + s1.y * wv[5]) + (s1.z * wv[6] + s1.w * wv[7]); }
;         }
	v_add_co_u32_e32 v94, vcc, 0x6000, v8
	v_mov_b32_e32 v7, s15
	s_nop 0
	v_addc_co_u32_e32 v95, vcc, 0, v9, vcc
	v_add_co_u32_e32 v98, vcc, 0xc000, v8
	v_mov_b32_e32 v96, v168
	s_nop 0
	v_addc_co_u32_e32 v99, vcc, 0, v9, vcc
	v_add_co_u32_e32 v100, vcc, 0x12000, v8
	ds_read_b128 v[22:25], v7
	ds_read_b128 v[26:29], v7 offset:16
	ds_read_b128 v[30:33], v7 offset:4096
	ds_read_b128 v[34:37], v7 offset:4112
	ds_read_b128 v[38:41], v7 offset:8192
	ds_read_b128 v[42:45], v7 offset:8208
	ds_read_b128 v[46:49], v7 offset:12288
	ds_read_b128 v[50:53], v7 offset:12304
	ds_read_b128 v[54:57], v7 offset:16384
	ds_read_b128 v[58:61], v7 offset:16400
	ds_read_b128 v[62:65], v7 offset:20480
	ds_read_b128 v[66:69], v7 offset:20496
	ds_read_b128 v[70:73], v7 offset:24576
	ds_read_b128 v[74:77], v7 offset:24592
	ds_read_b128 v[78:81], v7 offset:28672
	ds_read_b128 v[82:85], v7 offset:28688
	v_addc_co_u32_e32 v101, vcc, 0, v9, vcc
	v_add_co_u32_e32 v102, vcc, 0x18000, v8
	ds_read_b128 v[86:89], v7 offset:32768
	ds_read_b128 v[90:93], v7 offset:32784
	v_addc_co_u32_e32 v103, vcc, 0, v9, vcc
	v_mov_b32_e32 v94, v169
	v_add_co_u32_e32 v104, vcc, 0x1e000, v8
	v_mov_b32_e32 v98, v170
	s_nop 0
	v_mov_b32_e32 v100, v171
	v_addc_co_u32_e32 v105, vcc, 0, v9, vcc
	v_add_co_u32_e32 v106, vcc, 0x24000, v8
	v_mov_b32_e32 v102, v172
	s_waitcnt lgkmcnt(14)
	v_mov_b32_e32 v108, v22
	v_mov_b32_e32 v22, v24
	v_mov_b32_e32 v24, v26
	v_mov_b32_e32 v26, v28
	s_waitcnt lgkmcnt(13)
	v_mov_b32_e32 v28, v38
	v_mov_b32_e32 v38, v40
	s_waitcnt lgkmcnt(12)
	v_mov_b32_e32 v40, v42
	v_mov_b32_e32 v42, v44
	s_waitcnt lgkmcnt(9)
	v_mov_b32_e32 v44, v54
	v_mov_b32_e32 v54, v56
	v_mov_b32_e32 v56, v173
	v_addc_co_u32_e32 v107, vcc, 0, v9, vcc
	v_add_co_u32_e32 v104, vcc, 0x2a000, v8
	v_mov_b32_e32 v109, v30
	s_nop 0
	v_addc_co_u32_e32 v105, vcc, 0, v9, vcc
	v_mov_b32_e32 v106, v174
	s_nop 0
	v_mov_b32_e32 v104, v175
	v_mov_b32_e32 v30, v23
	v_mov_b32_e32 v23, v32
	v_mov_b32_e32 v32, v25
	v_mov_b32_e32 v25, v34
	v_mov_b32_e32 v34, v27
	v_mov_b32_e32 v27, v36
	v_mov_b32_e32 v36, v29
	v_mov_b32_e32 v29, v46
	v_mov_b32_e32 v46, v39
	s_waitcnt lgkmcnt(6)
	v_mov_b32_e32 v111, v66
	v_mov_b32_e32 v66, v59
	v_mov_b32_e32 v59, v68
	v_mov_b32_e32 v68, v61
	s_waitcnt lgkmcnt(3)
	v_mov_b32_e32 v61, v78
	v_mov_b32_e32 v78, v71
	v_mov_b32_e32 v39, v48
	v_mov_b32_e32 v48, v41
	v_mov_b32_e32 v41, v50
	v_mov_b32_e32 v50, v43
	v_mov_b32_e32 v43, v52
	v_mov_b32_e32 v52, v45
	v_mov_b32_e32 v45, v62
	v_mov_b32_e32 v62, v55
	v_mov_b32_e32 v55, v64
	v_mov_b32_e32 v64, v57
	v_mov_b32_e32 v110, v58
	v_mov_b32_e32 v58, v60
	v_mov_b32_e32 v60, v70
	v_mov_b32_e32 v71, v80
	v_mov_b32_e32 v80, v73
	v_mov_b32_e32 v70, v72
	v_mov_b32_e32 v72, v74
	s_waitcnt lgkmcnt(2)
	v_mov_b32_e32 v73, v82
	v_mov_b32_e32 v82, v75
	v_mov_b32_e32 v74, v76
	v_mov_b32_e32 v75, v84
	v_mov_b32_e32 v84, v77
	s_waitcnt lgkmcnt(1)
	v_mov_b32_e32 v76, v87
	v_mov_b32_e32 v87, v89
	v_mov_b32_e32 v77, v88
	s_waitcnt lgkmcnt(0)
	v_mov_b32_e32 v89, v90
	v_mov_b32_e32 v90, v93
	v_mov_b32_e32 v88, v92
	s_add_i32 s14, s14, 8
	s_add_i32 s15, s15, 32
	s_cmpk_gt_u32 s14, 0x77
	v_lshl_add_u64 v[8:9], v[8:9], 0, s[12:13]
	v_pk_mul_f32 v[46:47], v[94:95], v[46:47] op_sel_hi:[0,1]
	v_pk_mul_f32 v[78:79], v[94:95], v[78:79] op_sel_hi:[0,1]
	v_pk_mul_f32 v[30:31], v[94:95], v[30:31] op_sel_hi:[0,1]
	v_pk_mul_f32 v[62:63], v[94:95], v[62:63] op_sel_hi:[0,1]
	v_pk_fma_f32 v[28:29], v[96:97], v[28:29], v[46:47] op_sel_hi:[0,1,1]
	v_pk_fma_f32 v[46:47], v[96:97], v[60:61], v[78:79] op_sel_hi:[0,1,1]
	v_pk_mul_f32 v[32:33], v[100:101], v[32:33] op_sel_hi:[0,1]
	v_pk_mul_f32 v[48:49], v[100:101], v[48:49] op_sel_hi:[0,1]
	v_pk_mul_f32 v[60:61], v[100:101], v[64:65] op_sel_hi:[0,1]
	v_pk_fma_f32 v[30:31], v[96:97], v[108:109], v[30:31] op_sel_hi:[0,1,1]
	v_pk_fma_f32 v[44:45], v[96:97], v[44:45], v[62:63] op_sel_hi:[0,1,1]
	v_pk_fma_f32 v[22:23], v[98:99], v[22:23], v[32:33] op_sel_hi:[0,1,1]
	v_pk_fma_f32 v[32:33], v[98:99], v[38:39], v[48:49] op_sel_hi:[0,1,1]
	v_pk_fma_f32 v[38:39], v[98:99], v[54:55], v[60:61] op_sel_hi:[0,1,1]
	v_pk_add_f32 v[22:23], v[30:31], v[22:23]
	v_pk_add_f32 v[30:31], v[44:45], v[38:39]
	v_pk_mul_f32 v[62:63], v[100:101], v[80:81] op_sel_hi:[0,1]
	v_mov_b32_e32 v97, v100
	v_pk_add_f32 v[28:29], v[28:29], v[32:33]
	v_pk_mul_f32 v[34:35], v[56:57], v[34:35] op_sel_hi:[0,1]
	v_pk_mul_f32 v[38:39], v[56:57], v[50:51] op_sel_hi:[0,1]
	v_pk_mul_f32 v[44:45], v[56:57], v[66:67] op_sel_hi:[0,1]
	v_pk_fma_f32 v[24:25], v[102:103], v[24:25], v[34:35] op_sel_hi:[0,1,1]
	v_pk_fma_f32 v[34:35], v[102:103], v[40:41], v[38:39] op_sel_hi:[0,1,1]
	v_pk_fma_f32 v[38:39], v[102:103], v[110:111], v[44:45] op_sel_hi:[0,1,1]
	v_mov_b32_e32 v95, v98
	v_pk_mul_f32 v[64:65], v[96:97], v[86:87]
	v_pk_fma_f32 v[48:49], v[98:99], v[70:71], v[62:63] op_sel_hi:[0,1,1]
	v_pk_add_f32 v[22:23], v[22:23], v[24:25]
	v_pk_mul_f32 v[24:25], v[104:105], v[36:37] op_sel_hi:[0,1]
	v_pk_add_f32 v[28:29], v[28:29], v[34:35]
	v_pk_mul_f32 v[34:35], v[104:105], v[52:53] op_sel_hi:[0,1]
	v_pk_add_f32 v[30:31], v[30:31], v[38:39]
	v_pk_mul_f32 v[36:37], v[104:105], v[68:69] op_sel_hi:[0,1]
	v_pk_mul_f32 v[38:39], v[104:105], v[84:85] op_sel_hi:[0,1]
	v_mov_b32_e32 v105, v56
	v_pk_fma_f32 v[54:55], v[94:95], v[76:77], v[64:65]
	v_pk_add_f32 v[32:33], v[46:47], v[48:49]
	v_pk_mul_f32 v[46:47], v[56:57], v[82:83] op_sel_hi:[0,1]
	v_pk_fma_f32 v[24:25], v[106:107], v[26:27], v[24:25] op_sel_hi:[0,1,1]
	v_pk_fma_f32 v[26:27], v[106:107], v[42:43], v[34:35] op_sel_hi:[0,1,1]
	v_pk_fma_f32 v[34:35], v[106:107], v[58:59], v[36:37] op_sel_hi:[0,1,1]
	v_pk_fma_f32 v[36:37], v[106:107], v[74:75], v[38:39] op_sel_hi:[0,1,1]
	v_mov_b32_e32 v107, v102
	v_pk_mul_f32 v[38:39], v[104:105], v[90:91]
	v_pk_fma_f32 v[40:41], v[102:103], v[72:73], v[46:47] op_sel_hi:[0,1,1]
	v_add_f32_e32 v7, v54, v55
	v_pk_add_f32 v[22:23], v[24:25], v[22:23]
	v_pk_add_f32 v[24:25], v[26:27], v[28:29]
	v_pk_add_f32 v[26:27], v[34:35], v[30:31]
	v_pk_fma_f32 v[30:31], v[106:107], v[88:89], v[38:39]
	v_pk_add_f32 v[32:33], v[32:33], v[40:41]
	v_add_f32_e32 v7, v7, v31
	v_pk_add_f32 v[28:29], v[36:37], v[32:33]
	v_add_f32_e32 v7, v30, v7
	v_pk_add_f32 v[10:11], v[10:11], v[22:23]
	v_pk_add_f32 v[12:13], v[12:13], v[24:25]
	v_pk_add_f32 v[14:15], v[14:15], v[26:27]
	v_pk_add_f32 v[16:17], v[16:17], v[28:29]
	v_add_f32_e32 v2, v2, v7
	s_waitcnt vmcnt(63)
; #define LAS __attribute__((address_space(3)))
; __device__ __forceinline__ void p0_prologue(const Args& a, const Frame& F) {
;     ...
;         for (int kk = 0; kk < 128; kk += 8) {
;             float wv[8];
; #pragma unroll
;             for (int u = 0; u < 8; ++u) wv[u] = W[(size_t)(k0 + kk + u) * 6144];
; #pragma unroll
;             for (int q = 0; q < 9; ++q) { const f32x4 s0 = *(const LAS f32x4*)(sc + q * 1024 + k0 + kk), s1 = *(const LAS f32x4*)(sc + q * 1024 + k0 + kk + 4);
;                 acc[q] += (s0.x * wv[0] + s0.y * wv[1]) + (s0.z * wv[2] + s0.w * wv[3]) + (s1.x * wv[4] + s1.y * wv[5]) + (s1.z * wv[6] + s1.w * wv[7]); }
;         }
	v_add_co_u32_e32 v94, vcc, 0x6000, v8
	v_mov_b32_e32 v7, s15
	s_nop 0
	v_addc_co_u32_e32 v95, vcc, 0, v9, vcc
	v_add_co_u32_e32 v98, vcc, 0xc000, v8
	v_mov_b32_e32 v96, v176
	s_nop 0
	v_addc_co_u32_e32 v99, vcc, 0, v9, vcc
	v_add_co_u32_e32 v100, vcc, 0x12000, v8
	ds_read_b128 v[22:25], v7
	ds_read_b128 v[26:29], v7 offset:16
	ds_read_b128 v[30:33], v7 offset:4096
	ds_read_b128 v[34:37], v7 offset:4112
	ds_read_b128 v[38:41], v7 offset:8192
	ds_read_b128 v[42:45], v7 offset:8208
	ds_read_b128 v[46:49], v7 offset:12288
	ds_read_b128 v[50:53], v7 offset:12304
	ds_read_b128 v[54:57], v7 offset:16384
	ds_read_b128 v[58:61], v7 offset:16400
	ds_read_b128 v[62:65], v7 offset:20480
	ds_read_b128 v[66:69], v7 offset:20496
	ds_read_b128 v[70:73], v7 offset:24576
	ds_read_b128 v[74:77], v7 offset:24592
	ds_read_b128 v[78:81], v7 offset:28672
	ds_read_b128 v[82:85], v7 offset:28688
	v_addc_co_u32_e32 v101, vcc, 0, v9, vcc
	v_add_co_u32_e32 v102, vcc, 0x18000, v8
	ds_read_b128 v[86:89], v7 offset:32768
	ds_read_b128 v[90:93], v7 offset:32784
	v_addc_co_u32_e32 v103, vcc, 0, v9, vcc
	v_mov_b32_e32 v94, v177
	v_add_co_u32_e32 v104, vcc, 0x1e000, v8
	v_mov_b32_e32 v98, v178
	s_nop 0
	v_mov_b32_e32 v100, v179
	v_addc_co_u32_e32 v105, vcc, 0, v9, vcc
	v_add_co_u32_e32 v106, vcc, 0x24000, v8
	v_mov_b32_e32 v102, v180
	s_waitcnt lgkmcnt(14)
	v_mov_b32_e32 v108, v22
	v_mov_b32_e32 v22, v24
	v_mov_b32_e32 v24, v26
	v_mov_b32_e32 v26, v28
	s_waitcnt lgkmcnt(13)
	v_mov_b32_e32 v28, v38
	v_mov_b32_e32 v38, v40
	s_waitcnt lgkmcnt(12)
	v_mov_b32_e32 v40, v42
	v_mov_b32_e32 v42, v44
	s_waitcnt lgkmcnt(9)
	v_mov_b32_e32 v44, v54
	v_mov_b32_e32 v54, v56
	v_mov_b32_e32 v56, v181
	v_addc_co_u32_e32 v107, vcc, 0, v9, vcc
	v_add_co_u32_e32 v104, vcc, 0x2a000, v8
	v_mov_b32_e32 v109, v30
	s_nop 0
	v_addc_co_u32_e32 v105, vcc, 0, v9, vcc
	v_mov_b32_e32 v106, v182
	s_nop 0
	v_mov_b32_e32 v104, v183
	v_mov_b32_e32 v30, v23
	v_mov_b32_e32 v23, v32
	v_mov_b32_e32 v32, v25
	v_mov_b32_e32 v25, v34
	v_mov_b32_e32 v34, v27
	v_mov_b32_e32 v27, v36
	v_mov_b32_e32 v36, v29
	v_mov_b32_e32 v29, v46
	v_mov_b32_e32 v46, v39
	s_waitcnt lgkmcnt(6)
	v_mov_b32_e32 v111, v66
	v_mov_b32_e32 v66, v59
	v_mov_b32_e32 v59, v68
	v_mov_b32_e32 v68, v61
	s_waitcnt lgkmcnt(3)
	v_mov_b32_e32 v61, v78
	v_mov_b32_e32 v78, v71
	v_mov_b32_e32 v39, v48
	v_mov_b32_e32 v48, v41
	v_mov_b32_e32 v41, v50
	v_mov_b32_e32 v50, v43
	v_mov_b32_e32 v43, v52
	v_mov_b32_e32 v52, v45
	v_mov_b32_e32 v45, v62
	v_mov_b32_e32 v62, v55
	v_mov_b32_e32 v55, v64
	v_mov_b32_e32 v64, v57
	v_mov_b32_e32 v110, v58
	v_mov_b32_e32 v58, v60
	v_mov_b32_e32 v60, v70
	v_mov_b32_e32 v71, v80
	v_mov_b32_e32 v80, v73
	v_mov_b32_e32 v70, v72
	v_mov_b32_e32 v72, v74
	s_waitcnt lgkmcnt(2)
	v_mov_b32_e32 v73, v82
	v_mov_b32_e32 v82, v75
	v_mov_b32_e32 v74, v76
	v_mov_b32_e32 v75, v84
	v_mov_b32_e32 v84, v77
	s_waitcnt lgkmcnt(1)
	v_mov_b32_e32 v76, v87
	v_mov_b32_e32 v87, v89
	v_mov_b32_e32 v77, v88
	s_waitcnt lgkmcnt(0)
	v_mov_b32_e32 v89, v90
	v_mov_b32_e32 v90, v93
	v_mov_b32_e32 v88, v92
	s_add_i32 s14, s14, 8
	s_add_i32 s15, s15, 32
	s_cmpk_gt_u32 s14, 0x77
	v_lshl_add_u64 v[8:9], v[8:9], 0, s[12:13]
	v_pk_mul_f32 v[46:47], v[94:95], v[46:47] op_sel_hi:[0,1]
	v_pk_mul_f32 v[78:79], v[94:95], v[78:79] op_sel_hi:[0,1]
	v_pk_mul_f32 v[30:31], v[94:95], v[30:31] op_sel_hi:[0,1]
	v_pk_mul_f32 v[62:63], v[94:95], v[62:63] op_sel_hi:[0,1]
	v_pk_fma_f32 v[28:29], v[96:97], v[28:29], v[46:47] op_sel_hi:[0,1,1]
	v_pk_fma_f32 v[46:47], v[96:97], v[60:61], v[78:79] op_sel_hi:[0,1,1]
	v_pk_mul_f32 v[32:33], v[100:101], v[32:33] op_sel_hi:[0,1]
	v_pk_mul_f32 v[48:49], v[100:101], v[48:49] op_sel_hi:[0,1]
	v_pk_mul_f32 v[60:61], v[100:101], v[64:65] op_sel_hi:[0,1]
	v_pk_fma_f32 v[30:31], v[96:97], v[108:109], v[30:31] op_sel_hi:[0,1,1]
	v_pk_fma_f32 v[44:45], v[96:97], v[44:45], v[62:63] op_sel_hi:[0,1,1]
	v_pk_fma_f32 v[22:23], v[98:99], v[22:23], v[32:33] op_sel_hi:[0,1,1]
	v_pk_fma_f32 v[32:33], v[98:99], v[38:39], v[48:49] op_sel_hi:[0,1,1]
	v_pk_fma_f32 v[38:39], v[98:99], v[54:55], v[60:61] op_sel_hi:[0,1,1]
	v_pk_add_f32 v[22:23], v[30:31], v[22:23]
	v_pk_add_f32 v[30:31], v[44:45], v[38:39]
	v_pk_mul_f32 v[62:63], v[100:101], v[80:81] op_sel_hi:[0,1]
	v_mov_b32_e32 v97, v100
	v_pk_add_f32 v[28:29], v[28:29], v[32:33]
	v_pk_mul_f32 v[34:35], v[56:57], v[34:35] op_sel_hi:[0,1]
	v_pk_mul_f32 v[38:39], v[56:57], v[50:51] op_sel_hi:[0,1]
	v_pk_mul_f32 v[44:45], v[56:57], v[66:67] op_sel_hi:[0,1]
	v_pk_fma_f32 v[24:25], v[102:103], v[24:25], v[34:35] op_sel_hi:[0,1,1]
	v_pk_fma_f32 v[34:35], v[102:103], v[40:41], v[38:39] op_sel_hi:[0,1,1]
	v_pk_fma_f32 v[38:39], v[102:103], v[110:111], v[44:45] op_sel_hi:[0,1,1]
	v_mov_b32_e32 v95, v98
	v_pk_mul_f32 v[64:65], v[96:97], v[86:87]
	v_pk_fma_f32 v[48:49], v[98:99], v[70:71], v[62:63] op_sel_hi:[0,1,1]
	v_pk_add_f32 v[22:23], v[22:23], v[24:25]
	v_pk_mul_f32 v[24:25], v[104:105], v[36:37] op_sel_hi:[0,1]
	v_pk_add_f32 v[28:29], v[28:29], v[34:35]
	v_pk_mul_f32 v[34:35], v[104:105], v[52:53] op_sel_hi:[0,1]
	v_pk_add_f32 v[30:31], v[30:31], v[38:39]
	v_pk_mul_f32 v[36:37], v[104:105], v[68:69] op_sel_hi:[0,1]
	v_pk_mul_f32 v[38:39], v[104:105], v[84:85] op_sel_hi:[0,1]
	v_mov_b32_e32 v105, v56
	v_pk_fma_f32 v[54:55], v[94:95], v[76:77], v[64:65]
	v_pk_add_f32 v[32:33], v[46:47], v[48:49]
	v_pk_mul_f32 v[46:47], v[56:57], v[82:83] op_sel_hi:[0,1]
	v_pk_fma_f32 v[24:25], v[106:107], v[26:27], v[24:25] op_sel_hi:[0,1,1]
	v_pk_fma_f32 v[26:27], v[106:107], v[42:43], v[34:35] op_sel_hi:[0,1,1]
	v_pk_fma_f32 v[34:35], v[106:107], v[58:59], v[36:37] op_sel_hi:[0,1,1]
	v_pk_fma_f32 v[36:37], v[106:107], v[74:75], v[38:39] op_sel_hi:[0,1,1]
	v_mov_b32_e32 v107, v102
	v_pk_mul_f32 v[38:39], v[104:105], v[90:91]
	v_pk_fma_f32 v[40:41], v[102:103], v[72:73], v[46:47] op_sel_hi:[0,1,1]
	v_add_f32_e32 v7, v54, v55
	v_pk_add_f32 v[22:23], v[24:25], v[22:23]
	v_pk_add_f32 v[24:25], v[26:27], v[28:29]
	v_pk_add_f32 v[26:27], v[34:35], v[30:31]
	v_pk_fma_f32 v[30:31], v[106:107], v[88:89], v[38:39]
	v_pk_add_f32 v[32:33], v[32:33], v[40:41]
	v_add_f32_e32 v7, v7, v31
	v_pk_add_f32 v[28:29], v[36:37], v[32:33]
	v_add_f32_e32 v7, v30, v7
	v_pk_add_f32 v[10:11], v[10:11], v[22:23]
	v_pk_add_f32 v[12:13], v[12:13], v[24:25]
	v_pk_add_f32 v[14:15], v[14:15], v[26:27]
	v_pk_add_f32 v[16:17], v[16:17], v[28:29]
	v_add_f32_e32 v2, v2, v7
	s_waitcnt vmcnt(56)
; #define LAS __attribute__((address_space(3)))
; __device__ __forceinline__ void p0_prologue(const Args& a, const Frame& F) {
;     ...
;         for (int kk = 0; kk < 128; kk += 8) {
;             float wv[8];
; #pragma unroll
;             for (int u = 0; u < 8; ++u) wv[u] = W[(size_t)(k0 + kk + u) * 6144];
; #pragma unroll
;             for (int q = 0; q < 9; ++q) { const f32x4 s0 = *(const LAS f32x4*)(sc + q * 1024 + k0 + kk), s1 = *(const LAS f32x4*)(sc + q * 1024 + k0 + kk + 4);
;                 acc[q] += (s0.x * wv[0] + s0.y * wv[1]) + (s0.z * wv[2] + s0.w * wv[3]) + (s1.x * wv[4] + s1.y * wv[5]) + (s1.z * wv[6] + s1.w * wv[7]); }
;         }
	v_add_co_u32_e32 v94, vcc, 0x6000, v8
	v_mov_b32_e32 v7, s15
	s_nop 0
	v_addc_co_u32_e32 v95, vcc, 0, v9, vcc
	v_add_co_u32_e32 v98, vcc, 0xc000, v8
	v_mov_b32_e32 v96, v184
	s_nop 0
	v_addc_co_u32_e32 v99, vcc, 0, v9, vcc
	v_add_co_u32_e32 v100, vcc, 0x12000, v8
	ds_read_b128 v[22:25], v7
	ds_read_b128 v[26:29], v7 offset:16
	ds_read_b128 v[30:33], v7 offset:4096
	ds_read_b128 v[34:37], v7 offset:4112
	ds_read_b128 v[38:41], v7 offset:8192
	ds_read_b128 v[42:45], v7 offset:8208
	ds_read_b128 v[46:49], v7 offset:12288
	ds_read_b128 v[50:53], v7 offset:12304
	ds_read_b128 v[54:57], v7 offset:16384
	ds_read_b128 v[58:61], v7 offset:16400
	ds_read_b128 v[62:65], v7 offset:20480
	ds_read_b128 v[66:69], v7 offset:20496
	ds_read_b128 v[70:73], v7 offset:24576
	ds_read_b128 v[74:77], v7 offset:24592
	ds_read_b128 v[78:81], v7 offset:28672
	ds_read_b128 v[82:85], v7 offset:28688
	v_addc_co_u32_e32 v101, vcc, 0, v9, vcc
	v_add_co_u32_e32 v102, vcc, 0x18000, v8
	ds_read_b128 v[86:89], v7 offset:32768
	ds_read_b128 v[90:93], v7 offset:32784
	v_addc_co_u32_e32 v103, vcc, 0, v9, vcc
	v_mov_b32_e32 v94, v185
	v_add_co_u32_e32 v104, vcc, 0x1e000, v8
	v_mov_b32_e32 v98, v186
	s_nop 0
	v_mov_b32_e32 v100, v187
	v_addc_co_u32_e32 v105, vcc, 0, v9, vcc
	v_add_co_u32_e32 v106, vcc, 0x24000, v8
	v_mov_b32_e32 v102, v188
	s_waitcnt lgkmcnt(14)
	v_mov_b32_e32 v108, v22
	v_mov_b32_e32 v22, v24
	v_mov_b32_e32 v24, v26
	v_mov_b32_e32 v26, v28
	s_waitcnt lgkmcnt(13)
	v_mov_b32_e32 v28, v38
	v_mov_b32_e32 v38, v40
	s_waitcnt lgkmcnt(12)
	v_mov_b32_e32 v40, v42
	v_mov_b32_e32 v42, v44
	s_waitcnt lgkmcnt(9)
	v_mov_b32_e32 v44, v54
	v_mov_b32_e32 v54, v56
	v_mov_b32_e32 v56, v189
	v_addc_co_u32_e32 v107, vcc, 0, v9, vcc
	v_add_co_u32_e32 v104, vcc, 0x2a000, v8
	v_mov_b32_e32 v109, v30
	s_nop 0
	v_addc_co_u32_e32 v105, vcc, 0, v9, vcc
	v_mov_b32_e32 v106, v190
	s_nop 0
	v_mov_b32_e32 v104, v191
	v_mov_b32_e32 v30, v23
	v_mov_b32_e32 v23, v32
	v_mov_b32_e32 v32, v25
	v_mov_b32_e32 v25, v34
	v_mov_b32_e32 v34, v27
	v_mov_b32_e32 v27, v36
	v_mov_b32_e32 v36, v29
	v_mov_b32_e32 v29, v46
	v_mov_b32_e32 v46, v39
	s_waitcnt lgkmcnt(6)
	v_mov_b32_e32 v111, v66
	v_mov_b32_e32 v66, v59
	v_mov_b32_e32 v59, v68
	v_mov_b32_e32 v68, v61
	s_waitcnt lgkmcnt(3)
	v_mov_b32_e32 v61, v78
	v_mov_b32_e32 v78, v71
	v_mov_b32_e32 v39, v48
	v_mov_b32_e32 v48, v41
	v_mov_b32_e32 v41, v50
	v_mov_b32_e32 v50, v43
	v_mov_b32_e32 v43, v52
	v_mov_b32_e32 v52, v45
	v_mov_b32_e32 v45, v62
	v_mov_b32_e32 v62, v55
	v_mov_b32_e32 v55, v64
	v_mov_b32_e32 v64, v57
	v_mov_b32_e32 v110, v58
	v_mov_b32_e32 v58, v60
	v_mov_b32_e32 v60, v70
	v_mov_b32_e32 v71, v80
	v_mov_b32_e32 v80, v73
	v_mov_b32_e32 v70, v72
	v_mov_b32_e32 v72, v74
	s_waitcnt lgkmcnt(2)
	v_mov_b32_e32 v73, v82
	v_mov_b32_e32 v82, v75
	v_mov_b32_e32 v74, v76
	v_mov_b32_e32 v75, v84
	v_mov_b32_e32 v84, v77
	s_waitcnt lgkmcnt(1)
	v_mov_b32_e32 v76, v87
	v_mov_b32_e32 v87, v89
	v_mov_b32_e32 v77, v88
	s_waitcnt lgkmcnt(0)
	v_mov_b32_e32 v89, v90
	v_mov_b32_e32 v90, v93
	v_mov_b32_e32 v88, v92
	s_add_i32 s14, s14, 8
	s_add_i32 s15, s15, 32
	s_cmpk_gt_u32 s14, 0x77
	v_lshl_add_u64 v[8:9], v[8:9], 0, s[12:13]
	v_pk_mul_f32 v[46:47], v[94:95], v[46:47] op_sel_hi:[0,1]
	v_pk_mul_f32 v[78:79], v[94:95], v[78:79] op_sel_hi:[0,1]
	v_pk_mul_f32 v[30:31], v[94:95], v[30:31] op_sel_hi:[0,1]
	v_pk_mul_f32 v[62:63], v[94:95], v[62:63] op_sel_hi:[0,1]
	v_pk_fma_f32 v[28:29], v[96:97], v[28:29], v[46:47] op_sel_hi:[0,1,1]
	v_pk_fma_f32 v[46:47], v[96:97], v[60:61], v[78:79] op_sel_hi:[0,1,1]
	v_pk_mul_f32 v[32:33], v[100:101], v[32:33] op_sel_hi:[0,1]
	v_pk_mul_f32 v[48:49], v[100:101], v[48:49] op_sel_hi:[0,1]
	v_pk_mul_f32 v[60:61], v[100:101], v[64:65] op_sel_hi:[0,1]
	v_pk_fma_f32 v[30:31], v[96:97], v[108:109], v[30:31] op_sel_hi:[0,1,1]
	v_pk_fma_f32 v[44:45], v[96:97], v[44:45], v[62:63] op_sel_hi:[0,1,1]
	v_pk_fma_f32 v[22:23], v[98:99], v[22:23], v[32:33] op_sel_hi:[0,1,1]
	v_pk_fma_f32 v[32:33], v[98:99], v[38:39], v[48:49] op_sel_hi:[0,1,1]
	v_pk_fma_f32 v[38:39], v[98:99], v[54:55], v[60:61] op_sel_hi:[0,1,1]
	v_pk_add_f32 v[22:23], v[30:31], v[22:23]
	v_pk_add_f32 v[30:31], v[44:45], v[38:39]
	v_pk_mul_f32 v[62:63], v[100:101], v[80:81] op_sel_hi:[0,1]
	v_mov_b32_e32 v97, v100
	v_pk_add_f32 v[28:29], v[28:29], v[32:33]
	v_pk_mul_f32 v[34:35], v[56:57], v[34:35] op_sel_hi:[0,1]
	v_pk_mul_f32 v[38:39], v[56:57], v[50:51] op_sel_hi:[0,1]
	v_pk_mul_f32 v[44:45], v[56:57], v[66:67] op_sel_hi:[0,1]
	v_pk_fma_f32 v[24:25], v[102:103], v[24:25], v[34:35] op_sel_hi:[0,1,1]
	v_pk_fma_f32 v[34:35], v[102:103], v[40:41], v[38:39] op_sel_hi:[0,1,1]
	v_pk_fma_f32 v[38:39], v[102:103], v[110:111], v[44:45] op_sel_hi:[0,1,1]
	v_mov_b32_e32 v95, v98
	v_pk_mul_f32 v[64:65], v[96:97], v[86:87]
	v_pk_fma_f32 v[48:49], v[98:99], v[70:71], v[62:63] op_sel_hi:[0,1,1]
	v_pk_add_f32 v[22:23], v[22:23], v[24:25]
	v_pk_mul_f32 v[24:25], v[104:105], v[36:37] op_sel_hi:[0,1]
	v_pk_add_f32 v[28:29], v[28:29], v[34:35]
	v_pk_mul_f32 v[34:35], v[104:105], v[52:53] op_sel_hi:[0,1]
	v_pk_add_f32 v[30:31], v[30:31], v[38:39]
	v_pk_mul_f32 v[36:37], v[104:105], v[68:69] op_sel_hi:[0,1]
	v_pk_mul_f32 v[38:39], v[104:105], v[84:85] op_sel_hi:[0,1]
	v_mov_b32_e32 v105, v56
	v_pk_fma_f32 v[54:55], v[94:95], v[76:77], v[64:65]
	v_pk_add_f32 v[32:33], v[46:47], v[48:49]
	v_pk_mul_f32 v[46:47], v[56:57], v[82:83] op_sel_hi:[0,1]
	v_pk_fma_f32 v[24:25], v[106:107], v[26:27], v[24:25] op_sel_hi:[0,1,1]
	v_pk_fma_f32 v[26:27], v[106:107], v[42:43], v[34:35] op_sel_hi:[0,1,1]
	v_pk_fma_f32 v[34:35], v[106:107], v[58:59], v[36:37] op_sel_hi:[0,1,1]
	v_pk_fma_f32 v[36:37], v[106:107], v[74:75], v[38:39] op_sel_hi:[0,1,1]
	v_mov_b32_e32 v107, v102
	v_pk_mul_f32 v[38:39], v[104:105], v[90:91]
	v_pk_fma_f32 v[40:41], v[102:103], v[72:73], v[46:47] op_sel_hi:[0,1,1]
	v_add_f32_e32 v7, v54, v55
	v_pk_add_f32 v[22:23], v[24:25], v[22:23]
	v_pk_add_f32 v[24:25], v[26:27], v[28:29]
	v_pk_add_f32 v[26:27], v[34:35], v[30:31]
	v_pk_fma_f32 v[30:31], v[106:107], v[88:89], v[38:39]
	v_pk_add_f32 v[32:33], v[32:33], v[40:41]
	v_add_f32_e32 v7, v7, v31
	v_pk_add_f32 v[28:29], v[36:37], v[32:33]
	v_add_f32_e32 v7, v30, v7
	v_pk_add_f32 v[10:11], v[10:11], v[22:23]
	v_pk_add_f32 v[12:13], v[12:13], v[24:25]
	v_pk_add_f32 v[14:15], v[14:15], v[26:27]
	v_pk_add_f32 v[16:17], v[16:17], v[28:29]
	v_add_f32_e32 v2, v2, v7
	s_waitcnt vmcnt(48)
; #define LAS __attribute__((address_space(3)))
; __device__ __forceinline__ void p0_prologue(const Args& a, const Frame& F) {
;     ...
;         for (int kk = 0; kk < 128; kk += 8) {
;             float wv[8];
; #pragma unroll
;             for (int u = 0; u < 8; ++u) wv[u] = W[(size_t)(k0 + kk + u) * 6144];
; #pragma unroll
;             for (int q = 0; q < 9; ++q) { const f32x4 s0 = *(const LAS f32x4*)(sc + q * 1024 + k0 + kk), s1 = *(const LAS f32x4*)(sc + q * 1024 + k0 + kk + 4);
;                 acc[q] += (s0.x * wv[0] + s0.y * wv[1]) + (s0.z * wv[2] + s0.w * wv[3]) + (s1.x * wv[4] + s1.y * wv[5]) + (s1.z * wv[6] + s1.w * wv[7]); }
;         }
	v_add_co_u32_e32 v94, vcc, 0x6000, v8
	v_mov_b32_e32 v7, s15
	s_nop 0
	v_addc_co_u32_e32 v95, vcc, 0, v9, vcc
	v_add_co_u32_e32 v98, vcc, 0xc000, v8
	v_mov_b32_e32 v96, v192
	s_nop 0
	v_addc_co_u32_e32 v99, vcc, 0, v9, vcc
	v_add_co_u32_e32 v100, vcc, 0x12000, v8
	ds_read_b128 v[22:25], v7
	ds_read_b128 v[26:29], v7 offset:16
	ds_read_b128 v[30:33], v7 offset:4096
	ds_read_b128 v[34:37], v7 offset:4112
	ds_read_b128 v[38:41], v7 offset:8192
	ds_read_b128 v[42:45], v7 offset:8208
	ds_read_b128 v[46:49], v7 offset:12288
	ds_read_b128 v[50:53], v7 offset:12304
	ds_read_b128 v[54:57], v7 offset:16384
	ds_read_b128 v[58:61], v7 offset:16400
	ds_read_b128 v[62:65], v7 offset:20480
	ds_read_b128 v[66:69], v7 offset:20496
	ds_read_b128 v[70:73], v7 offset:24576
	ds_read_b128 v[74:77], v7 offset:24592
	ds_read_b128 v[78:81], v7 offset:28672
	ds_read_b128 v[82:85], v7 offset:28688
	v_addc_co_u32_e32 v101, vcc, 0, v9, vcc
	v_add_co_u32_e32 v102, vcc, 0x18000, v8
	ds_read_b128 v[86:89], v7 offset:32768
	ds_read_b128 v[90:93], v7 offset:32784
	v_addc_co_u32_e32 v103, vcc, 0, v9, vcc
	v_mov_b32_e32 v94, v193
	v_add_co_u32_e32 v104, vcc, 0x1e000, v8
	v_mov_b32_e32 v98, v194
	s_nop 0
	v_mov_b32_e32 v100, v195
	v_addc_co_u32_e32 v105, vcc, 0, v9, vcc
	v_add_co_u32_e32 v106, vcc, 0x24000, v8
	v_mov_b32_e32 v102, v196
	s_waitcnt lgkmcnt(14)
	v_mov_b32_e32 v108, v22
	v_mov_b32_e32 v22, v24
	v_mov_b32_e32 v24, v26
	v_mov_b32_e32 v26, v28
	s_waitcnt lgkmcnt(13)
	v_mov_b32_e32 v28, v38
	v_mov_b32_e32 v38, v40
	s_waitcnt lgkmcnt(12)
	v_mov_b32_e32 v40, v42
	v_mov_b32_e32 v42, v44
	s_waitcnt lgkmcnt(9)
	v_mov_b32_e32 v44, v54
	v_mov_b32_e32 v54, v56
	v_mov_b32_e32 v56, v197
	v_addc_co_u32_e32 v107, vcc, 0, v9, vcc
	v_add_co_u32_e32 v104, vcc, 0x2a000, v8
	v_mov_b32_e32 v109, v30
	s_nop 0
	v_addc_co_u32_e32 v105, vcc, 0, v9, vcc
	v_mov_b32_e32 v106, v198
	s_nop 0
	v_mov_b32_e32 v104, v199
	v_mov_b32_e32 v30, v23
	v_mov_b32_e32 v23, v32
	v_mov_b32_e32 v32, v25
	v_mov_b32_e32 v25, v34
	v_mov_b32_e32 v34, v27
	v_mov_b32_e32 v27, v36
	v_mov_b32_e32 v36, v29
	v_mov_b32_e32 v29, v46
	v_mov_b32_e32 v46, v39
	s_waitcnt lgkmcnt(6)
	v_mov_b32_e32 v111, v66
	v_mov_b32_e32 v66, v59
	v_mov_b32_e32 v59, v68
	v_mov_b32_e32 v68, v61
	s_waitcnt lgkmcnt(3)
	v_mov_b32_e32 v61, v78
	v_mov_b32_e32 v78, v71
	v_mov_b32_e32 v39, v48
	v_mov_b32_e32 v48, v41
	v_mov_b32_e32 v41, v50
	v_mov_b32_e32 v50, v43
	v_mov_b32_e32 v43, v52
	v_mov_b32_e32 v52, v45
	v_mov_b32_e32 v45, v62
	v_mov_b32_e32 v62, v55
	v_mov_b32_e32 v55, v64
	v_mov_b32_e32 v64, v57
	v_mov_b32_e32 v110, v58
	v_mov_b32_e32 v58, v60
	v_mov_b32_e32 v60, v70
	v_mov_b32_e32 v71, v80
	v_mov_b32_e32 v80, v73
	v_mov_b32_e32 v70, v72
	v_mov_b32_e32 v72, v74
	s_waitcnt lgkmcnt(2)
	v_mov_b32_e32 v73, v82
	v_mov_b32_e32 v82, v75
	v_mov_b32_e32 v74, v76
	v_mov_b32_e32 v75, v84
	v_mov_b32_e32 v84, v77
	s_waitcnt lgkmcnt(1)
	v_mov_b32_e32 v76, v87
	v_mov_b32_e32 v87, v89
	v_mov_b32_e32 v77, v88
	s_waitcnt lgkmcnt(0)
	v_mov_b32_e32 v89, v90
	v_mov_b32_e32 v90, v93
	v_mov_b32_e32 v88, v92
	s_add_i32 s14, s14, 8
	s_add_i32 s15, s15, 32
	s_cmpk_gt_u32 s14, 0x77
	v_lshl_add_u64 v[8:9], v[8:9], 0, s[12:13]
	v_pk_mul_f32 v[46:47], v[94:95], v[46:47] op_sel_hi:[0,1]
	v_pk_mul_f32 v[78:79], v[94:95], v[78:79] op_sel_hi:[0,1]
	v_pk_mul_f32 v[30:31], v[94:95], v[30:31] op_sel_hi:[0,1]
	v_pk_mul_f32 v[62:63], v[94:95], v[62:63] op_sel_hi:[0,1]
	v_pk_fma_f32 v[28:29], v[96:97], v[28:29], v[46:47] op_sel_hi:[0,1,1]
	v_pk_fma_f32 v[46:47], v[96:97], v[60:61], v[78:79] op_sel_hi:[0,1,1]
	v_pk_mul_f32 v[32:33], v[100:101], v[32:33] op_sel_hi:[0,1]
	v_pk_mul_f32 v[48:49], v[100:101], v[48:49] op_sel_hi:[0,1]
	v_pk_mul_f32 v[60:61], v[100:101], v[64:65] op_sel_hi:[0,1]
	v_pk_fma_f32 v[30:31], v[96:97], v[108:109], v[30:31] op_sel_hi:[0,1,1]
	v_pk_fma_f32 v[44:45], v[96:97], v[44:45], v[62:63] op_sel_hi:[0,1,1]
	v_pk_fma_f32 v[22:23], v[98:99], v[22:23], v[32:33] op_sel_hi:[0,1,1]
	v_pk_fma_f32 v[32:33], v[98:99], v[38:39], v[48:49] op_sel_hi:[0,1,1]
	v_pk_fma_f32 v[38:39], v[98:99], v[54:55], v[60:61] op_sel_hi:[0,1,1]
	v_pk_add_f32 v[22:23], v[30:31], v[22:23]
	v_pk_add_f32 v[30:31], v[44:45], v[38:39]
	v_pk_mul_f32 v[62:63], v[100:101], v[80:81] op_sel_hi:[0,1]
	v_mov_b32_e32 v97, v100
	v_pk_add_f32 v[28:29], v[28:29], v[32:33]
	v_pk_mul_f32 v[34:35], v[56:57], v[34:35] op_sel_hi:[0,1]
	v_pk_mul_f32 v[38:39], v[56:57], v[50:51] op_sel_hi:[0,1]
	v_pk_mul_f32 v[44:45], v[56:57], v[66:67] op_sel_hi:[0,1]
	v_pk_fma_f32 v[24:25], v[102:103], v[24:25], v[34:35] op_sel_hi:[0,1,1]
	v_pk_fma_f32 v[34:35], v[102:103], v[40:41], v[38:39] op_sel_hi:[0,1,1]
	v_pk_fma_f32 v[38:39], v[102:103], v[110:111], v[44:45] op_sel_hi:[0,1,1]
	v_mov_b32_e32 v95, v98
	v_pk_mul_f32 v[64:65], v[96:97], v[86:87]
	v_pk_fma_f32 v[48:49], v[98:99], v[70:71], v[62:63] op_sel_hi:[0,1,1]
	v_pk_add_f32 v[22:23], v[22:23], v[24:25]
	v_pk_mul_f32 v[24:25], v[104:105], v[36:37] op_sel_hi:[0,1]
	v_pk_add_f32 v[28:29], v[28:29], v[34:35]
	v_pk_mul_f32 v[34:35], v[104:105], v[52:53] op_sel_hi:[0,1]
	v_pk_add_f32 v[30:31], v[30:31], v[38:39]
	v_pk_mul_f32 v[36:37], v[104:105], v[68:69] op_sel_hi:[0,1]
	v_pk_mul_f32 v[38:39], v[104:105], v[84:85] op_sel_hi:[0,1]
	v_mov_b32_e32 v105, v56
	v_pk_fma_f32 v[54:55], v[94:95], v[76:77], v[64:65]
	v_pk_add_f32 v[32:33], v[46:47], v[48:49]
	v_pk_mul_f32 v[46:47], v[56:57], v[82:83] op_sel_hi:[0,1]
	v_pk_fma_f32 v[24:25], v[106:107], v[26:27], v[24:25] op_sel_hi:[0,1,1]
	v_pk_fma_f32 v[26:27], v[106:107], v[42:43], v[34:35] op_sel_hi:[0,1,1]
	v_pk_fma_f32 v[34:35], v[106:107], v[58:59], v[36:37] op_sel_hi:[0,1,1]
	v_pk_fma_f32 v[36:37], v[106:107], v[74:75], v[38:39] op_sel_hi:[0,1,1]
	v_mov_b32_e32 v107, v102
	v_pk_mul_f32 v[38:39], v[104:105], v[90:91]
	v_pk_fma_f32 v[40:41], v[102:103], v[72:73], v[46:47] op_sel_hi:[0,1,1]
	v_add_f32_e32 v7, v54, v55
	v_pk_add_f32 v[22:23], v[24:25], v[22:23]
	v_pk_add_f32 v[24:25], v[26:27], v[28:29]
	v_pk_add_f32 v[26:27], v[34:35], v[30:31]
	v_pk_fma_f32 v[30:31], v[106:107], v[88:89], v[38:39]
	v_pk_add_f32 v[32:33], v[32:33], v[40:41]
	v_add_f32_e32 v7, v7, v31
	v_pk_add_f32 v[28:29], v[36:37], v[32:33]
	v_add_f32_e32 v7, v30, v7
	v_pk_add_f32 v[10:11], v[10:11], v[22:23]
	v_pk_add_f32 v[12:13], v[12:13], v[24:25]
	v_pk_add_f32 v[14:15], v[14:15], v[26:27]
	v_pk_add_f32 v[16:17], v[16:17], v[28:29]
	v_add_f32_e32 v2, v2, v7
	s_waitcnt vmcnt(40)
; #define LAS __attribute__((address_space(3)))
; __device__ __forceinline__ void p0_prologue(const Args& a, const Frame& F) {
;     ...
;         for (int kk = 0; kk < 128; kk += 8) {
;             float wv[8];
; #pragma unroll
;             for (int u = 0; u < 8; ++u) wv[u] = W[(size_t)(k0 + kk + u) * 6144];
; #pragma unroll
;             for (int q = 0; q < 9; ++q) { const f32x4 s0 = *(const LAS f32x4*)(sc + q * 1024 + k0 + kk), s1 = *(const LAS f32x4*)(sc + q * 1024 + k0 + kk + 4);
;                 acc[q] += (s0.x * wv[0] + s0.y * wv[1]) + (s0.z * wv[2] + s0.w * wv[3]) + (s1.x * wv[4] + s1.y * wv[5]) + (s1.z * wv[6] + s1.w * wv[7]); }
;         }
	v_add_co_u32_e32 v94, vcc, 0x6000, v8
	v_mov_b32_e32 v7, s15
	s_nop 0
	v_addc_co_u32_e32 v95, vcc, 0, v9, vcc
	v_add_co_u32_e32 v98, vcc, 0xc000, v8
	v_mov_b32_e32 v96, v200
	s_nop 0
	v_addc_co_u32_e32 v99, vcc, 0, v9, vcc
	v_add_co_u32_e32 v100, vcc, 0x12000, v8
	ds_read_b128 v[22:25], v7
	ds_read_b128 v[26:29], v7 offset:16
	ds_read_b128 v[30:33], v7 offset:4096
	ds_read_b128 v[34:37], v7 offset:4112
	ds_read_b128 v[38:41], v7 offset:8192
	ds_read_b128 v[42:45], v7 offset:8208
	ds_read_b128 v[46:49], v7 offset:12288
	ds_read_b128 v[50:53], v7 offset:12304
	ds_read_b128 v[54:57], v7 offset:16384
	ds_read_b128 v[58:61], v7 offset:16400
	ds_read_b128 v[62:65], v7 offset:20480
	ds_read_b128 v[66:69], v7 offset:20496
	ds_read_b128 v[70:73], v7 offset:24576
	ds_read_b128 v[74:77], v7 offset:24592
	ds_read_b128 v[78:81], v7 offset:28672
	ds_read_b128 v[82:85], v7 offset:28688
	v_addc_co_u32_e32 v101, vcc, 0, v9, vcc
	v_add_co_u32_e32 v102, vcc, 0x18000, v8
	ds_read_b128 v[86:89], v7 offset:32768
	ds_read_b128 v[90:93], v7 offset:32784
	v_addc_co_u32_e32 v103, vcc, 0, v9, vcc
	v_mov_b32_e32 v94, v201
	v_add_co_u32_e32 v104, vcc, 0x1e000, v8
	v_mov_b32_e32 v98, v202
	s_nop 0
	v_mov_b32_e32 v100, v203
	v_addc_co_u32_e32 v105, vcc, 0, v9, vcc
	v_add_co_u32_e32 v106, vcc, 0x24000, v8
	v_mov_b32_e32 v102, v204
	s_waitcnt lgkmcnt(14)
	v_mov_b32_e32 v108, v22
	v_mov_b32_e32 v22, v24
	v_mov_b32_e32 v24, v26
	v_mov_b32_e32 v26, v28
	s_waitcnt lgkmcnt(13)
	v_mov_b32_e32 v28, v38
	v_mov_b32_e32 v38, v40
	s_waitcnt lgkmcnt(12)
	v_mov_b32_e32 v40, v42
	v_mov_b32_e32 v42, v44
	s_waitcnt lgkmcnt(9)
	v_mov_b32_e32 v44, v54
	v_mov_b32_e32 v54, v56
	v_mov_b32_e32 v56, v205
	v_addc_co_u32_e32 v107, vcc, 0, v9, vcc
	v_add_co_u32_e32 v104, vcc, 0x2a000, v8
	v_mov_b32_e32 v109, v30
	s_nop 0
	v_addc_co_u32_e32 v105, vcc, 0, v9, vcc
	v_mov_b32_e32 v106, v206
	s_nop 0
	v_mov_b32_e32 v104, v207
	v_mov_b32_e32 v30, v23
	v_mov_b32_e32 v23, v32
	v_mov_b32_e32 v32, v25
	v_mov_b32_e32 v25, v34
	v_mov_b32_e32 v34, v27
	v_mov_b32_e32 v27, v36
	v_mov_b32_e32 v36, v29
	v_mov_b32_e32 v29, v46
	v_mov_b32_e32 v46, v39
	s_waitcnt lgkmcnt(6)
	v_mov_b32_e32 v111, v66
	v_mov_b32_e32 v66, v59
	v_mov_b32_e32 v59, v68
	v_mov_b32_e32 v68, v61
	s_waitcnt lgkmcnt(3)
	v_mov_b32_e32 v61, v78
	v_mov_b32_e32 v78, v71
	v_mov_b32_e32 v39, v48
	v_mov_b32_e32 v48, v41
	v_mov_b32_e32 v41, v50
	v_mov_b32_e32 v50, v43
	v_mov_b32_e32 v43, v52
	v_mov_b32_e32 v52, v45
	v_mov_b32_e32 v45, v62
	v_mov_b32_e32 v62, v55
	v_mov_b32_e32 v55, v64
	v_mov_b32_e32 v64, v57
	v_mov_b32_e32 v110, v58
	v_mov_b32_e32 v58, v60
	v_mov_b32_e32 v60, v70
	v_mov_b32_e32 v71, v80
	v_mov_b32_e32 v80, v73
	v_mov_b32_e32 v70, v72
	v_mov_b32_e32 v72, v74
	s_waitcnt lgkmcnt(2)
	v_mov_b32_e32 v73, v82
	v_mov_b32_e32 v82, v75
	v_mov_b32_e32 v74, v76
	v_mov_b32_e32 v75, v84
	v_mov_b32_e32 v84, v77
	s_waitcnt lgkmcnt(1)
	v_mov_b32_e32 v76, v87
	v_mov_b32_e32 v87, v89
	v_mov_b32_e32 v77, v88
	s_waitcnt lgkmcnt(0)
	v_mov_b32_e32 v89, v90
	v_mov_b32_e32 v90, v93
	v_mov_b32_e32 v88, v92
	s_add_i32 s14, s14, 8
	s_add_i32 s15, s15, 32
	s_cmpk_gt_u32 s14, 0x77
	v_lshl_add_u64 v[8:9], v[8:9], 0, s[12:13]
	v_pk_mul_f32 v[46:47], v[94:95], v[46:47] op_sel_hi:[0,1]
	v_pk_mul_f32 v[78:79], v[94:95], v[78:79] op_sel_hi:[0,1]
	v_pk_mul_f32 v[30:31], v[94:95], v[30:31] op_sel_hi:[0,1]
	v_pk_mul_f32 v[62:63], v[94:95], v[62:63] op_sel_hi:[0,1]
	v_pk_fma_f32 v[28:29], v[96:97], v[28:29], v[46:47] op_sel_hi:[0,1,1]
	v_pk_fma_f32 v[46:47], v[96:97], v[60:61], v[78:79] op_sel_hi:[0,1,1]
	v_pk_mul_f32 v[32:33], v[100:101], v[32:33] op_sel_hi:[0,1]
	v_pk_mul_f32 v[48:49], v[100:101], v[48:49] op_sel_hi:[0,1]
	v_pk_mul_f32 v[60:61], v[100:101], v[64:65] op_sel_hi:[0,1]
	v_pk_fma_f32 v[30:31], v[96:97], v[108:109], v[30:31] op_sel_hi:[0,1,1]
	v_pk_fma_f32 v[44:45], v[96:97], v[44:45], v[62:63] op_sel_hi:[0,1,1]
	v_pk_fma_f32 v[22:23], v[98:99], v[22:23], v[32:33] op_sel_hi:[0,1,1]
	v_pk_fma_f32 v[32:33], v[98:99], v[38:39], v[48:49] op_sel_hi:[0,1,1]
	v_pk_fma_f32 v[38:39], v[98:99], v[54:55], v[60:61] op_sel_hi:[0,1,1]
	v_pk_add_f32 v[22:23], v[30:31], v[22:23]
	v_pk_add_f32 v[30:31], v[44:45], v[38:39]
	v_pk_mul_f32 v[62:63], v[100:101], v[80:81] op_sel_hi:[0,1]
	v_mov_b32_e32 v97, v100
	v_pk_add_f32 v[28:29], v[28:29], v[32:33]
	v_pk_mul_f32 v[34:35], v[56:57], v[34:35] op_sel_hi:[0,1]
	v_pk_mul_f32 v[38:39], v[56:57], v[50:51] op_sel_hi:[0,1]
	v_pk_mul_f32 v[44:45], v[56:57], v[66:67] op_sel_hi:[0,1]
	v_pk_fma_f32 v[24:25], v[102:103], v[24:25], v[34:35] op_sel_hi:[0,1,1]
	v_pk_fma_f32 v[34:35], v[102:103], v[40:41], v[38:39] op_sel_hi:[0,1,1]
	v_pk_fma_f32 v[38:39], v[102:103], v[110:111], v[44:45] op_sel_hi:[0,1,1]
	v_mov_b32_e32 v95, v98
	v_pk_mul_f32 v[64:65], v[96:97], v[86:87]
	v_pk_fma_f32 v[48:49], v[98:99], v[70:71], v[62:63] op_sel_hi:[0,1,1]
	v_pk_add_f32 v[22:23], v[22:23], v[24:25]
	v_pk_mul_f32 v[24:25], v[104:105], v[36:37] op_sel_hi:[0,1]
	v_pk_add_f32 v[28:29], v[28:29], v[34:35]
	v_pk_mul_f32 v[34:35], v[104:105], v[52:53] op_sel_hi:[0,1]
	v_pk_add_f32 v[30:31], v[30:31], v[38:39]
	v_pk_mul_f32 v[36:37], v[104:105], v[68:69] op_sel_hi:[0,1]
	v_pk_mul_f32 v[38:39], v[104:105], v[84:85] op_sel_hi:[0,1]
	v_mov_b32_e32 v105, v56
	v_pk_fma_f32 v[54:55], v[94:95], v[76:77], v[64:65]
	v_pk_add_f32 v[32:33], v[46:47], v[48:49]
	v_pk_mul_f32 v[46:47], v[56:57], v[82:83] op_sel_hi:[0,1]
	v_pk_fma_f32 v[24:25], v[106:107], v[26:27], v[24:25] op_sel_hi:[0,1,1]
	v_pk_fma_f32 v[26:27], v[106:107], v[42:43], v[34:35] op_sel_hi:[0,1,1]
	v_pk_fma_f32 v[34:35], v[106:107], v[58:59], v[36:37] op_sel_hi:[0,1,1]
	v_pk_fma_f32 v[36:37], v[106:107], v[74:75], v[38:39] op_sel_hi:[0,1,1]
	v_mov_b32_e32 v107, v102
	v_pk_mul_f32 v[38:39], v[104:105], v[90:91]
	v_pk_fma_f32 v[40:41], v[102:103], v[72:73], v[46:47] op_sel_hi:[0,1,1]
	v_add_f32_e32 v7, v54, v55
	v_pk_add_f32 v[22:23], v[24:25], v[22:23]
	v_pk_add_f32 v[24:25], v[26:27], v[28:29]
	v_pk_add_f32 v[26:27], v[34:35], v[30:31]
	v_pk_fma_f32 v[30:31], v[106:107], v[88:89], v[38:39]
	v_pk_add_f32 v[32:33], v[32:33], v[40:41]
	v_add_f32_e32 v7, v7, v31
	v_pk_add_f32 v[28:29], v[36:37], v[32:33]
	v_add_f32_e32 v7, v30, v7
	v_pk_add_f32 v[10:11], v[10:11], v[22:23]
	v_pk_add_f32 v[12:13], v[12:13], v[24:25]
	v_pk_add_f32 v[14:15], v[14:15], v[26:27]
	v_pk_add_f32 v[16:17], v[16:17], v[28:29]
	v_add_f32_e32 v2, v2, v7
	s_waitcnt vmcnt(32)
; #define LAS __attribute__((address_space(3)))
; __device__ __forceinline__ void p0_prologue(const Args& a, const Frame& F) {
;     ...
;         for (int kk = 0; kk < 128; kk += 8) {
;             float wv[8];
; #pragma unroll
;             for (int u = 0; u < 8; ++u) wv[u] = W[(size_t)(k0 + kk + u) * 6144];
; #pragma unroll
;             for (int q = 0; q < 9; ++q) { const f32x4 s0 = *(const LAS f32x4*)(sc + q * 1024 + k0 + kk), s1 = *(const LAS f32x4*)(sc + q * 1024 + k0 + kk + 4);
;                 acc[q] += (s0.x * wv[0] + s0.y * wv[1]) + (s0.z * wv[2] + s0.w * wv[3]) + (s1.x * wv[4] + s1.y * wv[5]) + (s1.z * wv[6] + s1.w * wv[7]); }
;         }
	v_add_co_u32_e32 v94, vcc, 0x6000, v8
	v_mov_b32_e32 v7, s15
	s_nop 0
	v_addc_co_u32_e32 v95, vcc, 0, v9, vcc
	v_add_co_u32_e32 v98, vcc, 0xc000, v8
	v_mov_b32_e32 v96, v208
	s_nop 0
	v_addc_co_u32_e32 v99, vcc, 0, v9, vcc
	v_add_co_u32_e32 v100, vcc, 0x12000, v8
	ds_read_b128 v[22:25], v7
	ds_read_b128 v[26:29], v7 offset:16
	ds_read_b128 v[30:33], v7 offset:4096
	ds_read_b128 v[34:37], v7 offset:4112
	ds_read_b128 v[38:41], v7 offset:8192
	ds_read_b128 v[42:45], v7 offset:8208
	ds_read_b128 v[46:49], v7 offset:12288
	ds_read_b128 v[50:53], v7 offset:12304
	ds_read_b128 v[54:57], v7 offset:16384
	ds_read_b128 v[58:61], v7 offset:16400
	ds_read_b128 v[62:65], v7 offset:20480
	ds_read_b128 v[66:69], v7 offset:20496
	ds_read_b128 v[70:73], v7 offset:24576
	ds_read_b128 v[74:77], v7 offset:24592
	ds_read_b128 v[78:81], v7 offset:28672
	ds_read_b128 v[82:85], v7 offset:28688
	v_addc_co_u32_e32 v101, vcc, 0, v9, vcc
	v_add_co_u32_e32 v102, vcc, 0x18000, v8
	ds_read_b128 v[86:89], v7 offset:32768
	ds_read_b128 v[90:93], v7 offset:32784
	v_addc_co_u32_e32 v103, vcc, 0, v9, vcc
	v_mov_b32_e32 v94, v209
	v_add_co_u32_e32 v104, vcc, 0x1e000, v8
	v_mov_b32_e32 v98, v210
	s_nop 0
	v_mov_b32_e32 v100, v211
	v_addc_co_u32_e32 v105, vcc, 0, v9, vcc
	v_add_co_u32_e32 v106, vcc, 0x24000, v8
	v_mov_b32_e32 v102, v212
	s_waitcnt lgkmcnt(14)
	v_mov_b32_e32 v108, v22
	v_mov_b32_e32 v22, v24
	v_mov_b32_e32 v24, v26
	v_mov_b32_e32 v26, v28
	s_waitcnt lgkmcnt(13)
	v_mov_b32_e32 v28, v38
	v_mov_b32_e32 v38, v40
	s_waitcnt lgkmcnt(12)
	v_mov_b32_e32 v40, v42
	v_mov_b32_e32 v42, v44
	s_waitcnt lgkmcnt(9)
	v_mov_b32_e32 v44, v54
	v_mov_b32_e32 v54, v56
	v_mov_b32_e32 v56, v213
	v_addc_co_u32_e32 v107, vcc, 0, v9, vcc
	v_add_co_u32_e32 v104, vcc, 0x2a000, v8
	v_mov_b32_e32 v109, v30
	s_nop 0
	v_addc_co_u32_e32 v105, vcc, 0, v9, vcc
	v_mov_b32_e32 v106, v214
	s_nop 0
	v_mov_b32_e32 v104, v215
	v_mov_b32_e32 v30, v23
	v_mov_b32_e32 v23, v32
	v_mov_b32_e32 v32, v25
	v_mov_b32_e32 v25, v34
	v_mov_b32_e32 v34, v27
	v_mov_b32_e32 v27, v36
	v_mov_b32_e32 v36, v29
	v_mov_b32_e32 v29, v46
	v_mov_b32_e32 v46, v39
	s_waitcnt lgkmcnt(6)
	v_mov_b32_e32 v111, v66
	v_mov_b32_e32 v66, v59
	v_mov_b32_e32 v59, v68
	v_mov_b32_e32 v68, v61
	s_waitcnt lgkmcnt(3)
	v_mov_b32_e32 v61, v78
	v_mov_b32_e32 v78, v71
	v_mov_b32_e32 v39, v48
	v_mov_b32_e32 v48, v41
	v_mov_b32_e32 v41, v50
	v_mov_b32_e32 v50, v43
	v_mov_b32_e32 v43, v52
	v_mov_b32_e32 v52, v45
	v_mov_b32_e32 v45, v62
	v_mov_b32_e32 v62, v55
	v_mov_b32_e32 v55, v64
	v_mov_b32_e32 v64, v57
	v_mov_b32_e32 v110, v58
	v_mov_b32_e32 v58, v60
	v_mov_b32_e32 v60, v70
	v_mov_b32_e32 v71, v80
	v_mov_b32_e32 v80, v73
	v_mov_b32_e32 v70, v72
	v_mov_b32_e32 v72, v74
	s_waitcnt lgkmcnt(2)
	v_mov_b32_e32 v73, v82
	v_mov_b32_e32 v82, v75
	v_mov_b32_e32 v74, v76
	v_mov_b32_e32 v75, v84
	v_mov_b32_e32 v84, v77
	s_waitcnt lgkmcnt(1)
	v_mov_b32_e32 v76, v87
	v_mov_b32_e32 v87, v89
	v_mov_b32_e32 v77, v88
	s_waitcnt lgkmcnt(0)
	v_mov_b32_e32 v89, v90
	v_mov_b32_e32 v90, v93
	v_mov_b32_e32 v88, v92
	s_add_i32 s14, s14, 8
	s_add_i32 s15, s15, 32
	s_cmpk_gt_u32 s14, 0x77
	v_lshl_add_u64 v[8:9], v[8:9], 0, s[12:13]
	v_pk_mul_f32 v[46:47], v[94:95], v[46:47] op_sel_hi:[0,1]
	v_pk_mul_f32 v[78:79], v[94:95], v[78:79] op_sel_hi:[0,1]
	v_pk_mul_f32 v[30:31], v[94:95], v[30:31] op_sel_hi:[0,1]
	v_pk_mul_f32 v[62:63], v[94:95], v[62:63] op_sel_hi:[0,1]
	v_pk_fma_f32 v[28:29], v[96:97], v[28:29], v[46:47] op_sel_hi:[0,1,1]
	v_pk_fma_f32 v[46:47], v[96:97], v[60:61], v[78:79] op_sel_hi:[0,1,1]
	v_pk_mul_f32 v[32:33], v[100:101], v[32:33] op_sel_hi:[0,1]
	v_pk_mul_f32 v[48:49], v[100:101], v[48:49] op_sel_hi:[0,1]
	v_pk_mul_f32 v[60:61], v[100:101], v[64:65] op_sel_hi:[0,1]
	v_pk_fma_f32 v[30:31], v[96:97], v[108:109], v[30:31] op_sel_hi:[0,1,1]
	v_pk_fma_f32 v[44:45], v[96:97], v[44:45], v[62:63] op_sel_hi:[0,1,1]
	v_pk_fma_f32 v[22:23], v[98:99], v[22:23], v[32:33] op_sel_hi:[0,1,1]
	v_pk_fma_f32 v[32:33], v[98:99], v[38:39], v[48:49] op_sel_hi:[0,1,1]
	v_pk_fma_f32 v[38:39], v[98:99], v[54:55], v[60:61] op_sel_hi:[0,1,1]
	v_pk_add_f32 v[22:23], v[30:31], v[22:23]
	v_pk_add_f32 v[30:31], v[44:45], v[38:39]
	v_pk_mul_f32 v[62:63], v[100:101], v[80:81] op_sel_hi:[0,1]
	v_mov_b32_e32 v97, v100
	v_pk_add_f32 v[28:29], v[28:29], v[32:33]
	v_pk_mul_f32 v[34:35], v[56:57], v[34:35] op_sel_hi:[0,1]
	v_pk_mul_f32 v[38:39], v[56:57], v[50:51] op_sel_hi:[0,1]
	v_pk_mul_f32 v[44:45], v[56:57], v[66:67] op_sel_hi:[0,1]
	v_pk_fma_f32 v[24:25], v[102:103], v[24:25], v[34:35] op_sel_hi:[0,1,1]
	v_pk_fma_f32 v[34:35], v[102:103], v[40:41], v[38:39] op_sel_hi:[0,1,1]
	v_pk_fma_f32 v[38:39], v[102:103], v[110:111], v[44:45] op_sel_hi:[0,1,1]
	v_mov_b32_e32 v95, v98
	v_pk_mul_f32 v[64:65], v[96:97], v[86:87]
	v_pk_fma_f32 v[48:49], v[98:99], v[70:71], v[62:63] op_sel_hi:[0,1,1]
	v_pk_add_f32 v[22:23], v[22:23], v[24:25]
	v_pk_mul_f32 v[24:25], v[104:105], v[36:37] op_sel_hi:[0,1]
	v_pk_add_f32 v[28:29], v[28:29], v[34:35]
	v_pk_mul_f32 v[34:35], v[104:105], v[52:53] op_sel_hi:[0,1]
	v_pk_add_f32 v[30:31], v[30:31], v[38:39]
	v_pk_mul_f32 v[36:37], v[104:105], v[68:69] op_sel_hi:[0,1]
	v_pk_mul_f32 v[38:39], v[104:105], v[84:85] op_sel_hi:[0,1]
	v_mov_b32_e32 v105, v56
	v_pk_fma_f32 v[54:55], v[94:95], v[76:77], v[64:65]
	v_pk_add_f32 v[32:33], v[46:47], v[48:49]
	v_pk_mul_f32 v[46:47], v[56:57], v[82:83] op_sel_hi:[0,1]
	v_pk_fma_f32 v[24:25], v[106:107], v[26:27], v[24:25] op_sel_hi:[0,1,1]
	v_pk_fma_f32 v[26:27], v[106:107], v[42:43], v[34:35] op_sel_hi:[0,1,1]
	v_pk_fma_f32 v[34:35], v[106:107], v[58:59], v[36:37] op_sel_hi:[0,1,1]
	v_pk_fma_f32 v[36:37], v[106:107], v[74:75], v[38:39] op_sel_hi:[0,1,1]
	v_mov_b32_e32 v107, v102
	v_pk_mul_f32 v[38:39], v[104:105], v[90:91]
	v_pk_fma_f32 v[40:41], v[102:103], v[72:73], v[46:47] op_sel_hi:[0,1,1]
	v_add_f32_e32 v7, v54, v55
	v_pk_add_f32 v[22:23], v[24:25], v[22:23]
	v_pk_add_f32 v[24:25], v[26:27], v[28:29]
	v_pk_add_f32 v[26:27], v[34:35], v[30:31]
	v_pk_fma_f32 v[30:31], v[106:107], v[88:89], v[38:39]
	v_pk_add_f32 v[32:33], v[32:33], v[40:41]
	v_add_f32_e32 v7, v7, v31
	v_pk_add_f32 v[28:29], v[36:37], v[32:33]
	v_add_f32_e32 v7, v30, v7
	v_pk_add_f32 v[10:11], v[10:11], v[22:23]
	v_pk_add_f32 v[12:13], v[12:13], v[24:25]
	v_pk_add_f32 v[14:15], v[14:15], v[26:27]
	v_pk_add_f32 v[16:17], v[16:17], v[28:29]
	v_add_f32_e32 v2, v2, v7
	s_waitcnt vmcnt(24)
; #define LAS __attribute__((address_space(3)))
; __device__ __forceinline__ void p0_prologue(const Args& a, const Frame& F) {
;     ...
;         for (int kk = 0; kk < 128; kk += 8) {
;             float wv[8];
; #pragma unroll
;             for (int u = 0; u < 8; ++u) wv[u] = W[(size_t)(k0 + kk + u) * 6144];
; #pragma unroll
;             for (int q = 0; q < 9; ++q) { const f32x4 s0 = *(const LAS f32x4*)(sc + q * 1024 + k0 + kk), s1 = *(const LAS f32x4*)(sc + q * 1024 + k0 + kk + 4);
;                 acc[q] += (s0.x * wv[0] + s0.y * wv[1]) + (s0.z * wv[2] + s0.w * wv[3]) + (s1.x * wv[4] + s1.y * wv[5]) + (s1.z * wv[6] + s1.w * wv[7]); }
;         }
	v_add_co_u32_e32 v94, vcc, 0x6000, v8
	v_mov_b32_e32 v7, s15
	s_nop 0
	v_addc_co_u32_e32 v95, vcc, 0, v9, vcc
	v_add_co_u32_e32 v98, vcc, 0xc000, v8
	v_mov_b32_e32 v96, v216
	s_nop 0
	v_addc_co_u32_e32 v99, vcc, 0, v9, vcc
	v_add_co_u32_e32 v100, vcc, 0x12000, v8
	ds_read_b128 v[22:25], v7
	ds_read_b128 v[26:29], v7 offset:16
	ds_read_b128 v[30:33], v7 offset:4096
	ds_read_b128 v[34:37], v7 offset:4112
	ds_read_b128 v[38:41], v7 offset:8192
	ds_read_b128 v[42:45], v7 offset:8208
	ds_read_b128 v[46:49], v7 offset:12288
	ds_read_b128 v[50:53], v7 offset:12304
	ds_read_b128 v[54:57], v7 offset:16384
	ds_read_b128 v[58:61], v7 offset:16400
	ds_read_b128 v[62:65], v7 offset:20480
	ds_read_b128 v[66:69], v7 offset:20496
	ds_read_b128 v[70:73], v7 offset:24576
	ds_read_b128 v[74:77], v7 offset:24592
	ds_read_b128 v[78:81], v7 offset:28672
	ds_read_b128 v[82:85], v7 offset:28688
	v_addc_co_u32_e32 v101, vcc, 0, v9, vcc
	v_add_co_u32_e32 v102, vcc, 0x18000, v8
	ds_read_b128 v[86:89], v7 offset:32768
	ds_read_b128 v[90:93], v7 offset:32784
	v_addc_co_u32_e32 v103, vcc, 0, v9, vcc
	v_mov_b32_e32 v94, v217
	v_add_co_u32_e32 v104, vcc, 0x1e000, v8
	v_mov_b32_e32 v98, v218
	s_nop 0
	v_mov_b32_e32 v100, v219
	v_addc_co_u32_e32 v105, vcc, 0, v9, vcc
	v_add_co_u32_e32 v106, vcc, 0x24000, v8
	v_mov_b32_e32 v102, v220
	s_waitcnt lgkmcnt(14)
	v_mov_b32_e32 v108, v22
	v_mov_b32_e32 v22, v24
	v_mov_b32_e32 v24, v26
	v_mov_b32_e32 v26, v28
	s_waitcnt lgkmcnt(13)
	v_mov_b32_e32 v28, v38
	v_mov_b32_e32 v38, v40
	s_waitcnt lgkmcnt(12)
	v_mov_b32_e32 v40, v42
	v_mov_b32_e32 v42, v44
	s_waitcnt lgkmcnt(9)
	v_mov_b32_e32 v44, v54
	v_mov_b32_e32 v54, v56
	v_mov_b32_e32 v56, v221
	v_addc_co_u32_e32 v107, vcc, 0, v9, vcc
	v_add_co_u32_e32 v104, vcc, 0x2a000, v8
	v_mov_b32_e32 v109, v30
	s_nop 0
	v_addc_co_u32_e32 v105, vcc, 0, v9, vcc
	v_mov_b32_e32 v106, v222
	s_nop 0
	v_mov_b32_e32 v104, v223
	v_mov_b32_e32 v30, v23
	v_mov_b32_e32 v23, v32
	v_mov_b32_e32 v32, v25
	v_mov_b32_e32 v25, v34
	v_mov_b32_e32 v34, v27
	v_mov_b32_e32 v27, v36
	v_mov_b32_e32 v36, v29
	v_mov_b32_e32 v29, v46
	v_mov_b32_e32 v46, v39
	s_waitcnt lgkmcnt(6)
	v_mov_b32_e32 v111, v66
	v_mov_b32_e32 v66, v59
	v_mov_b32_e32 v59, v68
	v_mov_b32_e32 v68, v61
	s_waitcnt lgkmcnt(3)
	v_mov_b32_e32 v61, v78
	v_mov_b32_e32 v78, v71
	v_mov_b32_e32 v39, v48
	v_mov_b32_e32 v48, v41
	v_mov_b32_e32 v41, v50
	v_mov_b32_e32 v50, v43
	v_mov_b32_e32 v43, v52
	v_mov_b32_e32 v52, v45
	v_mov_b32_e32 v45, v62
	v_mov_b32_e32 v62, v55
	v_mov_b32_e32 v55, v64
	v_mov_b32_e32 v64, v57
	v_mov_b32_e32 v110, v58
	v_mov_b32_e32 v58, v60
	v_mov_b32_e32 v60, v70
	v_mov_b32_e32 v71, v80
	v_mov_b32_e32 v80, v73
	v_mov_b32_e32 v70, v72
	v_mov_b32_e32 v72, v74
	s_waitcnt lgkmcnt(2)
	v_mov_b32_e32 v73, v82
	v_mov_b32_e32 v82, v75
	v_mov_b32_e32 v74, v76
	v_mov_b32_e32 v75, v84
	v_mov_b32_e32 v84, v77
	s_waitcnt lgkmcnt(1)
	v_mov_b32_e32 v76, v87
	v_mov_b32_e32 v87, v89
	v_mov_b32_e32 v77, v88
	s_waitcnt lgkmcnt(0)
	v_mov_b32_e32 v89, v90
	v_mov_b32_e32 v90, v93
	v_mov_b32_e32 v88, v92
	s_add_i32 s14, s14, 8
	s_add_i32 s15, s15, 32
	s_cmpk_gt_u32 s14, 0x77
	v_lshl_add_u64 v[8:9], v[8:9], 0, s[12:13]
	v_pk_mul_f32 v[46:47], v[94:95], v[46:47] op_sel_hi:[0,1]
	v_pk_mul_f32 v[78:79], v[94:95], v[78:79] op_sel_hi:[0,1]
	v_pk_mul_f32 v[30:31], v[94:95], v[30:31] op_sel_hi:[0,1]
	v_pk_mul_f32 v[62:63], v[94:95], v[62:63] op_sel_hi:[0,1]
	v_pk_fma_f32 v[28:29], v[96:97], v[28:29], v[46:47] op_sel_hi:[0,1,1]
	v_pk_fma_f32 v[46:47], v[96:97], v[60:61], v[78:79] op_sel_hi:[0,1,1]
	v_pk_mul_f32 v[32:33], v[100:101], v[32:33] op_sel_hi:[0,1]
	v_pk_mul_f32 v[48:49], v[100:101], v[48:49] op_sel_hi:[0,1]
	v_pk_mul_f32 v[60:61], v[100:101], v[64:65] op_sel_hi:[0,1]
	v_pk_fma_f32 v[30:31], v[96:97], v[108:109], v[30:31] op_sel_hi:[0,1,1]
	v_pk_fma_f32 v[44:45], v[96:97], v[44:45], v[62:63] op_sel_hi:[0,1,1]
	v_pk_fma_f32 v[22:23], v[98:99], v[22:23], v[32:33] op_sel_hi:[0,1,1]
	v_pk_fma_f32 v[32:33], v[98:99], v[38:39], v[48:49] op_sel_hi:[0,1,1]
	v_pk_fma_f32 v[38:39], v[98:99], v[54:55], v[60:61] op_sel_hi:[0,1,1]
	v_pk_add_f32 v[22:23], v[30:31], v[22:23]
	v_pk_add_f32 v[30:31], v[44:45], v[38:39]
	v_pk_mul_f32 v[62:63], v[100:101], v[80:81] op_sel_hi:[0,1]
	v_mov_b32_e32 v97, v100
	v_pk_add_f32 v[28:29], v[28:29], v[32:33]
	v_pk_mul_f32 v[34:35], v[56:57], v[34:35] op_sel_hi:[0,1]
	v_pk_mul_f32 v[38:39], v[56:57], v[50:51] op_sel_hi:[0,1]
	v_pk_mul_f32 v[44:45], v[56:57], v[66:67] op_sel_hi:[0,1]
	v_pk_fma_f32 v[24:25], v[102:103], v[24:25], v[34:35] op_sel_hi:[0,1,1]
	v_pk_fma_f32 v[34:35], v[102:103], v[40:41], v[38:39] op_sel_hi:[0,1,1]
	v_pk_fma_f32 v[38:39], v[102:103], v[110:111], v[44:45] op_sel_hi:[0,1,1]
	v_mov_b32_e32 v95, v98
	v_pk_mul_f32 v[64:65], v[96:97], v[86:87]
	v_pk_fma_f32 v[48:49], v[98:99], v[70:71], v[62:63] op_sel_hi:[0,1,1]
	v_pk_add_f32 v[22:23], v[22:23], v[24:25]
	v_pk_mul_f32 v[24:25], v[104:105], v[36:37] op_sel_hi:[0,1]
	v_pk_add_f32 v[28:29], v[28:29], v[34:35]
	v_pk_mul_f32 v[34:35], v[104:105], v[52:53] op_sel_hi:[0,1]
	v_pk_add_f32 v[30:31], v[30:31], v[38:39]
	v_pk_mul_f32 v[36:37], v[104:105], v[68:69] op_sel_hi:[0,1]
	v_pk_mul_f32 v[38:39], v[104:105], v[84:85] op_sel_hi:[0,1]
	v_mov_b32_e32 v105, v56
	v_pk_fma_f32 v[54:55], v[94:95], v[76:77], v[64:65]
	v_pk_add_f32 v[32:33], v[46:47], v[48:49]
	v_pk_mul_f32 v[46:47], v[56:57], v[82:83] op_sel_hi:[0,1]
	v_pk_fma_f32 v[24:25], v[106:107], v[26:27], v[24:25] op_sel_hi:[0,1,1]
	v_pk_fma_f32 v[26:27], v[106:107], v[42:43], v[34:35] op_sel_hi:[0,1,1]
	v_pk_fma_f32 v[34:35], v[106:107], v[58:59], v[36:37] op_sel_hi:[0,1,1]
	v_pk_fma_f32 v[36:37], v[106:107], v[74:75], v[38:39] op_sel_hi:[0,1,1]
	v_mov_b32_e32 v107, v102
	v_pk_mul_f32 v[38:39], v[104:105], v[90:91]
	v_pk_fma_f32 v[40:41], v[102:103], v[72:73], v[46:47] op_sel_hi:[0,1,1]
	v_add_f32_e32 v7, v54, v55
	v_pk_add_f32 v[22:23], v[24:25], v[22:23]
	v_pk_add_f32 v[24:25], v[26:27], v[28:29]
	v_pk_add_f32 v[26:27], v[34:35], v[30:31]
	v_pk_fma_f32 v[30:31], v[106:107], v[88:89], v[38:39]
	v_pk_add_f32 v[32:33], v[32:33], v[40:41]
	v_add_f32_e32 v7, v7, v31
	v_pk_add_f32 v[28:29], v[36:37], v[32:33]
	v_add_f32_e32 v7, v30, v7
	v_pk_add_f32 v[10:11], v[10:11], v[22:23]
	v_pk_add_f32 v[12:13], v[12:13], v[24:25]
	v_pk_add_f32 v[14:15], v[14:15], v[26:27]
	v_pk_add_f32 v[16:17], v[16:17], v[28:29]
	v_add_f32_e32 v2, v2, v7
	s_waitcnt vmcnt(16)
; #define LAS __attribute__((address_space(3)))
; __device__ __forceinline__ void p0_prologue(const Args& a, const Frame& F) {
;     ...
;         for (int kk = 0; kk < 128; kk += 8) {
;             float wv[8];
; #pragma unroll
;             for (int u = 0; u < 8; ++u) wv[u] = W[(size_t)(k0 + kk + u) * 6144];
; #pragma unroll
;             for (int q = 0; q < 9; ++q) { const f32x4 s0 = *(const LAS f32x4*)(sc + q * 1024 + k0 + kk), s1 = *(const LAS f32x4*)(sc + q * 1024 + k0 + kk + 4);
;                 acc[q] += (s0.x * wv[0] + s0.y * wv[1]) + (s0.z * wv[2] + s0.w * wv[3]) + (s1.x * wv[4] + s1.y * wv[5]) + (s1.z * wv[6] + s1.w * wv[7]); }
;         }
	v_add_co_u32_e32 v94, vcc, 0x6000, v8
	v_mov_b32_e32 v7, s15
	s_nop 0
	v_addc_co_u32_e32 v95, vcc, 0, v9, vcc
	v_add_co_u32_e32 v98, vcc, 0xc000, v8
	v_mov_b32_e32 v96, v224
	s_nop 0
	v_addc_co_u32_e32 v99, vcc, 0, v9, vcc
	v_add_co_u32_e32 v100, vcc, 0x12000, v8
	ds_read_b128 v[22:25], v7
	ds_read_b128 v[26:29], v7 offset:16
	ds_read_b128 v[30:33], v7 offset:4096
	ds_read_b128 v[34:37], v7 offset:4112
	ds_read_b128 v[38:41], v7 offset:8192
	ds_read_b128 v[42:45], v7 offset:8208
	ds_read_b128 v[46:49], v7 offset:12288
	ds_read_b128 v[50:53], v7 offset:12304
	ds_read_b128 v[54:57], v7 offset:16384
	ds_read_b128 v[58:61], v7 offset:16400
	ds_read_b128 v[62:65], v7 offset:20480
	ds_read_b128 v[66:69], v7 offset:20496
	ds_read_b128 v[70:73], v7 offset:24576
	ds_read_b128 v[74:77], v7 offset:24592
	ds_read_b128 v[78:81], v7 offset:28672
	ds_read_b128 v[82:85], v7 offset:28688
	v_addc_co_u32_e32 v101, vcc, 0, v9, vcc
	v_add_co_u32_e32 v102, vcc, 0x18000, v8
	ds_read_b128 v[86:89], v7 offset:32768
	ds_read_b128 v[90:93], v7 offset:32784
	v_addc_co_u32_e32 v103, vcc, 0, v9, vcc
	v_mov_b32_e32 v94, v225
	v_add_co_u32_e32 v104, vcc, 0x1e000, v8
	v_mov_b32_e32 v98, v226
	s_nop 0
	v_mov_b32_e32 v100, v227
	v_addc_co_u32_e32 v105, vcc, 0, v9, vcc
	v_add_co_u32_e32 v106, vcc, 0x24000, v8
	v_mov_b32_e32 v102, v228
	s_waitcnt lgkmcnt(14)
	v_mov_b32_e32 v108, v22
	v_mov_b32_e32 v22, v24
	v_mov_b32_e32 v24, v26
	v_mov_b32_e32 v26, v28
	s_waitcnt lgkmcnt(13)
	v_mov_b32_e32 v28, v38
	v_mov_b32_e32 v38, v40
	s_waitcnt lgkmcnt(12)
	v_mov_b32_e32 v40, v42
	v_mov_b32_e32 v42, v44
	s_waitcnt lgkmcnt(9)
	v_mov_b32_e32 v44, v54
	v_mov_b32_e32 v54, v56
	v_mov_b32_e32 v56, v229
	v_addc_co_u32_e32 v107, vcc, 0, v9, vcc
	v_add_co_u32_e32 v104, vcc, 0x2a000, v8
	v_mov_b32_e32 v109, v30
	s_nop 0
	v_addc_co_u32_e32 v105, vcc, 0, v9, vcc
	v_mov_b32_e32 v106, v230
	s_nop 0
	v_mov_b32_e32 v104, v231
	v_mov_b32_e32 v30, v23
	v_mov_b32_e32 v23, v32
	v_mov_b32_e32 v32, v25
	v_mov_b32_e32 v25, v34
	v_mov_b32_e32 v34, v27
	v_mov_b32_e32 v27, v36
	v_mov_b32_e32 v36, v29
	v_mov_b32_e32 v29, v46
	v_mov_b32_e32 v46, v39
	s_waitcnt lgkmcnt(6)
	v_mov_b32_e32 v111, v66
	v_mov_b32_e32 v66, v59
	v_mov_b32_e32 v59, v68
	v_mov_b32_e32 v68, v61
	s_waitcnt lgkmcnt(3)
	v_mov_b32_e32 v61, v78
	v_mov_b32_e32 v78, v71
	v_mov_b32_e32 v39, v48
	v_mov_b32_e32 v48, v41
	v_mov_b32_e32 v41, v50
	v_mov_b32_e32 v50, v43
	v_mov_b32_e32 v43, v52
	v_mov_b32_e32 v52, v45
	v_mov_b32_e32 v45, v62
	v_mov_b32_e32 v62, v55
	v_mov_b32_e32 v55, v64
	v_mov_b32_e32 v64, v57
	v_mov_b32_e32 v110, v58
	v_mov_b32_e32 v58, v60
	v_mov_b32_e32 v60, v70
	v_mov_b32_e32 v71, v80
	v_mov_b32_e32 v80, v73
	v_mov_b32_e32 v70, v72
	v_mov_b32_e32 v72, v74
	s_waitcnt lgkmcnt(2)
	v_mov_b32_e32 v73, v82
	v_mov_b32_e32 v82, v75
	v_mov_b32_e32 v74, v76
	v_mov_b32_e32 v75, v84
	v_mov_b32_e32 v84, v77
	s_waitcnt lgkmcnt(1)
	v_mov_b32_e32 v76, v87
	v_mov_b32_e32 v87, v89
	v_mov_b32_e32 v77, v88
	s_waitcnt lgkmcnt(0)
	v_mov_b32_e32 v89, v90
	v_mov_b32_e32 v90, v93
	v_mov_b32_e32 v88, v92
	s_add_i32 s14, s14, 8
	s_add_i32 s15, s15, 32
	s_cmpk_gt_u32 s14, 0x77
	v_lshl_add_u64 v[8:9], v[8:9], 0, s[12:13]
	v_pk_mul_f32 v[46:47], v[94:95], v[46:47] op_sel_hi:[0,1]
	v_pk_mul_f32 v[78:79], v[94:95], v[78:79] op_sel_hi:[0,1]
	v_pk_mul_f32 v[30:31], v[94:95], v[30:31] op_sel_hi:[0,1]
	v_pk_mul_f32 v[62:63], v[94:95], v[62:63] op_sel_hi:[0,1]
	v_pk_fma_f32 v[28:29], v[96:97], v[28:29], v[46:47] op_sel_hi:[0,1,1]
	v_pk_fma_f32 v[46:47], v[96:97], v[60:61], v[78:79] op_sel_hi:[0,1,1]
	v_pk_mul_f32 v[32:33], v[100:101], v[32:33] op_sel_hi:[0,1]
	v_pk_mul_f32 v[48:49], v[100:101], v[48:49] op_sel_hi:[0,1]
	v_pk_mul_f32 v[60:61], v[100:101], v[64:65] op_sel_hi:[0,1]
	v_pk_fma_f32 v[30:31], v[96:97], v[108:109], v[30:31] op_sel_hi:[0,1,1]
	v_pk_fma_f32 v[44:45], v[96:97], v[44:45], v[62:63] op_sel_hi:[0,1,1]
	v_pk_fma_f32 v[22:23], v[98:99], v[22:23], v[32:33] op_sel_hi:[0,1,1]
	v_pk_fma_f32 v[32:33], v[98:99], v[38:39], v[48:49] op_sel_hi:[0,1,1]
	v_pk_fma_f32 v[38:39], v[98:99], v[54:55], v[60:61] op_sel_hi:[0,1,1]
	v_pk_add_f32 v[22:23], v[30:31], v[22:23]
	v_pk_add_f32 v[30:31], v[44:45], v[38:39]
	v_pk_mul_f32 v[62:63], v[100:101], v[80:81] op_sel_hi:[0,1]
	v_mov_b32_e32 v97, v100
	v_pk_add_f32 v[28:29], v[28:29], v[32:33]
	v_pk_mul_f32 v[34:35], v[56:57], v[34:35] op_sel_hi:[0,1]
	v_pk_mul_f32 v[38:39], v[56:57], v[50:51] op_sel_hi:[0,1]
	v_pk_mul_f32 v[44:45], v[56:57], v[66:67] op_sel_hi:[0,1]
	v_pk_fma_f32 v[24:25], v[102:103], v[24:25], v[34:35] op_sel_hi:[0,1,1]
	v_pk_fma_f32 v[34:35], v[102:103], v[40:41], v[38:39] op_sel_hi:[0,1,1]
	v_pk_fma_f32 v[38:39], v[102:103], v[110:111], v[44:45] op_sel_hi:[0,1,1]
	v_mov_b32_e32 v95, v98
	v_pk_mul_f32 v[64:65], v[96:97], v[86:87]
	v_pk_fma_f32 v[48:49], v[98:99], v[70:71], v[62:63] op_sel_hi:[0,1,1]
	v_pk_add_f32 v[22:23], v[22:23], v[24:25]
	v_pk_mul_f32 v[24:25], v[104:105], v[36:37] op_sel_hi:[0,1]
	v_pk_add_f32 v[28:29], v[28:29], v[34:35]
	v_pk_mul_f32 v[34:35], v[104:105], v[52:53] op_sel_hi:[0,1]
	v_pk_add_f32 v[30:31], v[30:31], v[38:39]
	v_pk_mul_f32 v[36:37], v[104:105], v[68:69] op_sel_hi:[0,1]
	v_pk_mul_f32 v[38:39], v[104:105], v[84:85] op_sel_hi:[0,1]
	v_mov_b32_e32 v105, v56
	v_pk_fma_f32 v[54:55], v[94:95], v[76:77], v[64:65]
	v_pk_add_f32 v[32:33], v[46:47], v[48:49]
	v_pk_mul_f32 v[46:47], v[56:57], v[82:83] op_sel_hi:[0,1]
	v_pk_fma_f32 v[24:25], v[106:107], v[26:27], v[24:25] op_sel_hi:[0,1,1]
	v_pk_fma_f32 v[26:27], v[106:107], v[42:43], v[34:35] op_sel_hi:[0,1,1]
	v_pk_fma_f32 v[34:35], v[106:107], v[58:59], v[36:37] op_sel_hi:[0,1,1]
	v_pk_fma_f32 v[36:37], v[106:107], v[74:75], v[38:39] op_sel_hi:[0,1,1]
	v_mov_b32_e32 v107, v102
	v_pk_mul_f32 v[38:39], v[104:105], v[90:91]
	v_pk_fma_f32 v[40:41], v[102:103], v[72:73], v[46:47] op_sel_hi:[0,1,1]
	v_add_f32_e32 v7, v54, v55
	v_pk_add_f32 v[22:23], v[24:25], v[22:23]
	v_pk_add_f32 v[24:25], v[26:27], v[28:29]
	v_pk_add_f32 v[26:27], v[34:35], v[30:31]
	v_pk_fma_f32 v[30:31], v[106:107], v[88:89], v[38:39]
	v_pk_add_f32 v[32:33], v[32:33], v[40:41]
	v_add_f32_e32 v7, v7, v31
	v_pk_add_f32 v[28:29], v[36:37], v[32:33]
	v_add_f32_e32 v7, v30, v7
	v_pk_add_f32 v[10:11], v[10:11], v[22:23]
	v_pk_add_f32 v[12:13], v[12:13], v[24:25]
	v_pk_add_f32 v[14:15], v[14:15], v[26:27]
	v_pk_add_f32 v[16:17], v[16:17], v[28:29]
	v_add_f32_e32 v2, v2, v7
	s_waitcnt vmcnt(8)
; #define LAS __attribute__((address_space(3)))
; __device__ __forceinline__ void p0_prologue(const Args& a, const Frame& F) {
;     ...
;         for (int kk = 0; kk < 128; kk += 8) {
;             float wv[8];
; #pragma unroll
;             for (int u = 0; u < 8; ++u) wv[u] = W[(size_t)(k0 + kk + u) * 6144];
; #pragma unroll
;             for (int q = 0; q < 9; ++q) { const f32x4 s0 = *(const LAS f32x4*)(sc + q * 1024 + k0 + kk), s1 = *(const LAS f32x4*)(sc + q * 1024 + k0 + kk + 4);
;                 acc[q] += (s0.x * wv[0] + s0.y * wv[1]) + (s0.z * wv[2] + s0.w * wv[3]) + (s1.x * wv[4] + s1.y * wv[5]) + (s1.z * wv[6] + s1.w * wv[7]); }
;         }
	v_add_co_u32_e32 v94, vcc, 0x6000, v8
	v_mov_b32_e32 v7, s15
	s_nop 0
	v_addc_co_u32_e32 v95, vcc, 0, v9, vcc
	v_add_co_u32_e32 v98, vcc, 0xc000, v8
	v_mov_b32_e32 v96, v232
	s_nop 0
	v_addc_co_u32_e32 v99, vcc, 0, v9, vcc
	v_add_co_u32_e32 v100, vcc, 0x12000, v8
	ds_read_b128 v[22:25], v7
	ds_read_b128 v[26:29], v7 offset:16
	ds_read_b128 v[30:33], v7 offset:4096
	ds_read_b128 v[34:37], v7 offset:4112
	ds_read_b128 v[38:41], v7 offset:8192
	ds_read_b128 v[42:45], v7 offset:8208
	ds_read_b128 v[46:49], v7 offset:12288
	ds_read_b128 v[50:53], v7 offset:12304
	ds_read_b128 v[54:57], v7 offset:16384
	ds_read_b128 v[58:61], v7 offset:16400
	ds_read_b128 v[62:65], v7 offset:20480
	ds_read_b128 v[66:69], v7 offset:20496
	ds_read_b128 v[70:73], v7 offset:24576
	ds_read_b128 v[74:77], v7 offset:24592
	ds_read_b128 v[78:81], v7 offset:28672
	ds_read_b128 v[82:85], v7 offset:28688
	v_addc_co_u32_e32 v101, vcc, 0, v9, vcc
	v_add_co_u32_e32 v102, vcc, 0x18000, v8
	ds_read_b128 v[86:89], v7 offset:32768
	ds_read_b128 v[90:93], v7 offset:32784
	v_addc_co_u32_e32 v103, vcc, 0, v9, vcc
	v_mov_b32_e32 v94, v233
	v_add_co_u32_e32 v104, vcc, 0x1e000, v8
	v_mov_b32_e32 v98, v234
	s_nop 0
	v_mov_b32_e32 v100, v235
	v_addc_co_u32_e32 v105, vcc, 0, v9, vcc
	v_add_co_u32_e32 v106, vcc, 0x24000, v8
	v_mov_b32_e32 v102, v236
	s_waitcnt lgkmcnt(14)
	v_mov_b32_e32 v108, v22
	v_mov_b32_e32 v22, v24
	v_mov_b32_e32 v24, v26
	v_mov_b32_e32 v26, v28
	s_waitcnt lgkmcnt(13)
	v_mov_b32_e32 v28, v38
	v_mov_b32_e32 v38, v40
	s_waitcnt lgkmcnt(12)
	v_mov_b32_e32 v40, v42
	v_mov_b32_e32 v42, v44
	s_waitcnt lgkmcnt(9)
	v_mov_b32_e32 v44, v54
	v_mov_b32_e32 v54, v56
	v_mov_b32_e32 v56, v237
	v_addc_co_u32_e32 v107, vcc, 0, v9, vcc
	v_add_co_u32_e32 v104, vcc, 0x2a000, v8
	v_mov_b32_e32 v109, v30
	s_nop 0
	v_addc_co_u32_e32 v105, vcc, 0, v9, vcc
	v_mov_b32_e32 v106, v238
	s_nop 0
	v_mov_b32_e32 v104, v239
	v_mov_b32_e32 v30, v23
	v_mov_b32_e32 v23, v32
	v_mov_b32_e32 v32, v25
	v_mov_b32_e32 v25, v34
	v_mov_b32_e32 v34, v27
	v_mov_b32_e32 v27, v36
	v_mov_b32_e32 v36, v29
	v_mov_b32_e32 v29, v46
	v_mov_b32_e32 v46, v39
	s_waitcnt lgkmcnt(6)
	v_mov_b32_e32 v111, v66
	v_mov_b32_e32 v66, v59
	v_mov_b32_e32 v59, v68
	v_mov_b32_e32 v68, v61
	s_waitcnt lgkmcnt(3)
	v_mov_b32_e32 v61, v78
	v_mov_b32_e32 v78, v71
	v_mov_b32_e32 v39, v48
	v_mov_b32_e32 v48, v41
	v_mov_b32_e32 v41, v50
	v_mov_b32_e32 v50, v43
	v_mov_b32_e32 v43, v52
	v_mov_b32_e32 v52, v45
	v_mov_b32_e32 v45, v62
	v_mov_b32_e32 v62, v55
	v_mov_b32_e32 v55, v64
	v_mov_b32_e32 v64, v57
	v_mov_b32_e32 v110, v58
	v_mov_b32_e32 v58, v60
	v_mov_b32_e32 v60, v70
	v_mov_b32_e32 v71, v80
	v_mov_b32_e32 v80, v73
	v_mov_b32_e32 v70, v72
	v_mov_b32_e32 v72, v74
	s_waitcnt lgkmcnt(2)
	v_mov_b32_e32 v73, v82
	v_mov_b32_e32 v82, v75
	v_mov_b32_e32 v74, v76
	v_mov_b32_e32 v75, v84
	v_mov_b32_e32 v84, v77
	s_waitcnt lgkmcnt(1)
	v_mov_b32_e32 v76, v87
	v_mov_b32_e32 v87, v89
	v_mov_b32_e32 v77, v88
	s_waitcnt lgkmcnt(0)
	v_mov_b32_e32 v89, v90
	v_mov_b32_e32 v90, v93
	v_mov_b32_e32 v88, v92
	s_add_i32 s14, s14, 8
	s_add_i32 s15, s15, 32
	s_cmpk_gt_u32 s14, 0x77
	v_lshl_add_u64 v[8:9], v[8:9], 0, s[12:13]
	v_pk_mul_f32 v[46:47], v[94:95], v[46:47] op_sel_hi:[0,1]
	v_pk_mul_f32 v[78:79], v[94:95], v[78:79] op_sel_hi:[0,1]
	v_pk_mul_f32 v[30:31], v[94:95], v[30:31] op_sel_hi:[0,1]
	v_pk_mul_f32 v[62:63], v[94:95], v[62:63] op_sel_hi:[0,1]
	v_pk_fma_f32 v[28:29], v[96:97], v[28:29], v[46:47] op_sel_hi:[0,1,1]
	v_pk_fma_f32 v[46:47], v[96:97], v[60:61], v[78:79] op_sel_hi:[0,1,1]
	v_pk_mul_f32 v[32:33], v[100:101], v[32:33] op_sel_hi:[0,1]
	v_pk_mul_f32 v[48:49], v[100:101], v[48:49] op_sel_hi:[0,1]
	v_pk_mul_f32 v[60:61], v[100:101], v[64:65] op_sel_hi:[0,1]
	v_pk_fma_f32 v[30:31], v[96:97], v[108:109], v[30:31] op_sel_hi:[0,1,1]
	v_pk_fma_f32 v[44:45], v[96:97], v[44:45], v[62:63] op_sel_hi:[0,1,1]
	v_pk_fma_f32 v[22:23], v[98:99], v[22:23], v[32:33] op_sel_hi:[0,1,1]
	v_pk_fma_f32 v[32:33], v[98:99], v[38:39], v[48:49] op_sel_hi:[0,1,1]
	v_pk_fma_f32 v[38:39], v[98:99], v[54:55], v[60:61] op_sel_hi:[0,1,1]
	v_pk_add_f32 v[22:23], v[30:31], v[22:23]
	v_pk_add_f32 v[30:31], v[44:45], v[38:39]
	v_pk_mul_f32 v[62:63], v[100:101], v[80:81] op_sel_hi:[0,1]
	v_mov_b32_e32 v97, v100
	v_pk_add_f32 v[28:29], v[28:29], v[32:33]
	v_pk_mul_f32 v[34:35], v[56:57], v[34:35] op_sel_hi:[0,1]
	v_pk_mul_f32 v[38:39], v[56:57], v[50:51] op_sel_hi:[0,1]
	v_pk_mul_f32 v[44:45], v[56:57], v[66:67] op_sel_hi:[0,1]
	v_pk_fma_f32 v[24:25], v[102:103], v[24:25], v[34:35] op_sel_hi:[0,1,1]
	v_pk_fma_f32 v[34:35], v[102:103], v[40:41], v[38:39] op_sel_hi:[0,1,1]
	v_pk_fma_f32 v[38:39], v[102:103], v[110:111], v[44:45] op_sel_hi:[0,1,1]
	v_mov_b32_e32 v95, v98
	v_pk_mul_f32 v[64:65], v[96:97], v[86:87]
	v_pk_fma_f32 v[48:49], v[98:99], v[70:71], v[62:63] op_sel_hi:[0,1,1]
	v_pk_add_f32 v[22:23], v[22:23], v[24:25]
	v_pk_mul_f32 v[24:25], v[104:105], v[36:37] op_sel_hi:[0,1]
	v_pk_add_f32 v[28:29], v[28:29], v[34:35]
	v_pk_mul_f32 v[34:35], v[104:105], v[52:53] op_sel_hi:[0,1]
	v_pk_add_f32 v[30:31], v[30:31], v[38:39]
	v_pk_mul_f32 v[36:37], v[104:105], v[68:69] op_sel_hi:[0,1]
	v_pk_mul_f32 v[38:39], v[104:105], v[84:85] op_sel_hi:[0,1]
	v_mov_b32_e32 v105, v56
	v_pk_fma_f32 v[54:55], v[94:95], v[76:77], v[64:65]
	v_pk_add_f32 v[32:33], v[46:47], v[48:49]
	v_pk_mul_f32 v[46:47], v[56:57], v[82:83] op_sel_hi:[0,1]
	v_pk_fma_f32 v[24:25], v[106:107], v[26:27], v[24:25] op_sel_hi:[0,1,1]
	v_pk_fma_f32 v[26:27], v[106:107], v[42:43], v[34:35] op_sel_hi:[0,1,1]
	v_pk_fma_f32 v[34:35], v[106:107], v[58:59], v[36:37] op_sel_hi:[0,1,1]
	v_pk_fma_f32 v[36:37], v[106:107], v[74:75], v[38:39] op_sel_hi:[0,1,1]
	v_mov_b32_e32 v107, v102
	v_pk_mul_f32 v[38:39], v[104:105], v[90:91]
	v_pk_fma_f32 v[40:41], v[102:103], v[72:73], v[46:47] op_sel_hi:[0,1,1]
	v_add_f32_e32 v7, v54, v55
	v_pk_add_f32 v[22:23], v[24:25], v[22:23]
	v_pk_add_f32 v[24:25], v[26:27], v[28:29]
	v_pk_add_f32 v[26:27], v[34:35], v[30:31]
	v_pk_fma_f32 v[30:31], v[106:107], v[88:89], v[38:39]
	v_pk_add_f32 v[32:33], v[32:33], v[40:41]
	v_add_f32_e32 v7, v7, v31
	v_pk_add_f32 v[28:29], v[36:37], v[32:33]
	v_add_f32_e32 v7, v30, v7
	v_pk_add_f32 v[10:11], v[10:11], v[22:23]
	v_pk_add_f32 v[12:13], v[12:13], v[24:25]
	v_pk_add_f32 v[14:15], v[14:15], v[26:27]
	v_pk_add_f32 v[16:17], v[16:17], v[28:29]
	v_add_f32_e32 v2, v2, v7
	s_waitcnt vmcnt(0)
; #define LAS __attribute__((address_space(3)))
; __device__ __forceinline__ void p0_prologue(const Args& a, const Frame& F) {
;     ...
;         for (int kk = 0; kk < 128; kk += 8) {
;             float wv[8];
; #pragma unroll
;             for (int u = 0; u < 8; ++u) wv[u] = W[(size_t)(k0 + kk + u) * 6144];
; #pragma unroll
;             for (int q = 0; q < 9; ++q) { const f32x4 s0 = *(const LAS f32x4*)(sc + q * 1024 + k0 + kk), s1 = *(const LAS f32x4*)(sc + q * 1024 + k0 + kk + 4);
;                 acc[q] += (s0.x * wv[0] + s0.y * wv[1]) + (s0.z * wv[2] + s0.w * wv[3]) + (s1.x * wv[4] + s1.y * wv[5]) + (s1.z * wv[6] + s1.w * wv[7]); }
;         }
; #pragma unroll
;         for (int q = 0; q < 9; ++q) red[(F.wave * 9 + q) * 64 + F.lane] = acc[q];
;         __syncthreads();
;         for (int i = F.tid; i < 9 * 64; i += 512) { const int q = i >> 6, l = i & 63; float s = 0.f;
; #pragma unroll
;             for (int w8 = 0; w8 < 8; ++w8) s += red[(w8 * 9 + q) * 64 + l];
;             ((float*)(ws + WS_MOD))[q * 6144 + 64 * item + l] = s + a.in[IN_BADA][64 * item + l]; }
	v_add_co_u32_e32 v94, vcc, 0x6000, v8
	v_mov_b32_e32 v7, s15
	s_nop 0
	v_addc_co_u32_e32 v95, vcc, 0, v9, vcc
	v_add_co_u32_e32 v98, vcc, 0xc000, v8
	v_mov_b32_e32 v96, v240
	s_nop 0
	v_addc_co_u32_e32 v99, vcc, 0, v9, vcc
	v_add_co_u32_e32 v100, vcc, 0x12000, v8
	ds_read_b128 v[22:25], v7
	ds_read_b128 v[26:29], v7 offset:16
	ds_read_b128 v[30:33], v7 offset:4096
	ds_read_b128 v[34:37], v7 offset:4112
	ds_read_b128 v[38:41], v7 offset:8192
	ds_read_b128 v[42:45], v7 offset:8208
	ds_read_b128 v[46:49], v7 offset:12288
	ds_read_b128 v[50:53], v7 offset:12304
	ds_read_b128 v[54:57], v7 offset:16384
	ds_read_b128 v[58:61], v7 offset:16400
	ds_read_b128 v[62:65], v7 offset:20480
	ds_read_b128 v[66:69], v7 offset:20496
	ds_read_b128 v[70:73], v7 offset:24576
	ds_read_b128 v[74:77], v7 offset:24592
	ds_read_b128 v[78:81], v7 offset:28672
	ds_read_b128 v[82:85], v7 offset:28688
	v_addc_co_u32_e32 v101, vcc, 0, v9, vcc
	v_add_co_u32_e32 v102, vcc, 0x18000, v8
	ds_read_b128 v[86:89], v7 offset:32768
	ds_read_b128 v[90:93], v7 offset:32784
	v_addc_co_u32_e32 v103, vcc, 0, v9, vcc
	v_mov_b32_e32 v94, v241
	v_add_co_u32_e32 v104, vcc, 0x1e000, v8
	v_mov_b32_e32 v98, v242
	s_nop 0
	v_mov_b32_e32 v100, v243
	v_addc_co_u32_e32 v105, vcc, 0, v9, vcc
	v_add_co_u32_e32 v106, vcc, 0x24000, v8
	v_mov_b32_e32 v102, v244
	s_waitcnt lgkmcnt(14)
	v_mov_b32_e32 v108, v22
	v_mov_b32_e32 v22, v24
	v_mov_b32_e32 v24, v26
	v_mov_b32_e32 v26, v28
	s_waitcnt lgkmcnt(13)
	v_mov_b32_e32 v28, v38
	v_mov_b32_e32 v38, v40
	s_waitcnt lgkmcnt(12)
	v_mov_b32_e32 v40, v42
	v_mov_b32_e32 v42, v44
	s_waitcnt lgkmcnt(9)
	v_mov_b32_e32 v44, v54
	v_mov_b32_e32 v54, v56
	v_mov_b32_e32 v56, v245
	v_addc_co_u32_e32 v107, vcc, 0, v9, vcc
	v_add_co_u32_e32 v104, vcc, 0x2a000, v8
	v_mov_b32_e32 v109, v30
	s_nop 0
	v_addc_co_u32_e32 v105, vcc, 0, v9, vcc
	v_mov_b32_e32 v106, v246
	s_nop 0
	v_mov_b32_e32 v104, v247
	v_mov_b32_e32 v30, v23
	v_mov_b32_e32 v23, v32
	v_mov_b32_e32 v32, v25
	v_mov_b32_e32 v25, v34
	v_mov_b32_e32 v34, v27
	v_mov_b32_e32 v27, v36
	v_mov_b32_e32 v36, v29
	v_mov_b32_e32 v29, v46
	v_mov_b32_e32 v46, v39
	s_waitcnt lgkmcnt(6)
	v_mov_b32_e32 v111, v66
	v_mov_b32_e32 v66, v59
	v_mov_b32_e32 v59, v68
	v_mov_b32_e32 v68, v61
	s_waitcnt lgkmcnt(3)
	v_mov_b32_e32 v61, v78
	v_mov_b32_e32 v78, v71
	v_mov_b32_e32 v39, v48
	v_mov_b32_e32 v48, v41
	v_mov_b32_e32 v41, v50
	v_mov_b32_e32 v50, v43
	v_mov_b32_e32 v43, v52
	v_mov_b32_e32 v52, v45
	v_mov_b32_e32 v45, v62
	v_mov_b32_e32 v62, v55
	v_mov_b32_e32 v55, v64
	v_mov_b32_e32 v64, v57
	v_mov_b32_e32 v110, v58
	v_mov_b32_e32 v58, v60
	v_mov_b32_e32 v60, v70
	v_mov_b32_e32 v71, v80
	v_mov_b32_e32 v80, v73
	v_mov_b32_e32 v70, v72
	v_mov_b32_e32 v72, v74
	s_waitcnt lgkmcnt(2)
	v_mov_b32_e32 v73, v82
	v_mov_b32_e32 v82, v75
	v_mov_b32_e32 v74, v76
	v_mov_b32_e32 v75, v84
	v_mov_b32_e32 v84, v77
	s_waitcnt lgkmcnt(1)
	v_mov_b32_e32 v76, v87
	v_mov_b32_e32 v87, v89
	v_mov_b32_e32 v77, v88
	s_waitcnt lgkmcnt(0)
	v_mov_b32_e32 v89, v90
	v_mov_b32_e32 v90, v93
	v_mov_b32_e32 v88, v92
	s_add_i32 s14, s14, 8
	s_add_i32 s15, s15, 32
	s_cmpk_gt_u32 s14, 0x77
	v_lshl_add_u64 v[8:9], v[8:9], 0, s[12:13]
	v_pk_mul_f32 v[46:47], v[94:95], v[46:47] op_sel_hi:[0,1]
	v_pk_mul_f32 v[78:79], v[94:95], v[78:79] op_sel_hi:[0,1]
	v_pk_mul_f32 v[30:31], v[94:95], v[30:31] op_sel_hi:[0,1]
	v_pk_mul_f32 v[62:63], v[94:95], v[62:63] op_sel_hi:[0,1]
	v_pk_fma_f32 v[28:29], v[96:97], v[28:29], v[46:47] op_sel_hi:[0,1,1]
	v_pk_fma_f32 v[46:47], v[96:97], v[60:61], v[78:79] op_sel_hi:[0,1,1]
	v_pk_mul_f32 v[32:33], v[100:101], v[32:33] op_sel_hi:[0,1]
	v_pk_mul_f32 v[48:49], v[100:101], v[48:49] op_sel_hi:[0,1]
	v_pk_mul_f32 v[60:61], v[100:101], v[64:65] op_sel_hi:[0,1]
	v_pk_fma_f32 v[30:31], v[96:97], v[108:109], v[30:31] op_sel_hi:[0,1,1]
	v_pk_fma_f32 v[44:45], v[96:97], v[44:45], v[62:63] op_sel_hi:[0,1,1]
	v_pk_fma_f32 v[22:23], v[98:99], v[22:23], v[32:33] op_sel_hi:[0,1,1]
	v_pk_fma_f32 v[32:33], v[98:99], v[38:39], v[48:49] op_sel_hi:[0,1,1]
	v_pk_fma_f32 v[38:39], v[98:99], v[54:55], v[60:61] op_sel_hi:[0,1,1]
	v_pk_add_f32 v[22:23], v[30:31], v[22:23]
	v_pk_add_f32 v[30:31], v[44:45], v[38:39]
	v_pk_mul_f32 v[62:63], v[100:101], v[80:81] op_sel_hi:[0,1]
	v_mov_b32_e32 v97, v100
	v_pk_add_f32 v[28:29], v[28:29], v[32:33]
	v_pk_mul_f32 v[34:35], v[56:57], v[34:35] op_sel_hi:[0,1]
	v_pk_mul_f32 v[38:39], v[56:57], v[50:51] op_sel_hi:[0,1]
	v_pk_mul_f32 v[44:45], v[56:57], v[66:67] op_sel_hi:[0,1]
	v_pk_fma_f32 v[24:25], v[102:103], v[24:25], v[34:35] op_sel_hi:[0,1,1]
	v_pk_fma_f32 v[34:35], v[102:103], v[40:41], v[38:39] op_sel_hi:[0,1,1]
	v_pk_fma_f32 v[38:39], v[102:103], v[110:111], v[44:45] op_sel_hi:[0,1,1]
	v_mov_b32_e32 v95, v98
	v_pk_mul_f32 v[64:65], v[96:97], v[86:87]
	v_pk_fma_f32 v[48:49], v[98:99], v[70:71], v[62:63] op_sel_hi:[0,1,1]
	v_pk_add_f32 v[22:23], v[22:23], v[24:25]
	v_pk_mul_f32 v[24:25], v[104:105], v[36:37] op_sel_hi:[0,1]
	v_pk_add_f32 v[28:29], v[28:29], v[34:35]
	v_pk_mul_f32 v[34:35], v[104:105], v[52:53] op_sel_hi:[0,1]
	v_pk_add_f32 v[30:31], v[30:31], v[38:39]
	v_pk_mul_f32 v[36:37], v[104:105], v[68:69] op_sel_hi:[0,1]
	v_pk_mul_f32 v[38:39], v[104:105], v[84:85] op_sel_hi:[0,1]
	v_mov_b32_e32 v105, v56
	v_pk_fma_f32 v[54:55], v[94:95], v[76:77], v[64:65]
	v_pk_add_f32 v[32:33], v[46:47], v[48:49]
	v_pk_mul_f32 v[46:47], v[56:57], v[82:83] op_sel_hi:[0,1]
	v_pk_fma_f32 v[24:25], v[106:107], v[26:27], v[24:25] op_sel_hi:[0,1,1]
	v_pk_fma_f32 v[26:27], v[106:107], v[42:43], v[34:35] op_sel_hi:[0,1,1]
	v_pk_fma_f32 v[34:35], v[106:107], v[58:59], v[36:37] op_sel_hi:[0,1,1]
	v_pk_fma_f32 v[36:37], v[106:107], v[74:75], v[38:39] op_sel_hi:[0,1,1]
	v_mov_b32_e32 v107, v102
	v_pk_mul_f32 v[38:39], v[104:105], v[90:91]
	v_pk_fma_f32 v[40:41], v[102:103], v[72:73], v[46:47] op_sel_hi:[0,1,1]
	v_add_f32_e32 v7, v54, v55
	v_pk_add_f32 v[22:23], v[24:25], v[22:23]
	v_pk_add_f32 v[24:25], v[26:27], v[28:29]
	v_pk_add_f32 v[26:27], v[34:35], v[30:31]
	v_pk_fma_f32 v[30:31], v[106:107], v[88:89], v[38:39]
	v_pk_add_f32 v[32:33], v[32:33], v[40:41]
	v_add_f32_e32 v7, v7, v31
	v_pk_add_f32 v[28:29], v[36:37], v[32:33]
	v_add_f32_e32 v7, v30, v7
	v_pk_add_f32 v[10:11], v[10:11], v[22:23]
	v_pk_add_f32 v[12:13], v[12:13], v[24:25]
	v_pk_add_f32 v[14:15], v[14:15], v[26:27]
	v_pk_add_f32 v[16:17], v[16:17], v[28:29]
	v_add_f32_e32 v2, v2, v7
	ds_write2st64_b32 v21, v10, v11 offset1:1
	ds_write2st64_b32 v21, v12, v13 offset0:2 offset1:3
	ds_write2st64_b32 v21, v14, v15 offset0:4 offset1:5
	ds_write2st64_b32 v21, v16, v17 offset0:6 offset1:7
	ds_write_b32 v21, v2 offset:2048
	s_waitcnt lgkmcnt(0)
	s_barrier
	s_and_saveexec_b64 s[14:15], s[0:1]
	s_cbranch_execz .LBB0_10
	v_lshl_or_b32 v8, s45, 6, v252
	v_ashrrev_i32_e32 v9, 31, v8
	v_lshl_add_u64 v[8:9], v[8:9], 2, s[46:47]
	s_mov_b64 s[38:39], 0
	v_mov_b32_e32 v2, v20
	v_mov_b32_e32 v10, v19
	v_mov_b32_e32 v7, v18

; __device__ __forceinline__ void p0_prologue(const Args& a, const Frame& F) {
;     ...
;         if (r < I_WPA) {
;             const int g = r >> 8, cb = (r >> 4) & 15, n = (r & 15) * 64 + F.lane, k0 = g * 128 + cb * 8;
;             const float* wp = a.in[IN_WPOOL] + (size_t)k0 * 128; const float* ps = a.in[IN_PSCALE] + g * 128; const float* wb = a.in[IN_WBP] + (size_t)(g * 128) * 1024 + n;
;             float acc[8];
; #pragma unroll
;             for (int cc = 0; cc < 8; ++cc) acc[cc] = 0.f;
; #pragma unroll 4
;             for (int d = 0; d < 128; ++d) { const float wbv = wb[(size_t)d * 1024] * ps[d];
; #pragma unroll
;                 for (int cc = 0; cc < 8; ++cc) acc[cc] += wp[cc * 128 + d] * wbv; }
.LBB0_107:
	s_andn2_b64 vcc, exec, s[0:1]
	s_cbranch_vccnz .LBB0_24
	s_lshl_b32 s0, s85, 2
	s_and_b32 s0, s0, 0xf00
	v_lshl_or_b32 v2, v252, 2, s0
	s_lshr_b32 s0, s77, 1
	s_and_b32 s46, s0, 0x78
	s_ashr_i32 s0, s77, 1
	s_and_b32 s0, s0, 0xffffff80
	s_ashr_i32 s1, s0, 31
	s_lshl_b64 s[4:5], s[0:1], 12
	s_lshl_b64 s[34:35], s[0:1], 2
	s_add_u32 s8, s60, s34
	s_addc_u32 s33, s61, s35
	s_add_u32 s4, s64, s4
	s_addc_u32 s5, s65, s5
	s_or_b32 s0, s0, s46
	s_ashr_i32 s1, s0, 31
	v_lshl_add_u64 v[12:13], s[4:5], 0, v[2:3]
	s_lshl_b64 s[4:5], s[0:1], 9
	s_add_u32 s34, s58, s4
	v_mov_b32_e32 v14, 0
	s_addc_u32 s35, s59, s5
	s_mov_b64 s[4:5], 0
	v_mov_b32_e32 v15, v14
	v_mov_b32_e32 v16, v14
	v_mov_b32_e32 v18, v14
	v_mov_b32_e32 v17, v14
	v_mov_b32_e32 v19, v14
	v_mov_b32_e32 v20, v14
	v_mov_b32_e32 v21, v14
	v_lshlrev_b32_e32 v118, 2, v252
	s_mov_b32 s46, s8
	s_mov_b32 s47, s33
	s_nop 0
	global_load_dword v116, v118, s[46:47]
	global_load_dword v117, v118, s[46:47] offset:256
	global_load_dword v100, v118, s[34:35]
	global_load_dword v101, v118, s[34:35] offset:256
	global_load_dword v102, v118, s[34:35] offset:512
	global_load_dword v103, v118, s[34:35] offset:768
	global_load_dword v104, v118, s[34:35] offset:1024
	global_load_dword v105, v118, s[34:35] offset:1280
	global_load_dword v106, v118, s[34:35] offset:1536
	global_load_dword v107, v118, s[34:35] offset:1792
	global_load_dword v108, v118, s[34:35] offset:2048
	global_load_dword v109, v118, s[34:35] offset:2304
	global_load_dword v110, v118, s[34:35] offset:2560
	global_load_dword v111, v118, s[34:35] offset:2816
	global_load_dword v112, v118, s[34:35] offset:3072
	global_load_dword v113, v118, s[34:35] offset:3328
	global_load_dword v114, v118, s[34:35] offset:3584
	global_load_dword v115, v118, s[34:35] offset:3840
	s_mov_b64 s[46:47], 0x1000
	global_load_dword v120, v[12:13], off
	v_lshl_add_u64 v[12:13], v[12:13], 0, s[46:47]
	global_load_dword v121, v[12:13], off
	v_lshl_add_u64 v[12:13], v[12:13], 0, s[46:47]
	global_load_dword v122, v[12:13], off
	v_lshl_add_u64 v[12:13], v[12:13], 0, s[46:47]
	global_load_dword v123, v[12:13], off
	v_lshl_add_u64 v[12:13], v[12:13], 0, s[46:47]
	global_load_dword v124, v[12:13], off
	v_lshl_add_u64 v[12:13], v[12:13], 0, s[46:47]
	global_load_dword v125, v[12:13], off
	v_lshl_add_u64 v[12:13], v[12:13], 0, s[46:47]
	global_load_dword v126, v[12:13], off
	v_lshl_add_u64 v[12:13], v[12:13], 0, s[46:47]
	global_load_dword v127, v[12:13], off
	v_lshl_add_u64 v[12:13], v[12:13], 0, s[46:47]
	global_load_dword v128, v[12:13], off
	v_lshl_add_u64 v[12:13], v[12:13], 0, s[46:47]
	global_load_dword v129, v[12:13], off
	v_lshl_add_u64 v[12:13], v[12:13], 0, s[46:47]
	global_load_dword v130, v[12:13], off
	v_lshl_add_u64 v[12:13], v[12:13], 0, s[46:47]
	global_load_dword v131, v[12:13], off
	v_lshl_add_u64 v[12:13], v[12:13], 0, s[46:47]
	global_load_dword v132, v[12:13], off
	v_lshl_add_u64 v[12:13], v[12:13], 0, s[46:47]
	global_load_dword v133, v[12:13], off
	v_lshl_add_u64 v[12:13], v[12:13], 0, s[46:47]
	global_load_dword v134, v[12:13], off
	v_lshl_add_u64 v[12:13], v[12:13], 0, s[46:47]
	global_load_dword v135, v[12:13], off
	v_lshl_add_u64 v[12:13], v[12:13], 0, s[46:47]
	global_load_dword v136, v[12:13], off
	v_lshl_add_u64 v[12:13], v[12:13], 0, s[46:47]
	global_load_dword v137, v[12:13], off
	v_lshl_add_u64 v[12:13], v[12:13], 0, s[46:47]
	global_load_dword v138, v[12:13], off
	v_lshl_add_u64 v[12:13], v[12:13], 0, s[46:47]
	global_load_dword v139, v[12:13], off
	v_lshl_add_u64 v[12:13], v[12:13], 0, s[46:47]
	global_load_dword v140, v[12:13], off
	v_lshl_add_u64 v[12:13], v[12:13], 0, s[46:47]
	global_load_dword v141, v[12:13], off
	v_lshl_add_u64 v[12:13], v[12:13], 0, s[46:47]
	global_load_dword v142, v[12:13], off
	v_lshl_add_u64 v[12:13], v[12:13], 0, s[46:47]
	global_load_dword v143, v[12:13], off
	v_lshl_add_u64 v[12:13], v[12:13], 0, s[46:47]
	global_load_dword v144, v[12:13], off
	v_lshl_add_u64 v[12:13], v[12:13], 0, s[46:47]
	global_load_dword v145, v[12:13], off
	v_lshl_add_u64 v[12:13], v[12:13], 0, s[46:47]
	global_load_dword v146, v[12:13], off
	v_lshl_add_u64 v[12:13], v[12:13], 0, s[46:47]
	global_load_dword v147, v[12:13], off
	v_lshl_add_u64 v[12:13], v[12:13], 0, s[46:47]
	global_load_dword v148, v[12:13], off
	v_lshl_add_u64 v[12:13], v[12:13], 0, s[46:47]
	global_load_dword v149, v[12:13], off
	v_lshl_add_u64 v[12:13], v[12:13], 0, s[46:47]
	global_load_dword v150, v[12:13], off
	v_lshl_add_u64 v[12:13], v[12:13], 0, s[46:47]
	global_load_dword v151, v[12:13], off
	v_lshl_add_u64 v[12:13], v[12:13], 0, s[46:47]
	global_load_dword v152, v[12:13], off
	v_lshl_add_u64 v[12:13], v[12:13], 0, s[46:47]
	global_load_dword v153, v[12:13], off
	v_lshl_add_u64 v[12:13], v[12:13], 0, s[46:47]
	global_load_dword v154, v[12:13], off
	v_lshl_add_u64 v[12:13], v[12:13], 0, s[46:47]
	global_load_dword v155, v[12:13], off
	v_lshl_add_u64 v[12:13], v[12:13], 0, s[46:47]
	global_load_dword v156, v[12:13], off
	v_lshl_add_u64 v[12:13], v[12:13], 0, s[46:47]
	global_load_dword v157, v[12:13], off
	v_lshl_add_u64 v[12:13], v[12:13], 0, s[46:47]
	global_load_dword v158, v[12:13], off
	v_lshl_add_u64 v[12:13], v[12:13], 0, s[46:47]
	global_load_dword v159, v[12:13], off
	v_lshl_add_u64 v[12:13], v[12:13], 0, s[46:47]
	global_load_dword v160, v[12:13], off
	v_lshl_add_u64 v[12:13], v[12:13], 0, s[46:47]
	global_load_dword v161, v[12:13], off
	v_lshl_add_u64 v[12:13], v[12:13], 0, s[46:47]
	global_load_dword v162, v[12:13], off
	v_lshl_add_u64 v[12:13], v[12:13], 0, s[46:47]
	global_load_dword v163, v[12:13], off
	v_lshl_add_u64 v[12:13], v[12:13], 0, s[46:47]
; __device__ __forceinline__ void p0_prologue(const Args& a, const Frame& F) {
;     ...
;             for (int d = 0; d < 128; ++d) { const float wbv = wb[(size_t)d * 1024] * ps[d];
	global_load_dword v164, v[12:13], off
	v_lshl_add_u64 v[12:13], v[12:13], 0, s[46:47]
	global_load_dword v165, v[12:13], off
	v_lshl_add_u64 v[12:13], v[12:13], 0, s[46:47]
	global_load_dword v166, v[12:13], off
	v_lshl_add_u64 v[12:13], v[12:13], 0, s[46:47]
	global_load_dword v167, v[12:13], off
	v_lshl_add_u64 v[12:13], v[12:13], 0, s[46:47]
	global_load_dword v168, v[12:13], off
	v_lshl_add_u64 v[12:13], v[12:13], 0, s[46:47]
	global_load_dword v169, v[12:13], off
	v_lshl_add_u64 v[12:13], v[12:13], 0, s[46:47]
	global_load_dword v170, v[12:13], off
	v_lshl_add_u64 v[12:13], v[12:13], 0, s[46:47]
	global_load_dword v171, v[12:13], off
	v_lshl_add_u64 v[12:13], v[12:13], 0, s[46:47]
	global_load_dword v172, v[12:13], off
	v_lshl_add_u64 v[12:13], v[12:13], 0, s[46:47]
	global_load_dword v173, v[12:13], off
	v_lshl_add_u64 v[12:13], v[12:13], 0, s[46:47]
	global_load_dword v174, v[12:13], off
	v_lshl_add_u64 v[12:13], v[12:13], 0, s[46:47]
	global_load_dword v175, v[12:13], off
	v_lshl_add_u64 v[12:13], v[12:13], 0, s[46:47]
	global_load_dword v176, v[12:13], off
	v_lshl_add_u64 v[12:13], v[12:13], 0, s[46:47]
	global_load_dword v177, v[12:13], off
	v_lshl_add_u64 v[12:13], v[12:13], 0, s[46:47]
	global_load_dword v178, v[12:13], off
	v_lshl_add_u64 v[12:13], v[12:13], 0, s[46:47]
	global_load_dword v179, v[12:13], off
	v_lshl_add_u64 v[12:13], v[12:13], 0, s[46:47]
	global_load_dword v180, v[12:13], off
	v_lshl_add_u64 v[12:13], v[12:13], 0, s[46:47]
	global_load_dword v181, v[12:13], off
	v_lshl_add_u64 v[12:13], v[12:13], 0, s[46:47]
	global_load_dword v182, v[12:13], off
	v_lshl_add_u64 v[12:13], v[12:13], 0, s[46:47]
	global_load_dword v183, v[12:13], off
	v_lshl_add_u64 v[12:13], v[12:13], 0, s[46:47]
	global_load_dword v184, v[12:13], off
	v_lshl_add_u64 v[12:13], v[12:13], 0, s[46:47]
	global_load_dword v185, v[12:13], off
	v_lshl_add_u64 v[12:13], v[12:13], 0, s[46:47]
	global_load_dword v186, v[12:13], off
	v_lshl_add_u64 v[12:13], v[12:13], 0, s[46:47]
	global_load_dword v187, v[12:13], off
	v_lshl_add_u64 v[12:13], v[12:13], 0, s[46:47]
	global_load_dword v188, v[12:13], off
	v_lshl_add_u64 v[12:13], v[12:13], 0, s[46:47]
	global_load_dword v189, v[12:13], off
	v_lshl_add_u64 v[12:13], v[12:13], 0, s[46:47]
	global_load_dword v190, v[12:13], off
	v_lshl_add_u64 v[12:13], v[12:13], 0, s[46:47]
	global_load_dword v191, v[12:13], off
	v_lshl_add_u64 v[12:13], v[12:13], 0, s[46:47]
	global_load_dword v192, v[12:13], off
	v_lshl_add_u64 v[12:13], v[12:13], 0, s[46:47]
	global_load_dword v193, v[12:13], off
	v_lshl_add_u64 v[12:13], v[12:13], 0, s[46:47]
	global_load_dword v194, v[12:13], off
	v_lshl_add_u64 v[12:13], v[12:13], 0, s[46:47]
	global_load_dword v195, v[12:13], off
	v_lshl_add_u64 v[12:13], v[12:13], 0, s[46:47]
	global_load_dword v196, v[12:13], off
	v_lshl_add_u64 v[12:13], v[12:13], 0, s[46:47]
	global_load_dword v197, v[12:13], off
	v_lshl_add_u64 v[12:13], v[12:13], 0, s[46:47]
	global_load_dword v198, v[12:13], off
	v_lshl_add_u64 v[12:13], v[12:13], 0, s[46:47]
	global_load_dword v199, v[12:13], off
	v_lshl_add_u64 v[12:13], v[12:13], 0, s[46:47]
	global_load_dword v200, v[12:13], off
	v_lshl_add_u64 v[12:13], v[12:13], 0, s[46:47]
	global_load_dword v201, v[12:13], off
	v_lshl_add_u64 v[12:13], v[12:13], 0, s[46:47]
	global_load_dword v202, v[12:13], off
	v_lshl_add_u64 v[12:13], v[12:13], 0, s[46:47]
	global_load_dword v203, v[12:13], off
	v_lshl_add_u64 v[12:13], v[12:13], 0, s[46:47]
	global_load_dword v204, v[12:13], off
	v_lshl_add_u64 v[12:13], v[12:13], 0, s[46:47]
	global_load_dword v205, v[12:13], off
	v_lshl_add_u64 v[12:13], v[12:13], 0, s[46:47]
	global_load_dword v206, v[12:13], off
	v_lshl_add_u64 v[12:13], v[12:13], 0, s[46:47]
	global_load_dword v207, v[12:13], off
	v_lshl_add_u64 v[12:13], v[12:13], 0, s[46:47]
	global_load_dword v208, v[12:13], off
	v_lshl_add_u64 v[12:13], v[12:13], 0, s[46:47]
	global_load_dword v209, v[12:13], off
	v_lshl_add_u64 v[12:13], v[12:13], 0, s[46:47]
	global_load_dword v210, v[12:13], off
	v_lshl_add_u64 v[12:13], v[12:13], 0, s[46:47]
	global_load_dword v211, v[12:13], off
	v_lshl_add_u64 v[12:13], v[12:13], 0, s[46:47]
	global_load_dword v212, v[12:13], off
	v_lshl_add_u64 v[12:13], v[12:13], 0, s[46:47]
	global_load_dword v213, v[12:13], off
	v_lshl_add_u64 v[12:13], v[12:13], 0, s[46:47]
	global_load_dword v214, v[12:13], off
	v_lshl_add_u64 v[12:13], v[12:13], 0, s[46:47]
	global_load_dword v215, v[12:13], off
	v_lshl_add_u64 v[12:13], v[12:13], 0, s[46:47]
	global_load_dword v216, v[12:13], off
	v_lshl_add_u64 v[12:13], v[12:13], 0, s[46:47]
	global_load_dword v217, v[12:13], off
	v_lshl_add_u64 v[12:13], v[12:13], 0, s[46:47]
	global_load_dword v218, v[12:13], off
	v_lshl_add_u64 v[12:13], v[12:13], 0, s[46:47]
	global_load_dword v219, v[12:13], off
	v_lshl_add_u64 v[12:13], v[12:13], 0, s[46:47]
	global_load_dword v220, v[12:13], off
	v_lshl_add_u64 v[12:13], v[12:13], 0, s[46:47]
	global_load_dword v221, v[12:13], off
	v_lshl_add_u64 v[12:13], v[12:13], 0, s[46:47]
	global_load_dword v222, v[12:13], off
	v_lshl_add_u64 v[12:13], v[12:13], 0, s[46:47]
	global_load_dword v223, v[12:13], off
	v_lshl_add_u64 v[12:13], v[12:13], 0, s[46:47]
	global_load_dword v224, v[12:13], off
	v_lshl_add_u64 v[12:13], v[12:13], 0, s[46:47]
	global_load_dword v225, v[12:13], off
	v_lshl_add_u64 v[12:13], v[12:13], 0, s[46:47]
	global_load_dword v226, v[12:13], off
	v_lshl_add_u64 v[12:13], v[12:13], 0, s[46:47]
	global_load_dword v227, v[12:13], off
	v_lshl_add_u64 v[12:13], v[12:13], 0, s[46:47]
	global_load_dword v228, v[12:13], off
	v_lshl_add_u64 v[12:13], v[12:13], 0, s[46:47]
; __device__ __forceinline__ void p0_prologue(const Args& a, const Frame& F) {
;     ...
;             for (int d = 0; d < 128; ++d) { const float wbv = wb[(size_t)d * 1024] * ps[d];
; #pragma unroll
;                 for (int cc = 0; cc < 8; ++cc) acc[cc] += wp[cc * 128 + d] * wbv; }
	global_load_dword v229, v[12:13], off
	v_lshl_add_u64 v[12:13], v[12:13], 0, s[46:47]
	global_load_dword v230, v[12:13], off
	v_lshl_add_u64 v[12:13], v[12:13], 0, s[46:47]
	global_load_dword v231, v[12:13], off
	v_lshl_add_u64 v[12:13], v[12:13], 0, s[46:47]
	global_load_dword v232, v[12:13], off
	v_lshl_add_u64 v[12:13], v[12:13], 0, s[46:47]
	global_load_dword v233, v[12:13], off
	v_lshl_add_u64 v[12:13], v[12:13], 0, s[46:47]
	global_load_dword v234, v[12:13], off
	v_lshl_add_u64 v[12:13], v[12:13], 0, s[46:47]
	global_load_dword v235, v[12:13], off
	v_lshl_add_u64 v[12:13], v[12:13], 0, s[46:47]
	global_load_dword v236, v[12:13], off
	v_lshl_add_u64 v[12:13], v[12:13], 0, s[46:47]
	global_load_dword v237, v[12:13], off
	v_lshl_add_u64 v[12:13], v[12:13], 0, s[46:47]
	global_load_dword v238, v[12:13], off
	v_lshl_add_u64 v[12:13], v[12:13], 0, s[46:47]
	global_load_dword v239, v[12:13], off
	v_lshl_add_u64 v[12:13], v[12:13], 0, s[46:47]
	global_load_dword v240, v[12:13], off
	v_lshl_add_u64 v[12:13], v[12:13], 0, s[46:47]
	global_load_dword v241, v[12:13], off
	v_lshl_add_u64 v[12:13], v[12:13], 0, s[46:47]
	global_load_dword v242, v[12:13], off
	v_lshl_add_u64 v[12:13], v[12:13], 0, s[46:47]
	global_load_dword v243, v[12:13], off
	v_lshl_add_u64 v[12:13], v[12:13], 0, s[46:47]
	global_load_dword v244, v[12:13], off
	v_lshl_add_u64 v[12:13], v[12:13], 0, s[46:47]
	global_load_dword v245, v[12:13], off
	v_lshl_add_u64 v[12:13], v[12:13], 0, s[46:47]
	global_load_dword v246, v[12:13], off
	v_lshl_add_u64 v[12:13], v[12:13], 0, s[46:47]
	global_load_dword v247, v[12:13], off
	s_waitcnt vmcnt(63)
	v_readlane_b32 s98, v116, 0
	v_readlane_b32 s4, v100, 0
	v_readlane_b32 s5, v102, 0
	v_readlane_b32 s8, v104, 0
	v_readlane_b32 s33, v106, 0
	v_readlane_b32 s34, v108, 0
	v_readlane_b32 s35, v110, 0
	v_readlane_b32 s46, v112, 0
	v_readlane_b32 s47, v114, 0
	v_mul_f32_e32 v119, s98, v120
	v_fmac_f32_e32 v16, s4, v119
	v_fmac_f32_e32 v18, s5, v119
	v_fmac_f32_e32 v17, s8, v119
	v_fmac_f32_e32 v19, s33, v119
	v_fmac_f32_e32 v14, s34, v119
	v_fmac_f32_e32 v20, s35, v119
	v_fmac_f32_e32 v15, s46, v119
	v_fmac_f32_e32 v21, s47, v119
	v_readlane_b32 s98, v116, 1
	v_readlane_b32 s4, v100, 1
	v_readlane_b32 s5, v102, 1
	v_readlane_b32 s8, v104, 1
	v_readlane_b32 s33, v106, 1
	v_readlane_b32 s34, v108, 1
	v_readlane_b32 s35, v110, 1
	v_readlane_b32 s46, v112, 1
	v_readlane_b32 s47, v114, 1
	v_mul_f32_e32 v119, s98, v121
	v_fmac_f32_e32 v16, s4, v119
	v_fmac_f32_e32 v18, s5, v119
	v_fmac_f32_e32 v17, s8, v119
	v_fmac_f32_e32 v19, s33, v119
	v_fmac_f32_e32 v14, s34, v119
	v_fmac_f32_e32 v20, s35, v119
	v_fmac_f32_e32 v15, s46, v119
	v_fmac_f32_e32 v21, s47, v119
	v_readlane_b32 s98, v116, 2
	v_readlane_b32 s4, v100, 2
	v_readlane_b32 s5, v102, 2
	v_readlane_b32 s8, v104, 2
	v_readlane_b32 s33, v106, 2
	v_readlane_b32 s34, v108, 2
	v_readlane_b32 s35, v110, 2
	v_readlane_b32 s46, v112, 2
	v_readlane_b32 s47, v114, 2
	v_mul_f32_e32 v119, s98, v122
	v_fmac_f32_e32 v16, s4, v119
	v_fmac_f32_e32 v18, s5, v119
	v_fmac_f32_e32 v17, s8, v119
	v_fmac_f32_e32 v19, s33, v119
	v_fmac_f32_e32 v14, s34, v119
	v_fmac_f32_e32 v20, s35, v119
	v_fmac_f32_e32 v15, s46, v119
	v_fmac_f32_e32 v21, s47, v119
	v_readlane_b32 s98, v116, 3
	v_readlane_b32 s4, v100, 3
	v_readlane_b32 s5, v102, 3
	v_readlane_b32 s8, v104, 3
	v_readlane_b32 s33, v106, 3
	v_readlane_b32 s34, v108, 3
	v_readlane_b32 s35, v110, 3
	v_readlane_b32 s46, v112, 3
	v_readlane_b32 s47, v114, 3
	v_mul_f32_e32 v119, s98, v123
	v_fmac_f32_e32 v16, s4, v119
	v_fmac_f32_e32 v18, s5, v119
	v_fmac_f32_e32 v17, s8, v119
	v_fmac_f32_e32 v19, s33, v119
	v_fmac_f32_e32 v14, s34, v119
	v_fmac_f32_e32 v20, s35, v119
	v_fmac_f32_e32 v15, s46, v119
	v_fmac_f32_e32 v21, s47, v119
	v_readlane_b32 s98, v116, 4
	v_readlane_b32 s4, v100, 4
	v_readlane_b32 s5, v102, 4
	v_readlane_b32 s8, v104, 4
	v_readlane_b32 s33, v106, 4
	v_readlane_b32 s34, v108, 4
	v_readlane_b32 s35, v110, 4
	v_readlane_b32 s46, v112, 4
	v_readlane_b32 s47, v114, 4
	v_mul_f32_e32 v119, s98, v124
	v_fmac_f32_e32 v16, s4, v119
	v_fmac_f32_e32 v18, s5, v119
	v_fmac_f32_e32 v17, s8, v119
	v_fmac_f32_e32 v19, s33, v119
	v_fmac_f32_e32 v14, s34, v119
	v_fmac_f32_e32 v20, s35, v119
	v_fmac_f32_e32 v15, s46, v119
	v_fmac_f32_e32 v21, s47, v119
	v_readlane_b32 s98, v116, 5
	v_readlane_b32 s4, v100, 5
	v_readlane_b32 s5, v102, 5
	v_readlane_b32 s8, v104, 5
	v_readlane_b32 s33, v106, 5
	v_readlane_b32 s34, v108, 5
	v_readlane_b32 s35, v110, 5
	v_readlane_b32 s46, v112, 5
	v_readlane_b32 s47, v114, 5
	v_mul_f32_e32 v119, s98, v125
	v_fmac_f32_e32 v16, s4, v119
	v_fmac_f32_e32 v18, s5, v119
	v_fmac_f32_e32 v17, s8, v119
	v_fmac_f32_e32 v19, s33, v119
	v_fmac_f32_e32 v14, s34, v119
	v_fmac_f32_e32 v20, s35, v119
	v_fmac_f32_e32 v15, s46, v119
	v_fmac_f32_e32 v21, s47, v119
	v_readlane_b32 s98, v116, 6
	v_readlane_b32 s4, v100, 6
	v_readlane_b32 s5, v102, 6
	v_readlane_b32 s8, v104, 6
	v_readlane_b32 s33, v106, 6
	v_readlane_b32 s34, v108, 6
	v_readlane_b32 s35, v110, 6
	v_readlane_b32 s46, v112, 6
	v_readlane_b32 s47, v114, 6
	v_mul_f32_e32 v119, s98, v126
	v_fmac_f32_e32 v16, s4, v119
	v_fmac_f32_e32 v18, s5, v119
	v_fmac_f32_e32 v17, s8, v119
	v_fmac_f32_e32 v19, s33, v119
	v_fmac_f32_e32 v14, s34, v119
	v_fmac_f32_e32 v20, s35, v119
	v_fmac_f32_e32 v15, s46, v119
	v_fmac_f32_e32 v21, s47, v119
	v_readlane_b32 s98, v116, 7
	v_readlane_b32 s4, v100, 7
	v_readlane_b32 s5, v102, 7
	v_readlane_b32 s8, v104, 7
	v_readlane_b32 s33, v106, 7
	v_readlane_b32 s34, v108, 7
	v_readlane_b32 s35, v110, 7
	v_readlane_b32 s46, v112, 7
	v_readlane_b32 s47, v114, 7
	v_mul_f32_e32 v119, s98, v127
; __device__ __forceinline__ void p0_prologue(const Args& a, const Frame& F) {
;     ...
;             for (int d = 0; d < 128; ++d) { const float wbv = wb[(size_t)d * 1024] * ps[d];
; #pragma unroll
;                 for (int cc = 0; cc < 8; ++cc) acc[cc] += wp[cc * 128 + d] * wbv; }
	v_fmac_f32_e32 v16, s4, v119
	v_fmac_f32_e32 v18, s5, v119
	v_fmac_f32_e32 v17, s8, v119
	v_fmac_f32_e32 v19, s33, v119
	v_fmac_f32_e32 v14, s34, v119
	v_fmac_f32_e32 v20, s35, v119
	v_fmac_f32_e32 v15, s46, v119
	v_fmac_f32_e32 v21, s47, v119
	v_readlane_b32 s98, v116, 8
	v_readlane_b32 s4, v100, 8
	v_readlane_b32 s5, v102, 8
	v_readlane_b32 s8, v104, 8
	v_readlane_b32 s33, v106, 8
	v_readlane_b32 s34, v108, 8
	v_readlane_b32 s35, v110, 8
	v_readlane_b32 s46, v112, 8
	v_readlane_b32 s47, v114, 8
	v_mul_f32_e32 v119, s98, v128
	v_fmac_f32_e32 v16, s4, v119
	v_fmac_f32_e32 v18, s5, v119
	v_fmac_f32_e32 v17, s8, v119
	v_fmac_f32_e32 v19, s33, v119
	v_fmac_f32_e32 v14, s34, v119
	v_fmac_f32_e32 v20, s35, v119
	v_fmac_f32_e32 v15, s46, v119
	v_fmac_f32_e32 v21, s47, v119
	v_readlane_b32 s98, v116, 9
	v_readlane_b32 s4, v100, 9
	v_readlane_b32 s5, v102, 9
	v_readlane_b32 s8, v104, 9
	v_readlane_b32 s33, v106, 9
	v_readlane_b32 s34, v108, 9
	v_readlane_b32 s35, v110, 9
	v_readlane_b32 s46, v112, 9
	v_readlane_b32 s47, v114, 9
	v_mul_f32_e32 v119, s98, v129
	v_fmac_f32_e32 v16, s4, v119
	v_fmac_f32_e32 v18, s5, v119
	v_fmac_f32_e32 v17, s8, v119
	v_fmac_f32_e32 v19, s33, v119
	v_fmac_f32_e32 v14, s34, v119
	v_fmac_f32_e32 v20, s35, v119
	v_fmac_f32_e32 v15, s46, v119
	v_fmac_f32_e32 v21, s47, v119
	v_readlane_b32 s98, v116, 10
	v_readlane_b32 s4, v100, 10
	v_readlane_b32 s5, v102, 10
	v_readlane_b32 s8, v104, 10
	v_readlane_b32 s33, v106, 10
	v_readlane_b32 s34, v108, 10
	v_readlane_b32 s35, v110, 10
	v_readlane_b32 s46, v112, 10
	v_readlane_b32 s47, v114, 10
	v_mul_f32_e32 v119, s98, v130
	v_fmac_f32_e32 v16, s4, v119
	v_fmac_f32_e32 v18, s5, v119
	v_fmac_f32_e32 v17, s8, v119
	v_fmac_f32_e32 v19, s33, v119
	v_fmac_f32_e32 v14, s34, v119
	v_fmac_f32_e32 v20, s35, v119
	v_fmac_f32_e32 v15, s46, v119
	v_fmac_f32_e32 v21, s47, v119
	v_readlane_b32 s98, v116, 11
	v_readlane_b32 s4, v100, 11
	v_readlane_b32 s5, v102, 11
	v_readlane_b32 s8, v104, 11
	v_readlane_b32 s33, v106, 11
	v_readlane_b32 s34, v108, 11
	v_readlane_b32 s35, v110, 11
	v_readlane_b32 s46, v112, 11
	v_readlane_b32 s47, v114, 11
	v_mul_f32_e32 v119, s98, v131
	v_fmac_f32_e32 v16, s4, v119
	v_fmac_f32_e32 v18, s5, v119
	v_fmac_f32_e32 v17, s8, v119
	v_fmac_f32_e32 v19, s33, v119
	v_fmac_f32_e32 v14, s34, v119
	v_fmac_f32_e32 v20, s35, v119
	v_fmac_f32_e32 v15, s46, v119
	v_fmac_f32_e32 v21, s47, v119
	v_readlane_b32 s98, v116, 12
	v_readlane_b32 s4, v100, 12
	v_readlane_b32 s5, v102, 12
	v_readlane_b32 s8, v104, 12
	v_readlane_b32 s33, v106, 12
	v_readlane_b32 s34, v108, 12
	v_readlane_b32 s35, v110, 12
	v_readlane_b32 s46, v112, 12
	v_readlane_b32 s47, v114, 12
	v_mul_f32_e32 v119, s98, v132
	v_fmac_f32_e32 v16, s4, v119
	v_fmac_f32_e32 v18, s5, v119
	v_fmac_f32_e32 v17, s8, v119
	v_fmac_f32_e32 v19, s33, v119
	v_fmac_f32_e32 v14, s34, v119
	v_fmac_f32_e32 v20, s35, v119
	v_fmac_f32_e32 v15, s46, v119
	v_fmac_f32_e32 v21, s47, v119
	v_readlane_b32 s98, v116, 13
	v_readlane_b32 s4, v100, 13
	v_readlane_b32 s5, v102, 13
	v_readlane_b32 s8, v104, 13
	v_readlane_b32 s33, v106, 13
	v_readlane_b32 s34, v108, 13
	v_readlane_b32 s35, v110, 13
	v_readlane_b32 s46, v112, 13
	v_readlane_b32 s47, v114, 13
	v_mul_f32_e32 v119, s98, v133
	v_fmac_f32_e32 v16, s4, v119
	v_fmac_f32_e32 v18, s5, v119
	v_fmac_f32_e32 v17, s8, v119
	v_fmac_f32_e32 v19, s33, v119
	v_fmac_f32_e32 v14, s34, v119
	v_fmac_f32_e32 v20, s35, v119
	v_fmac_f32_e32 v15, s46, v119
	v_fmac_f32_e32 v21, s47, v119
	v_readlane_b32 s98, v116, 14
	v_readlane_b32 s4, v100, 14
	v_readlane_b32 s5, v102, 14
	v_readlane_b32 s8, v104, 14
	v_readlane_b32 s33, v106, 14
	v_readlane_b32 s34, v108, 14
	v_readlane_b32 s35, v110, 14
	v_readlane_b32 s46, v112, 14
	v_readlane_b32 s47, v114, 14
	v_mul_f32_e32 v119, s98, v134
	v_fmac_f32_e32 v16, s4, v119
	v_fmac_f32_e32 v18, s5, v119
	v_fmac_f32_e32 v17, s8, v119
	v_fmac_f32_e32 v19, s33, v119
	v_fmac_f32_e32 v14, s34, v119
	v_fmac_f32_e32 v20, s35, v119
	v_fmac_f32_e32 v15, s46, v119
	v_fmac_f32_e32 v21, s47, v119
	v_readlane_b32 s98, v116, 15
	v_readlane_b32 s4, v100, 15
	v_readlane_b32 s5, v102, 15
	v_readlane_b32 s8, v104, 15
	v_readlane_b32 s33, v106, 15
	v_readlane_b32 s34, v108, 15
	v_readlane_b32 s35, v110, 15
	v_readlane_b32 s46, v112, 15
	v_readlane_b32 s47, v114, 15
	v_mul_f32_e32 v119, s98, v135
	v_fmac_f32_e32 v16, s4, v119
	v_fmac_f32_e32 v18, s5, v119
	v_fmac_f32_e32 v17, s8, v119
	v_fmac_f32_e32 v19, s33, v119
	v_fmac_f32_e32 v14, s34, v119
	v_fmac_f32_e32 v20, s35, v119
	v_fmac_f32_e32 v15, s46, v119
	v_fmac_f32_e32 v21, s47, v119
	v_readlane_b32 s98, v116, 16
	v_readlane_b32 s4, v100, 16
	v_readlane_b32 s5, v102, 16
	v_readlane_b32 s8, v104, 16
	v_readlane_b32 s33, v106, 16
	v_readlane_b32 s34, v108, 16
	v_readlane_b32 s35, v110, 16
	v_readlane_b32 s46, v112, 16
	v_readlane_b32 s47, v114, 16
	v_mul_f32_e32 v119, s98, v136
	v_fmac_f32_e32 v16, s4, v119
	v_fmac_f32_e32 v18, s5, v119
	v_fmac_f32_e32 v17, s8, v119
	v_fmac_f32_e32 v19, s33, v119
	v_fmac_f32_e32 v14, s34, v119
	v_fmac_f32_e32 v20, s35, v119
	v_fmac_f32_e32 v15, s46, v119
	v_fmac_f32_e32 v21, s47, v119
	v_readlane_b32 s98, v116, 17
	v_readlane_b32 s4, v100, 17
	v_readlane_b32 s5, v102, 17
	v_readlane_b32 s8, v104, 17
	v_readlane_b32 s33, v106, 17
	v_readlane_b32 s34, v108, 17
	v_readlane_b32 s35, v110, 17
	v_readlane_b32 s46, v112, 17
	v_readlane_b32 s47, v114, 17
	v_mul_f32_e32 v119, s98, v137
	v_fmac_f32_e32 v16, s4, v119
	v_fmac_f32_e32 v18, s5, v119
	v_fmac_f32_e32 v17, s8, v119
	v_fmac_f32_e32 v19, s33, v119
	v_fmac_f32_e32 v14, s34, v119
	v_fmac_f32_e32 v20, s35, v119
	v_fmac_f32_e32 v15, s46, v119
; __device__ __forceinline__ void p0_prologue(const Args& a, const Frame& F) {
;     ...
;             for (int d = 0; d < 128; ++d) { const float wbv = wb[(size_t)d * 1024] * ps[d];
; #pragma unroll
;                 for (int cc = 0; cc < 8; ++cc) acc[cc] += wp[cc * 128 + d] * wbv; }
	v_fmac_f32_e32 v21, s47, v119
	v_readlane_b32 s98, v116, 18
	v_readlane_b32 s4, v100, 18
	v_readlane_b32 s5, v102, 18
	v_readlane_b32 s8, v104, 18
	v_readlane_b32 s33, v106, 18
	v_readlane_b32 s34, v108, 18
	v_readlane_b32 s35, v110, 18
	v_readlane_b32 s46, v112, 18
	v_readlane_b32 s47, v114, 18
	v_mul_f32_e32 v119, s98, v138
	v_fmac_f32_e32 v16, s4, v119
	v_fmac_f32_e32 v18, s5, v119
	v_fmac_f32_e32 v17, s8, v119
	v_fmac_f32_e32 v19, s33, v119
	v_fmac_f32_e32 v14, s34, v119
	v_fmac_f32_e32 v20, s35, v119
	v_fmac_f32_e32 v15, s46, v119
	v_fmac_f32_e32 v21, s47, v119
	v_readlane_b32 s98, v116, 19
	v_readlane_b32 s4, v100, 19
	v_readlane_b32 s5, v102, 19
	v_readlane_b32 s8, v104, 19
	v_readlane_b32 s33, v106, 19
	v_readlane_b32 s34, v108, 19
	v_readlane_b32 s35, v110, 19
	v_readlane_b32 s46, v112, 19
	v_readlane_b32 s47, v114, 19
	v_mul_f32_e32 v119, s98, v139
	v_fmac_f32_e32 v16, s4, v119
	v_fmac_f32_e32 v18, s5, v119
	v_fmac_f32_e32 v17, s8, v119
	v_fmac_f32_e32 v19, s33, v119
	v_fmac_f32_e32 v14, s34, v119
	v_fmac_f32_e32 v20, s35, v119
	v_fmac_f32_e32 v15, s46, v119
	v_fmac_f32_e32 v21, s47, v119
	v_readlane_b32 s98, v116, 20
	v_readlane_b32 s4, v100, 20
	v_readlane_b32 s5, v102, 20
	v_readlane_b32 s8, v104, 20
	v_readlane_b32 s33, v106, 20
	v_readlane_b32 s34, v108, 20
	v_readlane_b32 s35, v110, 20
	v_readlane_b32 s46, v112, 20
	v_readlane_b32 s47, v114, 20
	v_mul_f32_e32 v119, s98, v140
	v_fmac_f32_e32 v16, s4, v119
	v_fmac_f32_e32 v18, s5, v119
	v_fmac_f32_e32 v17, s8, v119
	v_fmac_f32_e32 v19, s33, v119
	v_fmac_f32_e32 v14, s34, v119
	v_fmac_f32_e32 v20, s35, v119
	v_fmac_f32_e32 v15, s46, v119
	v_fmac_f32_e32 v21, s47, v119
	v_readlane_b32 s98, v116, 21
	v_readlane_b32 s4, v100, 21
	v_readlane_b32 s5, v102, 21
	v_readlane_b32 s8, v104, 21
	v_readlane_b32 s33, v106, 21
	v_readlane_b32 s34, v108, 21
	v_readlane_b32 s35, v110, 21
	v_readlane_b32 s46, v112, 21
	v_readlane_b32 s47, v114, 21
	v_mul_f32_e32 v119, s98, v141
	v_fmac_f32_e32 v16, s4, v119
	v_fmac_f32_e32 v18, s5, v119
	v_fmac_f32_e32 v17, s8, v119
	v_fmac_f32_e32 v19, s33, v119
	v_fmac_f32_e32 v14, s34, v119
	v_fmac_f32_e32 v20, s35, v119
	v_fmac_f32_e32 v15, s46, v119
	v_fmac_f32_e32 v21, s47, v119
	v_readlane_b32 s98, v116, 22
	v_readlane_b32 s4, v100, 22
	v_readlane_b32 s5, v102, 22
	v_readlane_b32 s8, v104, 22
	v_readlane_b32 s33, v106, 22
	v_readlane_b32 s34, v108, 22
	v_readlane_b32 s35, v110, 22
	v_readlane_b32 s46, v112, 22
	v_readlane_b32 s47, v114, 22
	v_mul_f32_e32 v119, s98, v142
	v_fmac_f32_e32 v16, s4, v119
	v_fmac_f32_e32 v18, s5, v119
	v_fmac_f32_e32 v17, s8, v119
	v_fmac_f32_e32 v19, s33, v119
	v_fmac_f32_e32 v14, s34, v119
	v_fmac_f32_e32 v20, s35, v119
	v_fmac_f32_e32 v15, s46, v119
	v_fmac_f32_e32 v21, s47, v119
	v_readlane_b32 s98, v116, 23
	v_readlane_b32 s4, v100, 23
	v_readlane_b32 s5, v102, 23
	v_readlane_b32 s8, v104, 23
	v_readlane_b32 s33, v106, 23
	v_readlane_b32 s34, v108, 23
	v_readlane_b32 s35, v110, 23
	v_readlane_b32 s46, v112, 23
	v_readlane_b32 s47, v114, 23
	v_mul_f32_e32 v119, s98, v143
	v_fmac_f32_e32 v16, s4, v119
	v_fmac_f32_e32 v18, s5, v119
	v_fmac_f32_e32 v17, s8, v119
	v_fmac_f32_e32 v19, s33, v119
	v_fmac_f32_e32 v14, s34, v119
	v_fmac_f32_e32 v20, s35, v119
	v_fmac_f32_e32 v15, s46, v119
	v_fmac_f32_e32 v21, s47, v119
	v_readlane_b32 s98, v116, 24
	v_readlane_b32 s4, v100, 24
	v_readlane_b32 s5, v102, 24
	v_readlane_b32 s8, v104, 24
	v_readlane_b32 s33, v106, 24
	v_readlane_b32 s34, v108, 24
	v_readlane_b32 s35, v110, 24
	v_readlane_b32 s46, v112, 24
	v_readlane_b32 s47, v114, 24
	v_mul_f32_e32 v119, s98, v144
	v_fmac_f32_e32 v16, s4, v119
	v_fmac_f32_e32 v18, s5, v119
	v_fmac_f32_e32 v17, s8, v119
	v_fmac_f32_e32 v19, s33, v119
	v_fmac_f32_e32 v14, s34, v119
	v_fmac_f32_e32 v20, s35, v119
	v_fmac_f32_e32 v15, s46, v119
	v_fmac_f32_e32 v21, s47, v119
	v_readlane_b32 s98, v116, 25
	v_readlane_b32 s4, v100, 25
	v_readlane_b32 s5, v102, 25
	v_readlane_b32 s8, v104, 25
	v_readlane_b32 s33, v106, 25
	v_readlane_b32 s34, v108, 25
	v_readlane_b32 s35, v110, 25
	v_readlane_b32 s46, v112, 25
	v_readlane_b32 s47, v114, 25
	v_mul_f32_e32 v119, s98, v145
	v_fmac_f32_e32 v16, s4, v119
	v_fmac_f32_e32 v18, s5, v119
	v_fmac_f32_e32 v17, s8, v119
	v_fmac_f32_e32 v19, s33, v119
	v_fmac_f32_e32 v14, s34, v119
	v_fmac_f32_e32 v20, s35, v119
	v_fmac_f32_e32 v15, s46, v119
	v_fmac_f32_e32 v21, s47, v119
	v_readlane_b32 s98, v116, 26
	v_readlane_b32 s4, v100, 26
	v_readlane_b32 s5, v102, 26
	v_readlane_b32 s8, v104, 26
	v_readlane_b32 s33, v106, 26
	v_readlane_b32 s34, v108, 26
	v_readlane_b32 s35, v110, 26
	v_readlane_b32 s46, v112, 26
	v_readlane_b32 s47, v114, 26
	v_mul_f32_e32 v119, s98, v146
	v_fmac_f32_e32 v16, s4, v119
	v_fmac_f32_e32 v18, s5, v119
	v_fmac_f32_e32 v17, s8, v119
	v_fmac_f32_e32 v19, s33, v119
	v_fmac_f32_e32 v14, s34, v119
	v_fmac_f32_e32 v20, s35, v119
	v_fmac_f32_e32 v15, s46, v119
	v_fmac_f32_e32 v21, s47, v119
	v_readlane_b32 s98, v116, 27
	v_readlane_b32 s4, v100, 27
	v_readlane_b32 s5, v102, 27
	v_readlane_b32 s8, v104, 27
	v_readlane_b32 s33, v106, 27
	v_readlane_b32 s34, v108, 27
	v_readlane_b32 s35, v110, 27
	v_readlane_b32 s46, v112, 27
	v_readlane_b32 s47, v114, 27
	v_mul_f32_e32 v119, s98, v147
	v_fmac_f32_e32 v16, s4, v119
	v_fmac_f32_e32 v18, s5, v119
	v_fmac_f32_e32 v17, s8, v119
	v_fmac_f32_e32 v19, s33, v119
	v_fmac_f32_e32 v14, s34, v119
	v_fmac_f32_e32 v20, s35, v119
	v_fmac_f32_e32 v15, s46, v119
	v_fmac_f32_e32 v21, s47, v119
	v_readlane_b32 s98, v116, 28
	v_readlane_b32 s4, v100, 28
	v_readlane_b32 s5, v102, 28
	v_readlane_b32 s8, v104, 28
	v_readlane_b32 s33, v106, 28
	v_readlane_b32 s34, v108, 28
; __device__ __forceinline__ void p0_prologue(const Args& a, const Frame& F) {
;     ...
;             for (int d = 0; d < 128; ++d) { const float wbv = wb[(size_t)d * 1024] * ps[d];
; #pragma unroll
;                 for (int cc = 0; cc < 8; ++cc) acc[cc] += wp[cc * 128 + d] * wbv; }
	v_readlane_b32 s35, v110, 28
	v_readlane_b32 s46, v112, 28
	v_readlane_b32 s47, v114, 28
	v_mul_f32_e32 v119, s98, v148
	v_fmac_f32_e32 v16, s4, v119
	v_fmac_f32_e32 v18, s5, v119
	v_fmac_f32_e32 v17, s8, v119
	v_fmac_f32_e32 v19, s33, v119
	v_fmac_f32_e32 v14, s34, v119
	v_fmac_f32_e32 v20, s35, v119
	v_fmac_f32_e32 v15, s46, v119
	v_fmac_f32_e32 v21, s47, v119
	v_readlane_b32 s98, v116, 29
	v_readlane_b32 s4, v100, 29
	v_readlane_b32 s5, v102, 29
	v_readlane_b32 s8, v104, 29
	v_readlane_b32 s33, v106, 29
	v_readlane_b32 s34, v108, 29
	v_readlane_b32 s35, v110, 29
	v_readlane_b32 s46, v112, 29
	v_readlane_b32 s47, v114, 29
	v_mul_f32_e32 v119, s98, v149
	v_fmac_f32_e32 v16, s4, v119
	v_fmac_f32_e32 v18, s5, v119
	v_fmac_f32_e32 v17, s8, v119
	v_fmac_f32_e32 v19, s33, v119
	v_fmac_f32_e32 v14, s34, v119
	v_fmac_f32_e32 v20, s35, v119
	v_fmac_f32_e32 v15, s46, v119
	v_fmac_f32_e32 v21, s47, v119
	v_readlane_b32 s98, v116, 30
	v_readlane_b32 s4, v100, 30
	v_readlane_b32 s5, v102, 30
	v_readlane_b32 s8, v104, 30
	v_readlane_b32 s33, v106, 30
	v_readlane_b32 s34, v108, 30
	v_readlane_b32 s35, v110, 30
	v_readlane_b32 s46, v112, 30
	v_readlane_b32 s47, v114, 30
	v_mul_f32_e32 v119, s98, v150
	v_fmac_f32_e32 v16, s4, v119
	v_fmac_f32_e32 v18, s5, v119
	v_fmac_f32_e32 v17, s8, v119
	v_fmac_f32_e32 v19, s33, v119
	v_fmac_f32_e32 v14, s34, v119
	v_fmac_f32_e32 v20, s35, v119
	v_fmac_f32_e32 v15, s46, v119
	v_fmac_f32_e32 v21, s47, v119
	v_readlane_b32 s98, v116, 31
	v_readlane_b32 s4, v100, 31
	v_readlane_b32 s5, v102, 31
	v_readlane_b32 s8, v104, 31
	v_readlane_b32 s33, v106, 31
	v_readlane_b32 s34, v108, 31
	v_readlane_b32 s35, v110, 31
	v_readlane_b32 s46, v112, 31
	v_readlane_b32 s47, v114, 31
	v_mul_f32_e32 v119, s98, v151
	v_fmac_f32_e32 v16, s4, v119
	v_fmac_f32_e32 v18, s5, v119
	v_fmac_f32_e32 v17, s8, v119
	v_fmac_f32_e32 v19, s33, v119
	v_fmac_f32_e32 v14, s34, v119
	v_fmac_f32_e32 v20, s35, v119
	v_fmac_f32_e32 v15, s46, v119
	v_fmac_f32_e32 v21, s47, v119
	v_readlane_b32 s98, v116, 32
	v_readlane_b32 s4, v100, 32
	v_readlane_b32 s5, v102, 32
	v_readlane_b32 s8, v104, 32
	v_readlane_b32 s33, v106, 32
	v_readlane_b32 s34, v108, 32
	v_readlane_b32 s35, v110, 32
	v_readlane_b32 s46, v112, 32
	v_readlane_b32 s47, v114, 32
	v_mul_f32_e32 v119, s98, v152
	v_fmac_f32_e32 v16, s4, v119
	v_fmac_f32_e32 v18, s5, v119
	v_fmac_f32_e32 v17, s8, v119
	v_fmac_f32_e32 v19, s33, v119
	v_fmac_f32_e32 v14, s34, v119
	v_fmac_f32_e32 v20, s35, v119
	v_fmac_f32_e32 v15, s46, v119
	v_fmac_f32_e32 v21, s47, v119
	v_readlane_b32 s98, v116, 33
	v_readlane_b32 s4, v100, 33
	v_readlane_b32 s5, v102, 33
	v_readlane_b32 s8, v104, 33
	v_readlane_b32 s33, v106, 33
	v_readlane_b32 s34, v108, 33
	v_readlane_b32 s35, v110, 33
	v_readlane_b32 s46, v112, 33
	v_readlane_b32 s47, v114, 33
	v_mul_f32_e32 v119, s98, v153
	v_fmac_f32_e32 v16, s4, v119
	v_fmac_f32_e32 v18, s5, v119
	v_fmac_f32_e32 v17, s8, v119
	v_fmac_f32_e32 v19, s33, v119
	v_fmac_f32_e32 v14, s34, v119
	v_fmac_f32_e32 v20, s35, v119
	v_fmac_f32_e32 v15, s46, v119
	v_fmac_f32_e32 v21, s47, v119
	v_readlane_b32 s98, v116, 34
	v_readlane_b32 s4, v100, 34
	v_readlane_b32 s5, v102, 34
	v_readlane_b32 s8, v104, 34
	v_readlane_b32 s33, v106, 34
	v_readlane_b32 s34, v108, 34
	v_readlane_b32 s35, v110, 34
	v_readlane_b32 s46, v112, 34
	v_readlane_b32 s47, v114, 34
	v_mul_f32_e32 v119, s98, v154
	v_fmac_f32_e32 v16, s4, v119
	v_fmac_f32_e32 v18, s5, v119
	v_fmac_f32_e32 v17, s8, v119
	v_fmac_f32_e32 v19, s33, v119
	v_fmac_f32_e32 v14, s34, v119
	v_fmac_f32_e32 v20, s35, v119
	v_fmac_f32_e32 v15, s46, v119
	v_fmac_f32_e32 v21, s47, v119
	v_readlane_b32 s98, v116, 35
	v_readlane_b32 s4, v100, 35
	v_readlane_b32 s5, v102, 35
	v_readlane_b32 s8, v104, 35
	v_readlane_b32 s33, v106, 35
	v_readlane_b32 s34, v108, 35
	v_readlane_b32 s35, v110, 35
	v_readlane_b32 s46, v112, 35
	v_readlane_b32 s47, v114, 35
	v_mul_f32_e32 v119, s98, v155
	v_fmac_f32_e32 v16, s4, v119
	v_fmac_f32_e32 v18, s5, v119
	v_fmac_f32_e32 v17, s8, v119
	v_fmac_f32_e32 v19, s33, v119
	v_fmac_f32_e32 v14, s34, v119
	v_fmac_f32_e32 v20, s35, v119
	v_fmac_f32_e32 v15, s46, v119
	v_fmac_f32_e32 v21, s47, v119
	v_readlane_b32 s98, v116, 36
	v_readlane_b32 s4, v100, 36
	v_readlane_b32 s5, v102, 36
	v_readlane_b32 s8, v104, 36
	v_readlane_b32 s33, v106, 36
	v_readlane_b32 s34, v108, 36
	v_readlane_b32 s35, v110, 36
	v_readlane_b32 s46, v112, 36
	v_readlane_b32 s47, v114, 36
	v_mul_f32_e32 v119, s98, v156
	v_fmac_f32_e32 v16, s4, v119
	v_fmac_f32_e32 v18, s5, v119
	v_fmac_f32_e32 v17, s8, v119
	v_fmac_f32_e32 v19, s33, v119
	v_fmac_f32_e32 v14, s34, v119
	v_fmac_f32_e32 v20, s35, v119
	v_fmac_f32_e32 v15, s46, v119
	v_fmac_f32_e32 v21, s47, v119
	v_readlane_b32 s98, v116, 37
	v_readlane_b32 s4, v100, 37
	v_readlane_b32 s5, v102, 37
	v_readlane_b32 s8, v104, 37
	v_readlane_b32 s33, v106, 37
	v_readlane_b32 s34, v108, 37
	v_readlane_b32 s35, v110, 37
	v_readlane_b32 s46, v112, 37
	v_readlane_b32 s47, v114, 37
	v_mul_f32_e32 v119, s98, v157
	v_fmac_f32_e32 v16, s4, v119
	v_fmac_f32_e32 v18, s5, v119
	v_fmac_f32_e32 v17, s8, v119
	v_fmac_f32_e32 v19, s33, v119
	v_fmac_f32_e32 v14, s34, v119
	v_fmac_f32_e32 v20, s35, v119
	v_fmac_f32_e32 v15, s46, v119
	v_fmac_f32_e32 v21, s47, v119
	v_readlane_b32 s98, v116, 38
	v_readlane_b32 s4, v100, 38
	v_readlane_b32 s5, v102, 38
	v_readlane_b32 s8, v104, 38
	v_readlane_b32 s33, v106, 38
	v_readlane_b32 s34, v108, 38
	v_readlane_b32 s35, v110, 38
	v_readlane_b32 s46, v112, 38
	v_readlane_b32 s47, v114, 38
	v_mul_f32_e32 v119, s98, v158
	v_fmac_f32_e32 v16, s4, v119
	v_fmac_f32_e32 v18, s5, v119
	v_fmac_f32_e32 v17, s8, v119
; __device__ __forceinline__ void p0_prologue(const Args& a, const Frame& F) {
;     ...
;             for (int d = 0; d < 128; ++d) { const float wbv = wb[(size_t)d * 1024] * ps[d];
; #pragma unroll
;                 for (int cc = 0; cc < 8; ++cc) acc[cc] += wp[cc * 128 + d] * wbv; }
	v_fmac_f32_e32 v19, s33, v119
	v_fmac_f32_e32 v14, s34, v119
	v_fmac_f32_e32 v20, s35, v119
	v_fmac_f32_e32 v15, s46, v119
	v_fmac_f32_e32 v21, s47, v119
	v_readlane_b32 s98, v116, 39
	v_readlane_b32 s4, v100, 39
	v_readlane_b32 s5, v102, 39
	v_readlane_b32 s8, v104, 39
	v_readlane_b32 s33, v106, 39
	v_readlane_b32 s34, v108, 39
	v_readlane_b32 s35, v110, 39
	v_readlane_b32 s46, v112, 39
	v_readlane_b32 s47, v114, 39
	v_mul_f32_e32 v119, s98, v159
	v_fmac_f32_e32 v16, s4, v119
	v_fmac_f32_e32 v18, s5, v119
	v_fmac_f32_e32 v17, s8, v119
	v_fmac_f32_e32 v19, s33, v119
	v_fmac_f32_e32 v14, s34, v119
	v_fmac_f32_e32 v20, s35, v119
	v_fmac_f32_e32 v15, s46, v119
	v_fmac_f32_e32 v21, s47, v119
	v_readlane_b32 s98, v116, 40
	v_readlane_b32 s4, v100, 40
	v_readlane_b32 s5, v102, 40
	v_readlane_b32 s8, v104, 40
	v_readlane_b32 s33, v106, 40
	v_readlane_b32 s34, v108, 40
	v_readlane_b32 s35, v110, 40
	v_readlane_b32 s46, v112, 40
	v_readlane_b32 s47, v114, 40
	v_mul_f32_e32 v119, s98, v160
	v_fmac_f32_e32 v16, s4, v119
	v_fmac_f32_e32 v18, s5, v119
	v_fmac_f32_e32 v17, s8, v119
	v_fmac_f32_e32 v19, s33, v119
	v_fmac_f32_e32 v14, s34, v119
	v_fmac_f32_e32 v20, s35, v119
	v_fmac_f32_e32 v15, s46, v119
	v_fmac_f32_e32 v21, s47, v119
	v_readlane_b32 s98, v116, 41
	v_readlane_b32 s4, v100, 41
	v_readlane_b32 s5, v102, 41
	v_readlane_b32 s8, v104, 41
	v_readlane_b32 s33, v106, 41
	v_readlane_b32 s34, v108, 41
	v_readlane_b32 s35, v110, 41
	v_readlane_b32 s46, v112, 41
	v_readlane_b32 s47, v114, 41
	v_mul_f32_e32 v119, s98, v161
	v_fmac_f32_e32 v16, s4, v119
	v_fmac_f32_e32 v18, s5, v119
	v_fmac_f32_e32 v17, s8, v119
	v_fmac_f32_e32 v19, s33, v119
	v_fmac_f32_e32 v14, s34, v119
	v_fmac_f32_e32 v20, s35, v119
	v_fmac_f32_e32 v15, s46, v119
	v_fmac_f32_e32 v21, s47, v119
	v_readlane_b32 s98, v116, 42
	v_readlane_b32 s4, v100, 42
	v_readlane_b32 s5, v102, 42
	v_readlane_b32 s8, v104, 42
	v_readlane_b32 s33, v106, 42
	v_readlane_b32 s34, v108, 42
	v_readlane_b32 s35, v110, 42
	v_readlane_b32 s46, v112, 42
	v_readlane_b32 s47, v114, 42
	v_mul_f32_e32 v119, s98, v162
	v_fmac_f32_e32 v16, s4, v119
	v_fmac_f32_e32 v18, s5, v119
	v_fmac_f32_e32 v17, s8, v119
	v_fmac_f32_e32 v19, s33, v119
	v_fmac_f32_e32 v14, s34, v119
	v_fmac_f32_e32 v20, s35, v119
	v_fmac_f32_e32 v15, s46, v119
	v_fmac_f32_e32 v21, s47, v119
	v_readlane_b32 s98, v116, 43
	v_readlane_b32 s4, v100, 43
	v_readlane_b32 s5, v102, 43
	v_readlane_b32 s8, v104, 43
	v_readlane_b32 s33, v106, 43
	v_readlane_b32 s34, v108, 43
	v_readlane_b32 s35, v110, 43
	v_readlane_b32 s46, v112, 43
	v_readlane_b32 s47, v114, 43
	v_mul_f32_e32 v119, s98, v163
	v_fmac_f32_e32 v16, s4, v119
	v_fmac_f32_e32 v18, s5, v119
	v_fmac_f32_e32 v17, s8, v119
	v_fmac_f32_e32 v19, s33, v119
	v_fmac_f32_e32 v14, s34, v119
	v_fmac_f32_e32 v20, s35, v119
	v_fmac_f32_e32 v15, s46, v119
	v_fmac_f32_e32 v21, s47, v119
	v_readlane_b32 s98, v116, 44
	v_readlane_b32 s4, v100, 44
	v_readlane_b32 s5, v102, 44
	v_readlane_b32 s8, v104, 44
	v_readlane_b32 s33, v106, 44
	v_readlane_b32 s34, v108, 44
	v_readlane_b32 s35, v110, 44
	v_readlane_b32 s46, v112, 44
	v_readlane_b32 s47, v114, 44
	v_mul_f32_e32 v119, s98, v164
	v_fmac_f32_e32 v16, s4, v119
	v_fmac_f32_e32 v18, s5, v119
	v_fmac_f32_e32 v17, s8, v119
	v_fmac_f32_e32 v19, s33, v119
	v_fmac_f32_e32 v14, s34, v119
	v_fmac_f32_e32 v20, s35, v119
	v_fmac_f32_e32 v15, s46, v119
	v_fmac_f32_e32 v21, s47, v119
	v_readlane_b32 s98, v116, 45
	v_readlane_b32 s4, v100, 45
	v_readlane_b32 s5, v102, 45
	v_readlane_b32 s8, v104, 45
	v_readlane_b32 s33, v106, 45
	v_readlane_b32 s34, v108, 45
	v_readlane_b32 s35, v110, 45
	v_readlane_b32 s46, v112, 45
	v_readlane_b32 s47, v114, 45
	v_mul_f32_e32 v119, s98, v165
	v_fmac_f32_e32 v16, s4, v119
	v_fmac_f32_e32 v18, s5, v119
	v_fmac_f32_e32 v17, s8, v119
	v_fmac_f32_e32 v19, s33, v119
	v_fmac_f32_e32 v14, s34, v119
	v_fmac_f32_e32 v20, s35, v119
	v_fmac_f32_e32 v15, s46, v119
	v_fmac_f32_e32 v21, s47, v119
	v_readlane_b32 s98, v116, 46
	v_readlane_b32 s4, v100, 46
	v_readlane_b32 s5, v102, 46
	v_readlane_b32 s8, v104, 46
	v_readlane_b32 s33, v106, 46
	v_readlane_b32 s34, v108, 46
	v_readlane_b32 s35, v110, 46
	v_readlane_b32 s46, v112, 46
	v_readlane_b32 s47, v114, 46
	v_mul_f32_e32 v119, s98, v166
	v_fmac_f32_e32 v16, s4, v119
	v_fmac_f32_e32 v18, s5, v119
	v_fmac_f32_e32 v17, s8, v119
	v_fmac_f32_e32 v19, s33, v119
	v_fmac_f32_e32 v14, s34, v119
	v_fmac_f32_e32 v20, s35, v119
	v_fmac_f32_e32 v15, s46, v119
	v_fmac_f32_e32 v21, s47, v119
	v_readlane_b32 s98, v116, 47
	v_readlane_b32 s4, v100, 47
	v_readlane_b32 s5, v102, 47
	v_readlane_b32 s8, v104, 47
	v_readlane_b32 s33, v106, 47
	v_readlane_b32 s34, v108, 47
	v_readlane_b32 s35, v110, 47
	v_readlane_b32 s46, v112, 47
	v_readlane_b32 s47, v114, 47
	v_mul_f32_e32 v119, s98, v167
	v_fmac_f32_e32 v16, s4, v119
	v_fmac_f32_e32 v18, s5, v119
	v_fmac_f32_e32 v17, s8, v119
	v_fmac_f32_e32 v19, s33, v119
	v_fmac_f32_e32 v14, s34, v119
	v_fmac_f32_e32 v20, s35, v119
	v_fmac_f32_e32 v15, s46, v119
	v_fmac_f32_e32 v21, s47, v119
	v_readlane_b32 s98, v116, 48
	v_readlane_b32 s4, v100, 48
	v_readlane_b32 s5, v102, 48
	v_readlane_b32 s8, v104, 48
	v_readlane_b32 s33, v106, 48
	v_readlane_b32 s34, v108, 48
	v_readlane_b32 s35, v110, 48
	v_readlane_b32 s46, v112, 48
	v_readlane_b32 s47, v114, 48
	v_mul_f32_e32 v119, s98, v168
	v_fmac_f32_e32 v16, s4, v119
	v_fmac_f32_e32 v18, s5, v119
	v_fmac_f32_e32 v17, s8, v119
	v_fmac_f32_e32 v19, s33, v119
	v_fmac_f32_e32 v14, s34, v119
	v_fmac_f32_e32 v20, s35, v119
	v_fmac_f32_e32 v15, s46, v119
	v_fmac_f32_e32 v21, s47, v119
	v_readlane_b32 s98, v116, 49
	v_readlane_b32 s4, v100, 49
; __device__ __forceinline__ void p0_prologue(const Args& a, const Frame& F) {
;     ...
;             for (int d = 0; d < 128; ++d) { const float wbv = wb[(size_t)d * 1024] * ps[d];
; #pragma unroll
;                 for (int cc = 0; cc < 8; ++cc) acc[cc] += wp[cc * 128 + d] * wbv; }
	v_readlane_b32 s5, v102, 49
	v_readlane_b32 s8, v104, 49
	v_readlane_b32 s33, v106, 49
	v_readlane_b32 s34, v108, 49
	v_readlane_b32 s35, v110, 49
	v_readlane_b32 s46, v112, 49
	v_readlane_b32 s47, v114, 49
	v_mul_f32_e32 v119, s98, v169
	v_fmac_f32_e32 v16, s4, v119
	v_fmac_f32_e32 v18, s5, v119
	v_fmac_f32_e32 v17, s8, v119
	v_fmac_f32_e32 v19, s33, v119
	v_fmac_f32_e32 v14, s34, v119
	v_fmac_f32_e32 v20, s35, v119
	v_fmac_f32_e32 v15, s46, v119
	v_fmac_f32_e32 v21, s47, v119
	v_readlane_b32 s98, v116, 50
	v_readlane_b32 s4, v100, 50
	v_readlane_b32 s5, v102, 50
	v_readlane_b32 s8, v104, 50
	v_readlane_b32 s33, v106, 50
	v_readlane_b32 s34, v108, 50
	v_readlane_b32 s35, v110, 50
	v_readlane_b32 s46, v112, 50
	v_readlane_b32 s47, v114, 50
	v_mul_f32_e32 v119, s98, v170
	v_fmac_f32_e32 v16, s4, v119
	v_fmac_f32_e32 v18, s5, v119
	v_fmac_f32_e32 v17, s8, v119
	v_fmac_f32_e32 v19, s33, v119
	v_fmac_f32_e32 v14, s34, v119
	v_fmac_f32_e32 v20, s35, v119
	v_fmac_f32_e32 v15, s46, v119
	v_fmac_f32_e32 v21, s47, v119
	v_readlane_b32 s98, v116, 51
	v_readlane_b32 s4, v100, 51
	v_readlane_b32 s5, v102, 51
	v_readlane_b32 s8, v104, 51
	v_readlane_b32 s33, v106, 51
	v_readlane_b32 s34, v108, 51
	v_readlane_b32 s35, v110, 51
	v_readlane_b32 s46, v112, 51
	v_readlane_b32 s47, v114, 51
	v_mul_f32_e32 v119, s98, v171
	v_fmac_f32_e32 v16, s4, v119
	v_fmac_f32_e32 v18, s5, v119
	v_fmac_f32_e32 v17, s8, v119
	v_fmac_f32_e32 v19, s33, v119
	v_fmac_f32_e32 v14, s34, v119
	v_fmac_f32_e32 v20, s35, v119
	v_fmac_f32_e32 v15, s46, v119
	v_fmac_f32_e32 v21, s47, v119
	v_readlane_b32 s98, v116, 52
	v_readlane_b32 s4, v100, 52
	v_readlane_b32 s5, v102, 52
	v_readlane_b32 s8, v104, 52
	v_readlane_b32 s33, v106, 52
	v_readlane_b32 s34, v108, 52
	v_readlane_b32 s35, v110, 52
	v_readlane_b32 s46, v112, 52
	v_readlane_b32 s47, v114, 52
	v_mul_f32_e32 v119, s98, v172
	v_fmac_f32_e32 v16, s4, v119
	v_fmac_f32_e32 v18, s5, v119
	v_fmac_f32_e32 v17, s8, v119
	v_fmac_f32_e32 v19, s33, v119
	v_fmac_f32_e32 v14, s34, v119
	v_fmac_f32_e32 v20, s35, v119
	v_fmac_f32_e32 v15, s46, v119
	v_fmac_f32_e32 v21, s47, v119
	v_readlane_b32 s98, v116, 53
	v_readlane_b32 s4, v100, 53
	v_readlane_b32 s5, v102, 53
	v_readlane_b32 s8, v104, 53
	v_readlane_b32 s33, v106, 53
	v_readlane_b32 s34, v108, 53
	v_readlane_b32 s35, v110, 53
	v_readlane_b32 s46, v112, 53
	v_readlane_b32 s47, v114, 53
	v_mul_f32_e32 v119, s98, v173
	v_fmac_f32_e32 v16, s4, v119
	v_fmac_f32_e32 v18, s5, v119
	v_fmac_f32_e32 v17, s8, v119
	v_fmac_f32_e32 v19, s33, v119
	v_fmac_f32_e32 v14, s34, v119
	v_fmac_f32_e32 v20, s35, v119
	v_fmac_f32_e32 v15, s46, v119
	v_fmac_f32_e32 v21, s47, v119
	v_readlane_b32 s98, v116, 54
	v_readlane_b32 s4, v100, 54
	v_readlane_b32 s5, v102, 54
	v_readlane_b32 s8, v104, 54
	v_readlane_b32 s33, v106, 54
	v_readlane_b32 s34, v108, 54
	v_readlane_b32 s35, v110, 54
	v_readlane_b32 s46, v112, 54
	v_readlane_b32 s47, v114, 54
	v_mul_f32_e32 v119, s98, v174
	v_fmac_f32_e32 v16, s4, v119
	v_fmac_f32_e32 v18, s5, v119
	v_fmac_f32_e32 v17, s8, v119
	v_fmac_f32_e32 v19, s33, v119
	v_fmac_f32_e32 v14, s34, v119
	v_fmac_f32_e32 v20, s35, v119
	v_fmac_f32_e32 v15, s46, v119
	v_fmac_f32_e32 v21, s47, v119
	v_readlane_b32 s98, v116, 55
	v_readlane_b32 s4, v100, 55
	v_readlane_b32 s5, v102, 55
	v_readlane_b32 s8, v104, 55
	v_readlane_b32 s33, v106, 55
	v_readlane_b32 s34, v108, 55
	v_readlane_b32 s35, v110, 55
	v_readlane_b32 s46, v112, 55
	v_readlane_b32 s47, v114, 55
	v_mul_f32_e32 v119, s98, v175
	v_fmac_f32_e32 v16, s4, v119
	v_fmac_f32_e32 v18, s5, v119
	v_fmac_f32_e32 v17, s8, v119
	v_fmac_f32_e32 v19, s33, v119
	v_fmac_f32_e32 v14, s34, v119
	v_fmac_f32_e32 v20, s35, v119
	v_fmac_f32_e32 v15, s46, v119
	v_fmac_f32_e32 v21, s47, v119
	v_readlane_b32 s98, v116, 56
	v_readlane_b32 s4, v100, 56
	v_readlane_b32 s5, v102, 56
	v_readlane_b32 s8, v104, 56
	v_readlane_b32 s33, v106, 56
	v_readlane_b32 s34, v108, 56
	v_readlane_b32 s35, v110, 56
	v_readlane_b32 s46, v112, 56
	v_readlane_b32 s47, v114, 56
	v_mul_f32_e32 v119, s98, v176
	v_fmac_f32_e32 v16, s4, v119
	v_fmac_f32_e32 v18, s5, v119
	v_fmac_f32_e32 v17, s8, v119
	v_fmac_f32_e32 v19, s33, v119
	v_fmac_f32_e32 v14, s34, v119
	v_fmac_f32_e32 v20, s35, v119
	v_fmac_f32_e32 v15, s46, v119
	v_fmac_f32_e32 v21, s47, v119
	v_readlane_b32 s98, v116, 57
	v_readlane_b32 s4, v100, 57
	v_readlane_b32 s5, v102, 57
	v_readlane_b32 s8, v104, 57
	v_readlane_b32 s33, v106, 57
	v_readlane_b32 s34, v108, 57
	v_readlane_b32 s35, v110, 57
	v_readlane_b32 s46, v112, 57
	v_readlane_b32 s47, v114, 57
	v_mul_f32_e32 v119, s98, v177
	v_fmac_f32_e32 v16, s4, v119
	v_fmac_f32_e32 v18, s5, v119
	v_fmac_f32_e32 v17, s8, v119
	v_fmac_f32_e32 v19, s33, v119
	v_fmac_f32_e32 v14, s34, v119
	v_fmac_f32_e32 v20, s35, v119
	v_fmac_f32_e32 v15, s46, v119
	v_fmac_f32_e32 v21, s47, v119
	v_readlane_b32 s98, v116, 58
	v_readlane_b32 s4, v100, 58
	v_readlane_b32 s5, v102, 58
	v_readlane_b32 s8, v104, 58
	v_readlane_b32 s33, v106, 58
	v_readlane_b32 s34, v108, 58
	v_readlane_b32 s35, v110, 58
	v_readlane_b32 s46, v112, 58
	v_readlane_b32 s47, v114, 58
	v_mul_f32_e32 v119, s98, v178
	v_fmac_f32_e32 v16, s4, v119
	v_fmac_f32_e32 v18, s5, v119
	v_fmac_f32_e32 v17, s8, v119
	v_fmac_f32_e32 v19, s33, v119
	v_fmac_f32_e32 v14, s34, v119
	v_fmac_f32_e32 v20, s35, v119
	v_fmac_f32_e32 v15, s46, v119
	v_fmac_f32_e32 v21, s47, v119
	v_readlane_b32 s98, v116, 59
	v_readlane_b32 s4, v100, 59
	v_readlane_b32 s5, v102, 59
	v_readlane_b32 s8, v104, 59
	v_readlane_b32 s33, v106, 59
	v_readlane_b32 s34, v108, 59
	v_readlane_b32 s35, v110, 59
	v_readlane_b32 s46, v112, 59
	v_readlane_b32 s47, v114, 59
; __device__ __forceinline__ void p0_prologue(const Args& a, const Frame& F) {
;     ...
;             for (int d = 0; d < 128; ++d) { const float wbv = wb[(size_t)d * 1024] * ps[d];
; #pragma unroll
;                 for (int cc = 0; cc < 8; ++cc) acc[cc] += wp[cc * 128 + d] * wbv; }
	v_mul_f32_e32 v119, s98, v179
	v_fmac_f32_e32 v16, s4, v119
	v_fmac_f32_e32 v18, s5, v119
	v_fmac_f32_e32 v17, s8, v119
	v_fmac_f32_e32 v19, s33, v119
	v_fmac_f32_e32 v14, s34, v119
	v_fmac_f32_e32 v20, s35, v119
	v_fmac_f32_e32 v15, s46, v119
	v_fmac_f32_e32 v21, s47, v119
	v_readlane_b32 s98, v116, 60
	v_readlane_b32 s4, v100, 60
	v_readlane_b32 s5, v102, 60
	v_readlane_b32 s8, v104, 60
	v_readlane_b32 s33, v106, 60
	v_readlane_b32 s34, v108, 60
	v_readlane_b32 s35, v110, 60
	v_readlane_b32 s46, v112, 60
	v_readlane_b32 s47, v114, 60
	v_mul_f32_e32 v119, s98, v180
	v_fmac_f32_e32 v16, s4, v119
	v_fmac_f32_e32 v18, s5, v119
	v_fmac_f32_e32 v17, s8, v119
	v_fmac_f32_e32 v19, s33, v119
	v_fmac_f32_e32 v14, s34, v119
	v_fmac_f32_e32 v20, s35, v119
	v_fmac_f32_e32 v15, s46, v119
	v_fmac_f32_e32 v21, s47, v119
	v_readlane_b32 s98, v116, 61
	v_readlane_b32 s4, v100, 61
	v_readlane_b32 s5, v102, 61
	v_readlane_b32 s8, v104, 61
	v_readlane_b32 s33, v106, 61
	v_readlane_b32 s34, v108, 61
	v_readlane_b32 s35, v110, 61
	v_readlane_b32 s46, v112, 61
	v_readlane_b32 s47, v114, 61
	v_mul_f32_e32 v119, s98, v181
	v_fmac_f32_e32 v16, s4, v119
	v_fmac_f32_e32 v18, s5, v119
	v_fmac_f32_e32 v17, s8, v119
	v_fmac_f32_e32 v19, s33, v119
	v_fmac_f32_e32 v14, s34, v119
	v_fmac_f32_e32 v20, s35, v119
	v_fmac_f32_e32 v15, s46, v119
	v_fmac_f32_e32 v21, s47, v119
	v_readlane_b32 s98, v116, 62
	v_readlane_b32 s4, v100, 62
	v_readlane_b32 s5, v102, 62
	v_readlane_b32 s8, v104, 62
	v_readlane_b32 s33, v106, 62
	v_readlane_b32 s34, v108, 62
	v_readlane_b32 s35, v110, 62
	v_readlane_b32 s46, v112, 62
	v_readlane_b32 s47, v114, 62
	v_mul_f32_e32 v119, s98, v182
	v_fmac_f32_e32 v16, s4, v119
	v_fmac_f32_e32 v18, s5, v119
	v_fmac_f32_e32 v17, s8, v119
	v_fmac_f32_e32 v19, s33, v119
	v_fmac_f32_e32 v14, s34, v119
	v_fmac_f32_e32 v20, s35, v119
	v_fmac_f32_e32 v15, s46, v119
	v_fmac_f32_e32 v21, s47, v119
	v_readlane_b32 s98, v116, 63
	v_readlane_b32 s4, v100, 63
	v_readlane_b32 s5, v102, 63
	v_readlane_b32 s8, v104, 63
	v_readlane_b32 s33, v106, 63
	v_readlane_b32 s34, v108, 63
	v_readlane_b32 s35, v110, 63
	v_readlane_b32 s46, v112, 63
	v_readlane_b32 s47, v114, 63
	v_mul_f32_e32 v119, s98, v183
	v_fmac_f32_e32 v16, s4, v119
	v_fmac_f32_e32 v18, s5, v119
	v_fmac_f32_e32 v17, s8, v119
	v_fmac_f32_e32 v19, s33, v119
	v_fmac_f32_e32 v14, s34, v119
	v_fmac_f32_e32 v20, s35, v119
	v_fmac_f32_e32 v15, s46, v119
	v_fmac_f32_e32 v21, s47, v119
	v_readlane_b32 s98, v117, 0
	v_readlane_b32 s4, v101, 0
	v_readlane_b32 s5, v103, 0
	v_readlane_b32 s8, v105, 0
	v_readlane_b32 s33, v107, 0
	v_readlane_b32 s34, v109, 0
	v_readlane_b32 s35, v111, 0
	v_readlane_b32 s46, v113, 0
	v_readlane_b32 s47, v115, 0
	v_mul_f32_e32 v119, s98, v184
	v_fmac_f32_e32 v16, s4, v119
	v_fmac_f32_e32 v18, s5, v119
	v_fmac_f32_e32 v17, s8, v119
	v_fmac_f32_e32 v19, s33, v119
	v_fmac_f32_e32 v14, s34, v119
	v_fmac_f32_e32 v20, s35, v119
	v_fmac_f32_e32 v15, s46, v119
	v_fmac_f32_e32 v21, s47, v119
	s_waitcnt vmcnt(62)
	v_readlane_b32 s98, v117, 1
	v_readlane_b32 s4, v101, 1
	v_readlane_b32 s5, v103, 1
	v_readlane_b32 s8, v105, 1
	v_readlane_b32 s33, v107, 1
	v_readlane_b32 s34, v109, 1
	v_readlane_b32 s35, v111, 1
	v_readlane_b32 s46, v113, 1
	v_readlane_b32 s47, v115, 1
	v_mul_f32_e32 v119, s98, v185
	v_fmac_f32_e32 v16, s4, v119
	v_fmac_f32_e32 v18, s5, v119
	v_fmac_f32_e32 v17, s8, v119
	v_fmac_f32_e32 v19, s33, v119
	v_fmac_f32_e32 v14, s34, v119
	v_fmac_f32_e32 v20, s35, v119
	v_fmac_f32_e32 v15, s46, v119
	v_fmac_f32_e32 v21, s47, v119
	s_waitcnt vmcnt(61)
	v_readlane_b32 s98, v117, 2
	v_readlane_b32 s4, v101, 2
	v_readlane_b32 s5, v103, 2
	v_readlane_b32 s8, v105, 2
	v_readlane_b32 s33, v107, 2
	v_readlane_b32 s34, v109, 2
	v_readlane_b32 s35, v111, 2
	v_readlane_b32 s46, v113, 2
	v_readlane_b32 s47, v115, 2
	v_mul_f32_e32 v119, s98, v186
	v_fmac_f32_e32 v16, s4, v119
	v_fmac_f32_e32 v18, s5, v119
	v_fmac_f32_e32 v17, s8, v119
	v_fmac_f32_e32 v19, s33, v119
	v_fmac_f32_e32 v14, s34, v119
	v_fmac_f32_e32 v20, s35, v119
	v_fmac_f32_e32 v15, s46, v119
	v_fmac_f32_e32 v21, s47, v119
	s_waitcnt vmcnt(60)
	v_readlane_b32 s98, v117, 3
	v_readlane_b32 s4, v101, 3
	v_readlane_b32 s5, v103, 3
	v_readlane_b32 s8, v105, 3
	v_readlane_b32 s33, v107, 3
	v_readlane_b32 s34, v109, 3
	v_readlane_b32 s35, v111, 3
	v_readlane_b32 s46, v113, 3
	v_readlane_b32 s47, v115, 3
	v_mul_f32_e32 v119, s98, v187
	v_fmac_f32_e32 v16, s4, v119
	v_fmac_f32_e32 v18, s5, v119
	v_fmac_f32_e32 v17, s8, v119
	v_fmac_f32_e32 v19, s33, v119
	v_fmac_f32_e32 v14, s34, v119
	v_fmac_f32_e32 v20, s35, v119
	v_fmac_f32_e32 v15, s46, v119
	v_fmac_f32_e32 v21, s47, v119
	s_waitcnt vmcnt(59)
	v_readlane_b32 s98, v117, 4
	v_readlane_b32 s4, v101, 4
	v_readlane_b32 s5, v103, 4
	v_readlane_b32 s8, v105, 4
	v_readlane_b32 s33, v107, 4
	v_readlane_b32 s34, v109, 4
	v_readlane_b32 s35, v111, 4
	v_readlane_b32 s46, v113, 4
	v_readlane_b32 s47, v115, 4
	v_mul_f32_e32 v119, s98, v188
	v_fmac_f32_e32 v16, s4, v119
	v_fmac_f32_e32 v18, s5, v119
	v_fmac_f32_e32 v17, s8, v119
	v_fmac_f32_e32 v19, s33, v119
	v_fmac_f32_e32 v14, s34, v119
	v_fmac_f32_e32 v20, s35, v119
	v_fmac_f32_e32 v15, s46, v119
	v_fmac_f32_e32 v21, s47, v119
	s_waitcnt vmcnt(58)
	v_readlane_b32 s98, v117, 5
	v_readlane_b32 s4, v101, 5
	v_readlane_b32 s5, v103, 5
	v_readlane_b32 s8, v105, 5
	v_readlane_b32 s33, v107, 5
	v_readlane_b32 s34, v109, 5
	v_readlane_b32 s35, v111, 5
	v_readlane_b32 s46, v113, 5
	v_readlane_b32 s47, v115, 5
	v_mul_f32_e32 v119, s98, v189
	v_fmac_f32_e32 v16, s4, v119
	v_fmac_f32_e32 v18, s5, v119
	v_fmac_f32_e32 v17, s8, v119
	v_fmac_f32_e32 v19, s33, v119
	v_fmac_f32_e32 v14, s34, v119
	v_fmac_f32_e32 v20, s35, v119
	v_fmac_f32_e32 v15, s46, v119
	v_fmac_f32_e32 v21, s47, v119
	s_waitcnt vmcnt(57)
; __device__ __forceinline__ void p0_prologue(const Args& a, const Frame& F) {
;     ...
;             for (int d = 0; d < 128; ++d) { const float wbv = wb[(size_t)d * 1024] * ps[d];
; #pragma unroll
;                 for (int cc = 0; cc < 8; ++cc) acc[cc] += wp[cc * 128 + d] * wbv; }
	v_readlane_b32 s98, v117, 6
	v_readlane_b32 s4, v101, 6
	v_readlane_b32 s5, v103, 6
	v_readlane_b32 s8, v105, 6
	v_readlane_b32 s33, v107, 6
	v_readlane_b32 s34, v109, 6
	v_readlane_b32 s35, v111, 6
	v_readlane_b32 s46, v113, 6
	v_readlane_b32 s47, v115, 6
	v_mul_f32_e32 v119, s98, v190
	v_fmac_f32_e32 v16, s4, v119
	v_fmac_f32_e32 v18, s5, v119
	v_fmac_f32_e32 v17, s8, v119
	v_fmac_f32_e32 v19, s33, v119
	v_fmac_f32_e32 v14, s34, v119
	v_fmac_f32_e32 v20, s35, v119
	v_fmac_f32_e32 v15, s46, v119
	v_fmac_f32_e32 v21, s47, v119
	s_waitcnt vmcnt(56)
	v_readlane_b32 s98, v117, 7
	v_readlane_b32 s4, v101, 7
	v_readlane_b32 s5, v103, 7
	v_readlane_b32 s8, v105, 7
	v_readlane_b32 s33, v107, 7
	v_readlane_b32 s34, v109, 7
	v_readlane_b32 s35, v111, 7
	v_readlane_b32 s46, v113, 7
	v_readlane_b32 s47, v115, 7
	v_mul_f32_e32 v119, s98, v191
	v_fmac_f32_e32 v16, s4, v119
	v_fmac_f32_e32 v18, s5, v119
	v_fmac_f32_e32 v17, s8, v119
	v_fmac_f32_e32 v19, s33, v119
	v_fmac_f32_e32 v14, s34, v119
	v_fmac_f32_e32 v20, s35, v119
	v_fmac_f32_e32 v15, s46, v119
	v_fmac_f32_e32 v21, s47, v119
	s_waitcnt vmcnt(55)
	v_readlane_b32 s98, v117, 8
	v_readlane_b32 s4, v101, 8
	v_readlane_b32 s5, v103, 8
	v_readlane_b32 s8, v105, 8
	v_readlane_b32 s33, v107, 8
	v_readlane_b32 s34, v109, 8
	v_readlane_b32 s35, v111, 8
	v_readlane_b32 s46, v113, 8
	v_readlane_b32 s47, v115, 8
	v_mul_f32_e32 v119, s98, v192
	v_fmac_f32_e32 v16, s4, v119
	v_fmac_f32_e32 v18, s5, v119
	v_fmac_f32_e32 v17, s8, v119
	v_fmac_f32_e32 v19, s33, v119
	v_fmac_f32_e32 v14, s34, v119
	v_fmac_f32_e32 v20, s35, v119
	v_fmac_f32_e32 v15, s46, v119
	v_fmac_f32_e32 v21, s47, v119
	s_waitcnt vmcnt(54)
	v_readlane_b32 s98, v117, 9
	v_readlane_b32 s4, v101, 9
	v_readlane_b32 s5, v103, 9
	v_readlane_b32 s8, v105, 9
	v_readlane_b32 s33, v107, 9
	v_readlane_b32 s34, v109, 9
	v_readlane_b32 s35, v111, 9
	v_readlane_b32 s46, v113, 9
	v_readlane_b32 s47, v115, 9
	v_mul_f32_e32 v119, s98, v193
	v_fmac_f32_e32 v16, s4, v119
	v_fmac_f32_e32 v18, s5, v119
	v_fmac_f32_e32 v17, s8, v119
	v_fmac_f32_e32 v19, s33, v119
	v_fmac_f32_e32 v14, s34, v119
	v_fmac_f32_e32 v20, s35, v119
	v_fmac_f32_e32 v15, s46, v119
	v_fmac_f32_e32 v21, s47, v119
	s_waitcnt vmcnt(53)
	v_readlane_b32 s98, v117, 10
	v_readlane_b32 s4, v101, 10
	v_readlane_b32 s5, v103, 10
	v_readlane_b32 s8, v105, 10
	v_readlane_b32 s33, v107, 10
	v_readlane_b32 s34, v109, 10
	v_readlane_b32 s35, v111, 10
	v_readlane_b32 s46, v113, 10
	v_readlane_b32 s47, v115, 10
	v_mul_f32_e32 v119, s98, v194
	v_fmac_f32_e32 v16, s4, v119
	v_fmac_f32_e32 v18, s5, v119
	v_fmac_f32_e32 v17, s8, v119
	v_fmac_f32_e32 v19, s33, v119
	v_fmac_f32_e32 v14, s34, v119
	v_fmac_f32_e32 v20, s35, v119
	v_fmac_f32_e32 v15, s46, v119
	v_fmac_f32_e32 v21, s47, v119
	s_waitcnt vmcnt(52)
	v_readlane_b32 s98, v117, 11
	v_readlane_b32 s4, v101, 11
	v_readlane_b32 s5, v103, 11
	v_readlane_b32 s8, v105, 11
	v_readlane_b32 s33, v107, 11
	v_readlane_b32 s34, v109, 11
	v_readlane_b32 s35, v111, 11
	v_readlane_b32 s46, v113, 11
	v_readlane_b32 s47, v115, 11
	v_mul_f32_e32 v119, s98, v195
	v_fmac_f32_e32 v16, s4, v119
	v_fmac_f32_e32 v18, s5, v119
	v_fmac_f32_e32 v17, s8, v119
	v_fmac_f32_e32 v19, s33, v119
	v_fmac_f32_e32 v14, s34, v119
	v_fmac_f32_e32 v20, s35, v119
	v_fmac_f32_e32 v15, s46, v119
	v_fmac_f32_e32 v21, s47, v119
	s_waitcnt vmcnt(51)
	v_readlane_b32 s98, v117, 12
	v_readlane_b32 s4, v101, 12
	v_readlane_b32 s5, v103, 12
	v_readlane_b32 s8, v105, 12
	v_readlane_b32 s33, v107, 12
	v_readlane_b32 s34, v109, 12
	v_readlane_b32 s35, v111, 12
	v_readlane_b32 s46, v113, 12
	v_readlane_b32 s47, v115, 12
	v_mul_f32_e32 v119, s98, v196
	v_fmac_f32_e32 v16, s4, v119
	v_fmac_f32_e32 v18, s5, v119
	v_fmac_f32_e32 v17, s8, v119
	v_fmac_f32_e32 v19, s33, v119
	v_fmac_f32_e32 v14, s34, v119
	v_fmac_f32_e32 v20, s35, v119
	v_fmac_f32_e32 v15, s46, v119
	v_fmac_f32_e32 v21, s47, v119
	s_waitcnt vmcnt(50)
	v_readlane_b32 s98, v117, 13
	v_readlane_b32 s4, v101, 13
	v_readlane_b32 s5, v103, 13
	v_readlane_b32 s8, v105, 13
	v_readlane_b32 s33, v107, 13
	v_readlane_b32 s34, v109, 13
	v_readlane_b32 s35, v111, 13
	v_readlane_b32 s46, v113, 13
	v_readlane_b32 s47, v115, 13
	v_mul_f32_e32 v119, s98, v197
	v_fmac_f32_e32 v16, s4, v119
	v_fmac_f32_e32 v18, s5, v119
	v_fmac_f32_e32 v17, s8, v119
	v_fmac_f32_e32 v19, s33, v119
	v_fmac_f32_e32 v14, s34, v119
	v_fmac_f32_e32 v20, s35, v119
	v_fmac_f32_e32 v15, s46, v119
	v_fmac_f32_e32 v21, s47, v119
	s_waitcnt vmcnt(49)
	v_readlane_b32 s98, v117, 14
	v_readlane_b32 s4, v101, 14
	v_readlane_b32 s5, v103, 14
	v_readlane_b32 s8, v105, 14
	v_readlane_b32 s33, v107, 14
	v_readlane_b32 s34, v109, 14
	v_readlane_b32 s35, v111, 14
	v_readlane_b32 s46, v113, 14
	v_readlane_b32 s47, v115, 14
	v_mul_f32_e32 v119, s98, v198
	v_fmac_f32_e32 v16, s4, v119
	v_fmac_f32_e32 v18, s5, v119
	v_fmac_f32_e32 v17, s8, v119
	v_fmac_f32_e32 v19, s33, v119
	v_fmac_f32_e32 v14, s34, v119
	v_fmac_f32_e32 v20, s35, v119
	v_fmac_f32_e32 v15, s46, v119
	v_fmac_f32_e32 v21, s47, v119
	s_waitcnt vmcnt(48)
	v_readlane_b32 s98, v117, 15
	v_readlane_b32 s4, v101, 15
	v_readlane_b32 s5, v103, 15
	v_readlane_b32 s8, v105, 15
	v_readlane_b32 s33, v107, 15
	v_readlane_b32 s34, v109, 15
	v_readlane_b32 s35, v111, 15
	v_readlane_b32 s46, v113, 15
	v_readlane_b32 s47, v115, 15
	v_mul_f32_e32 v119, s98, v199
	v_fmac_f32_e32 v16, s4, v119
	v_fmac_f32_e32 v18, s5, v119
	v_fmac_f32_e32 v17, s8, v119
	v_fmac_f32_e32 v19, s33, v119
	v_fmac_f32_e32 v14, s34, v119
	v_fmac_f32_e32 v20, s35, v119
	v_fmac_f32_e32 v15, s46, v119
	v_fmac_f32_e32 v21, s47, v119
	s_waitcnt vmcnt(47)
; __device__ __forceinline__ void p0_prologue(const Args& a, const Frame& F) {
;     ...
;             for (int d = 0; d < 128; ++d) { const float wbv = wb[(size_t)d * 1024] * ps[d];
; #pragma unroll
;                 for (int cc = 0; cc < 8; ++cc) acc[cc] += wp[cc * 128 + d] * wbv; }
	v_readlane_b32 s98, v117, 16
	v_readlane_b32 s4, v101, 16
	v_readlane_b32 s5, v103, 16
	v_readlane_b32 s8, v105, 16
	v_readlane_b32 s33, v107, 16
	v_readlane_b32 s34, v109, 16
	v_readlane_b32 s35, v111, 16
	v_readlane_b32 s46, v113, 16
	v_readlane_b32 s47, v115, 16
	v_mul_f32_e32 v119, s98, v200
	v_fmac_f32_e32 v16, s4, v119
	v_fmac_f32_e32 v18, s5, v119
	v_fmac_f32_e32 v17, s8, v119
	v_fmac_f32_e32 v19, s33, v119
	v_fmac_f32_e32 v14, s34, v119
	v_fmac_f32_e32 v20, s35, v119
	v_fmac_f32_e32 v15, s46, v119
	v_fmac_f32_e32 v21, s47, v119
	s_waitcnt vmcnt(46)
	v_readlane_b32 s98, v117, 17
	v_readlane_b32 s4, v101, 17
	v_readlane_b32 s5, v103, 17
	v_readlane_b32 s8, v105, 17
	v_readlane_b32 s33, v107, 17
	v_readlane_b32 s34, v109, 17
	v_readlane_b32 s35, v111, 17
	v_readlane_b32 s46, v113, 17
	v_readlane_b32 s47, v115, 17
	v_mul_f32_e32 v119, s98, v201
	v_fmac_f32_e32 v16, s4, v119
	v_fmac_f32_e32 v18, s5, v119
	v_fmac_f32_e32 v17, s8, v119
	v_fmac_f32_e32 v19, s33, v119
	v_fmac_f32_e32 v14, s34, v119
	v_fmac_f32_e32 v20, s35, v119
	v_fmac_f32_e32 v15, s46, v119
	v_fmac_f32_e32 v21, s47, v119
	s_waitcnt vmcnt(45)
	v_readlane_b32 s98, v117, 18
	v_readlane_b32 s4, v101, 18
	v_readlane_b32 s5, v103, 18
	v_readlane_b32 s8, v105, 18
	v_readlane_b32 s33, v107, 18
	v_readlane_b32 s34, v109, 18
	v_readlane_b32 s35, v111, 18
	v_readlane_b32 s46, v113, 18
	v_readlane_b32 s47, v115, 18
	v_mul_f32_e32 v119, s98, v202
	v_fmac_f32_e32 v16, s4, v119
	v_fmac_f32_e32 v18, s5, v119
	v_fmac_f32_e32 v17, s8, v119
	v_fmac_f32_e32 v19, s33, v119
	v_fmac_f32_e32 v14, s34, v119
	v_fmac_f32_e32 v20, s35, v119
	v_fmac_f32_e32 v15, s46, v119
	v_fmac_f32_e32 v21, s47, v119
	s_waitcnt vmcnt(44)
	v_readlane_b32 s98, v117, 19
	v_readlane_b32 s4, v101, 19
	v_readlane_b32 s5, v103, 19
	v_readlane_b32 s8, v105, 19
	v_readlane_b32 s33, v107, 19
	v_readlane_b32 s34, v109, 19
	v_readlane_b32 s35, v111, 19
	v_readlane_b32 s46, v113, 19
	v_readlane_b32 s47, v115, 19
	v_mul_f32_e32 v119, s98, v203
	v_fmac_f32_e32 v16, s4, v119
	v_fmac_f32_e32 v18, s5, v119
	v_fmac_f32_e32 v17, s8, v119
	v_fmac_f32_e32 v19, s33, v119
	v_fmac_f32_e32 v14, s34, v119
	v_fmac_f32_e32 v20, s35, v119
	v_fmac_f32_e32 v15, s46, v119
	v_fmac_f32_e32 v21, s47, v119
	s_waitcnt vmcnt(43)
	v_readlane_b32 s98, v117, 20
	v_readlane_b32 s4, v101, 20
	v_readlane_b32 s5, v103, 20
	v_readlane_b32 s8, v105, 20
	v_readlane_b32 s33, v107, 20
	v_readlane_b32 s34, v109, 20
	v_readlane_b32 s35, v111, 20
	v_readlane_b32 s46, v113, 20
	v_readlane_b32 s47, v115, 20
	v_mul_f32_e32 v119, s98, v204
	v_fmac_f32_e32 v16, s4, v119
	v_fmac_f32_e32 v18, s5, v119
	v_fmac_f32_e32 v17, s8, v119
	v_fmac_f32_e32 v19, s33, v119
	v_fmac_f32_e32 v14, s34, v119
	v_fmac_f32_e32 v20, s35, v119
	v_fmac_f32_e32 v15, s46, v119
	v_fmac_f32_e32 v21, s47, v119
	s_waitcnt vmcnt(42)
	v_readlane_b32 s98, v117, 21
	v_readlane_b32 s4, v101, 21
	v_readlane_b32 s5, v103, 21
	v_readlane_b32 s8, v105, 21
	v_readlane_b32 s33, v107, 21
	v_readlane_b32 s34, v109, 21
	v_readlane_b32 s35, v111, 21
	v_readlane_b32 s46, v113, 21
	v_readlane_b32 s47, v115, 21
	v_mul_f32_e32 v119, s98, v205
	v_fmac_f32_e32 v16, s4, v119
	v_fmac_f32_e32 v18, s5, v119
	v_fmac_f32_e32 v17, s8, v119
	v_fmac_f32_e32 v19, s33, v119
	v_fmac_f32_e32 v14, s34, v119
	v_fmac_f32_e32 v20, s35, v119
	v_fmac_f32_e32 v15, s46, v119
	v_fmac_f32_e32 v21, s47, v119
	s_waitcnt vmcnt(41)
	v_readlane_b32 s98, v117, 22
	v_readlane_b32 s4, v101, 22
	v_readlane_b32 s5, v103, 22
	v_readlane_b32 s8, v105, 22
	v_readlane_b32 s33, v107, 22
	v_readlane_b32 s34, v109, 22
	v_readlane_b32 s35, v111, 22
	v_readlane_b32 s46, v113, 22
	v_readlane_b32 s47, v115, 22
	v_mul_f32_e32 v119, s98, v206
	v_fmac_f32_e32 v16, s4, v119
	v_fmac_f32_e32 v18, s5, v119
	v_fmac_f32_e32 v17, s8, v119
	v_fmac_f32_e32 v19, s33, v119
	v_fmac_f32_e32 v14, s34, v119
	v_fmac_f32_e32 v20, s35, v119
	v_fmac_f32_e32 v15, s46, v119
	v_fmac_f32_e32 v21, s47, v119
	s_waitcnt vmcnt(40)
	v_readlane_b32 s98, v117, 23
	v_readlane_b32 s4, v101, 23
	v_readlane_b32 s5, v103, 23
	v_readlane_b32 s8, v105, 23
	v_readlane_b32 s33, v107, 23
	v_readlane_b32 s34, v109, 23
	v_readlane_b32 s35, v111, 23
	v_readlane_b32 s46, v113, 23
	v_readlane_b32 s47, v115, 23
	v_mul_f32_e32 v119, s98, v207
	v_fmac_f32_e32 v16, s4, v119
	v_fmac_f32_e32 v18, s5, v119
	v_fmac_f32_e32 v17, s8, v119
	v_fmac_f32_e32 v19, s33, v119
	v_fmac_f32_e32 v14, s34, v119
	v_fmac_f32_e32 v20, s35, v119
	v_fmac_f32_e32 v15, s46, v119
	v_fmac_f32_e32 v21, s47, v119
	s_waitcnt vmcnt(39)
	v_readlane_b32 s98, v117, 24
	v_readlane_b32 s4, v101, 24
	v_readlane_b32 s5, v103, 24
	v_readlane_b32 s8, v105, 24
	v_readlane_b32 s33, v107, 24
	v_readlane_b32 s34, v109, 24
	v_readlane_b32 s35, v111, 24
	v_readlane_b32 s46, v113, 24
	v_readlane_b32 s47, v115, 24
	v_mul_f32_e32 v119, s98, v208
	v_fmac_f32_e32 v16, s4, v119
	v_fmac_f32_e32 v18, s5, v119
	v_fmac_f32_e32 v17, s8, v119
	v_fmac_f32_e32 v19, s33, v119
	v_fmac_f32_e32 v14, s34, v119
	v_fmac_f32_e32 v20, s35, v119
	v_fmac_f32_e32 v15, s46, v119
	v_fmac_f32_e32 v21, s47, v119
	s_waitcnt vmcnt(38)
	v_readlane_b32 s98, v117, 25
	v_readlane_b32 s4, v101, 25
	v_readlane_b32 s5, v103, 25
	v_readlane_b32 s8, v105, 25
	v_readlane_b32 s33, v107, 25
	v_readlane_b32 s34, v109, 25
	v_readlane_b32 s35, v111, 25
	v_readlane_b32 s46, v113, 25
	v_readlane_b32 s47, v115, 25
	v_mul_f32_e32 v119, s98, v209
	v_fmac_f32_e32 v16, s4, v119
	v_fmac_f32_e32 v18, s5, v119
	v_fmac_f32_e32 v17, s8, v119
	v_fmac_f32_e32 v19, s33, v119
	v_fmac_f32_e32 v14, s34, v119
	v_fmac_f32_e32 v20, s35, v119
	v_fmac_f32_e32 v15, s46, v119
	v_fmac_f32_e32 v21, s47, v119
	s_waitcnt vmcnt(37)
; __device__ __forceinline__ void p0_prologue(const Args& a, const Frame& F) {
;     ...
;             for (int d = 0; d < 128; ++d) { const float wbv = wb[(size_t)d * 1024] * ps[d];
; #pragma unroll
;                 for (int cc = 0; cc < 8; ++cc) acc[cc] += wp[cc * 128 + d] * wbv; }
	v_readlane_b32 s98, v117, 26
	v_readlane_b32 s4, v101, 26
	v_readlane_b32 s5, v103, 26
	v_readlane_b32 s8, v105, 26
	v_readlane_b32 s33, v107, 26
	v_readlane_b32 s34, v109, 26
	v_readlane_b32 s35, v111, 26
	v_readlane_b32 s46, v113, 26
	v_readlane_b32 s47, v115, 26
	v_mul_f32_e32 v119, s98, v210
	v_fmac_f32_e32 v16, s4, v119
	v_fmac_f32_e32 v18, s5, v119
	v_fmac_f32_e32 v17, s8, v119
	v_fmac_f32_e32 v19, s33, v119
	v_fmac_f32_e32 v14, s34, v119
	v_fmac_f32_e32 v20, s35, v119
	v_fmac_f32_e32 v15, s46, v119
	v_fmac_f32_e32 v21, s47, v119
	s_waitcnt vmcnt(36)
	v_readlane_b32 s98, v117, 27
	v_readlane_b32 s4, v101, 27
	v_readlane_b32 s5, v103, 27
	v_readlane_b32 s8, v105, 27
	v_readlane_b32 s33, v107, 27
	v_readlane_b32 s34, v109, 27
	v_readlane_b32 s35, v111, 27
	v_readlane_b32 s46, v113, 27
	v_readlane_b32 s47, v115, 27
	v_mul_f32_e32 v119, s98, v211
	v_fmac_f32_e32 v16, s4, v119
	v_fmac_f32_e32 v18, s5, v119
	v_fmac_f32_e32 v17, s8, v119
	v_fmac_f32_e32 v19, s33, v119
	v_fmac_f32_e32 v14, s34, v119
	v_fmac_f32_e32 v20, s35, v119
	v_fmac_f32_e32 v15, s46, v119
	v_fmac_f32_e32 v21, s47, v119
	s_waitcnt vmcnt(35)
	v_readlane_b32 s98, v117, 28
	v_readlane_b32 s4, v101, 28
	v_readlane_b32 s5, v103, 28
	v_readlane_b32 s8, v105, 28
	v_readlane_b32 s33, v107, 28
	v_readlane_b32 s34, v109, 28
	v_readlane_b32 s35, v111, 28
	v_readlane_b32 s46, v113, 28
	v_readlane_b32 s47, v115, 28
	v_mul_f32_e32 v119, s98, v212
	v_fmac_f32_e32 v16, s4, v119
	v_fmac_f32_e32 v18, s5, v119
	v_fmac_f32_e32 v17, s8, v119
	v_fmac_f32_e32 v19, s33, v119
	v_fmac_f32_e32 v14, s34, v119
	v_fmac_f32_e32 v20, s35, v119
	v_fmac_f32_e32 v15, s46, v119
	v_fmac_f32_e32 v21, s47, v119
	s_waitcnt vmcnt(34)
	v_readlane_b32 s98, v117, 29
	v_readlane_b32 s4, v101, 29
	v_readlane_b32 s5, v103, 29
	v_readlane_b32 s8, v105, 29
	v_readlane_b32 s33, v107, 29
	v_readlane_b32 s34, v109, 29
	v_readlane_b32 s35, v111, 29
	v_readlane_b32 s46, v113, 29
	v_readlane_b32 s47, v115, 29
	v_mul_f32_e32 v119, s98, v213
	v_fmac_f32_e32 v16, s4, v119
	v_fmac_f32_e32 v18, s5, v119
	v_fmac_f32_e32 v17, s8, v119
	v_fmac_f32_e32 v19, s33, v119
	v_fmac_f32_e32 v14, s34, v119
	v_fmac_f32_e32 v20, s35, v119
	v_fmac_f32_e32 v15, s46, v119
	v_fmac_f32_e32 v21, s47, v119
	s_waitcnt vmcnt(33)
	v_readlane_b32 s98, v117, 30
	v_readlane_b32 s4, v101, 30
	v_readlane_b32 s5, v103, 30
	v_readlane_b32 s8, v105, 30
	v_readlane_b32 s33, v107, 30
	v_readlane_b32 s34, v109, 30
	v_readlane_b32 s35, v111, 30
	v_readlane_b32 s46, v113, 30
	v_readlane_b32 s47, v115, 30
	v_mul_f32_e32 v119, s98, v214
	v_fmac_f32_e32 v16, s4, v119
	v_fmac_f32_e32 v18, s5, v119
	v_fmac_f32_e32 v17, s8, v119
	v_fmac_f32_e32 v19, s33, v119
	v_fmac_f32_e32 v14, s34, v119
	v_fmac_f32_e32 v20, s35, v119
	v_fmac_f32_e32 v15, s46, v119
	v_fmac_f32_e32 v21, s47, v119
	s_waitcnt vmcnt(32)
	v_readlane_b32 s98, v117, 31
	v_readlane_b32 s4, v101, 31
	v_readlane_b32 s5, v103, 31
	v_readlane_b32 s8, v105, 31
	v_readlane_b32 s33, v107, 31
	v_readlane_b32 s34, v109, 31
	v_readlane_b32 s35, v111, 31
	v_readlane_b32 s46, v113, 31
	v_readlane_b32 s47, v115, 31
	v_mul_f32_e32 v119, s98, v215
	v_fmac_f32_e32 v16, s4, v119
	v_fmac_f32_e32 v18, s5, v119
	v_fmac_f32_e32 v17, s8, v119
	v_fmac_f32_e32 v19, s33, v119
	v_fmac_f32_e32 v14, s34, v119
	v_fmac_f32_e32 v20, s35, v119
	v_fmac_f32_e32 v15, s46, v119
	v_fmac_f32_e32 v21, s47, v119
	s_waitcnt vmcnt(31)
	v_readlane_b32 s98, v117, 32
	v_readlane_b32 s4, v101, 32
	v_readlane_b32 s5, v103, 32
	v_readlane_b32 s8, v105, 32
	v_readlane_b32 s33, v107, 32
	v_readlane_b32 s34, v109, 32
	v_readlane_b32 s35, v111, 32
	v_readlane_b32 s46, v113, 32
	v_readlane_b32 s47, v115, 32
	v_mul_f32_e32 v119, s98, v216
	v_fmac_f32_e32 v16, s4, v119
	v_fmac_f32_e32 v18, s5, v119
	v_fmac_f32_e32 v17, s8, v119
	v_fmac_f32_e32 v19, s33, v119
	v_fmac_f32_e32 v14, s34, v119
	v_fmac_f32_e32 v20, s35, v119
	v_fmac_f32_e32 v15, s46, v119
	v_fmac_f32_e32 v21, s47, v119
	s_waitcnt vmcnt(30)
	v_readlane_b32 s98, v117, 33
	v_readlane_b32 s4, v101, 33
	v_readlane_b32 s5, v103, 33
	v_readlane_b32 s8, v105, 33
	v_readlane_b32 s33, v107, 33
	v_readlane_b32 s34, v109, 33
	v_readlane_b32 s35, v111, 33
	v_readlane_b32 s46, v113, 33
	v_readlane_b32 s47, v115, 33
	v_mul_f32_e32 v119, s98, v217
	v_fmac_f32_e32 v16, s4, v119
	v_fmac_f32_e32 v18, s5, v119
	v_fmac_f32_e32 v17, s8, v119
	v_fmac_f32_e32 v19, s33, v119
	v_fmac_f32_e32 v14, s34, v119
	v_fmac_f32_e32 v20, s35, v119
	v_fmac_f32_e32 v15, s46, v119
	v_fmac_f32_e32 v21, s47, v119
	s_waitcnt vmcnt(29)
	v_readlane_b32 s98, v117, 34
	v_readlane_b32 s4, v101, 34
	v_readlane_b32 s5, v103, 34
	v_readlane_b32 s8, v105, 34
	v_readlane_b32 s33, v107, 34
	v_readlane_b32 s34, v109, 34
	v_readlane_b32 s35, v111, 34
	v_readlane_b32 s46, v113, 34
	v_readlane_b32 s47, v115, 34
	v_mul_f32_e32 v119, s98, v218
	v_fmac_f32_e32 v16, s4, v119
	v_fmac_f32_e32 v18, s5, v119
	v_fmac_f32_e32 v17, s8, v119
	v_fmac_f32_e32 v19, s33, v119
	v_fmac_f32_e32 v14, s34, v119
	v_fmac_f32_e32 v20, s35, v119
	v_fmac_f32_e32 v15, s46, v119
	v_fmac_f32_e32 v21, s47, v119
	s_waitcnt vmcnt(28)
	v_readlane_b32 s98, v117, 35
	v_readlane_b32 s4, v101, 35
	v_readlane_b32 s5, v103, 35
	v_readlane_b32 s8, v105, 35
	v_readlane_b32 s33, v107, 35
	v_readlane_b32 s34, v109, 35
	v_readlane_b32 s35, v111, 35
	v_readlane_b32 s46, v113, 35
	v_readlane_b32 s47, v115, 35
	v_mul_f32_e32 v119, s98, v219
	v_fmac_f32_e32 v16, s4, v119
	v_fmac_f32_e32 v18, s5, v119
	v_fmac_f32_e32 v17, s8, v119
	v_fmac_f32_e32 v19, s33, v119
	v_fmac_f32_e32 v14, s34, v119
	v_fmac_f32_e32 v20, s35, v119
	v_fmac_f32_e32 v15, s46, v119
	v_fmac_f32_e32 v21, s47, v119
	s_waitcnt vmcnt(27)
; __device__ __forceinline__ void p0_prologue(const Args& a, const Frame& F) {
;     ...
;             for (int d = 0; d < 128; ++d) { const float wbv = wb[(size_t)d * 1024] * ps[d];
; #pragma unroll
;                 for (int cc = 0; cc < 8; ++cc) acc[cc] += wp[cc * 128 + d] * wbv; }
	v_readlane_b32 s98, v117, 36
	v_readlane_b32 s4, v101, 36
	v_readlane_b32 s5, v103, 36
	v_readlane_b32 s8, v105, 36
	v_readlane_b32 s33, v107, 36
	v_readlane_b32 s34, v109, 36
	v_readlane_b32 s35, v111, 36
	v_readlane_b32 s46, v113, 36
	v_readlane_b32 s47, v115, 36
	v_mul_f32_e32 v119, s98, v220
	v_fmac_f32_e32 v16, s4, v119
	v_fmac_f32_e32 v18, s5, v119
	v_fmac_f32_e32 v17, s8, v119
	v_fmac_f32_e32 v19, s33, v119
	v_fmac_f32_e32 v14, s34, v119
	v_fmac_f32_e32 v20, s35, v119
	v_fmac_f32_e32 v15, s46, v119
	v_fmac_f32_e32 v21, s47, v119
	s_waitcnt vmcnt(26)
	v_readlane_b32 s98, v117, 37
	v_readlane_b32 s4, v101, 37
	v_readlane_b32 s5, v103, 37
	v_readlane_b32 s8, v105, 37
	v_readlane_b32 s33, v107, 37
	v_readlane_b32 s34, v109, 37
	v_readlane_b32 s35, v111, 37
	v_readlane_b32 s46, v113, 37
	v_readlane_b32 s47, v115, 37
	v_mul_f32_e32 v119, s98, v221
	v_fmac_f32_e32 v16, s4, v119
	v_fmac_f32_e32 v18, s5, v119
	v_fmac_f32_e32 v17, s8, v119
	v_fmac_f32_e32 v19, s33, v119
	v_fmac_f32_e32 v14, s34, v119
	v_fmac_f32_e32 v20, s35, v119
	v_fmac_f32_e32 v15, s46, v119
	v_fmac_f32_e32 v21, s47, v119
	s_waitcnt vmcnt(25)
	v_readlane_b32 s98, v117, 38
	v_readlane_b32 s4, v101, 38
	v_readlane_b32 s5, v103, 38
	v_readlane_b32 s8, v105, 38
	v_readlane_b32 s33, v107, 38
	v_readlane_b32 s34, v109, 38
	v_readlane_b32 s35, v111, 38
	v_readlane_b32 s46, v113, 38
	v_readlane_b32 s47, v115, 38
	v_mul_f32_e32 v119, s98, v222
	v_fmac_f32_e32 v16, s4, v119
	v_fmac_f32_e32 v18, s5, v119
	v_fmac_f32_e32 v17, s8, v119
	v_fmac_f32_e32 v19, s33, v119
	v_fmac_f32_e32 v14, s34, v119
	v_fmac_f32_e32 v20, s35, v119
	v_fmac_f32_e32 v15, s46, v119
	v_fmac_f32_e32 v21, s47, v119
	s_waitcnt vmcnt(24)
	v_readlane_b32 s98, v117, 39
	v_readlane_b32 s4, v101, 39
	v_readlane_b32 s5, v103, 39
	v_readlane_b32 s8, v105, 39
	v_readlane_b32 s33, v107, 39
	v_readlane_b32 s34, v109, 39
	v_readlane_b32 s35, v111, 39
	v_readlane_b32 s46, v113, 39
	v_readlane_b32 s47, v115, 39
	v_mul_f32_e32 v119, s98, v223
	v_fmac_f32_e32 v16, s4, v119
	v_fmac_f32_e32 v18, s5, v119
	v_fmac_f32_e32 v17, s8, v119
	v_fmac_f32_e32 v19, s33, v119
	v_fmac_f32_e32 v14, s34, v119
	v_fmac_f32_e32 v20, s35, v119
	v_fmac_f32_e32 v15, s46, v119
	v_fmac_f32_e32 v21, s47, v119
	s_waitcnt vmcnt(23)
	v_readlane_b32 s98, v117, 40
	v_readlane_b32 s4, v101, 40
	v_readlane_b32 s5, v103, 40
	v_readlane_b32 s8, v105, 40
	v_readlane_b32 s33, v107, 40
	v_readlane_b32 s34, v109, 40
	v_readlane_b32 s35, v111, 40
	v_readlane_b32 s46, v113, 40
	v_readlane_b32 s47, v115, 40
	v_mul_f32_e32 v119, s98, v224
	v_fmac_f32_e32 v16, s4, v119
	v_fmac_f32_e32 v18, s5, v119
	v_fmac_f32_e32 v17, s8, v119
	v_fmac_f32_e32 v19, s33, v119
	v_fmac_f32_e32 v14, s34, v119
	v_fmac_f32_e32 v20, s35, v119
	v_fmac_f32_e32 v15, s46, v119
	v_fmac_f32_e32 v21, s47, v119
	s_waitcnt vmcnt(22)
	v_readlane_b32 s98, v117, 41
	v_readlane_b32 s4, v101, 41
	v_readlane_b32 s5, v103, 41
	v_readlane_b32 s8, v105, 41
	v_readlane_b32 s33, v107, 41
	v_readlane_b32 s34, v109, 41
	v_readlane_b32 s35, v111, 41
	v_readlane_b32 s46, v113, 41
	v_readlane_b32 s47, v115, 41
	v_mul_f32_e32 v119, s98, v225
	v_fmac_f32_e32 v16, s4, v119
	v_fmac_f32_e32 v18, s5, v119
	v_fmac_f32_e32 v17, s8, v119
	v_fmac_f32_e32 v19, s33, v119
	v_fmac_f32_e32 v14, s34, v119
	v_fmac_f32_e32 v20, s35, v119
	v_fmac_f32_e32 v15, s46, v119
	v_fmac_f32_e32 v21, s47, v119
	s_waitcnt vmcnt(21)
	v_readlane_b32 s98, v117, 42
	v_readlane_b32 s4, v101, 42
	v_readlane_b32 s5, v103, 42
	v_readlane_b32 s8, v105, 42
	v_readlane_b32 s33, v107, 42
	v_readlane_b32 s34, v109, 42
	v_readlane_b32 s35, v111, 42
	v_readlane_b32 s46, v113, 42
	v_readlane_b32 s47, v115, 42
	v_mul_f32_e32 v119, s98, v226
	v_fmac_f32_e32 v16, s4, v119
	v_fmac_f32_e32 v18, s5, v119
	v_fmac_f32_e32 v17, s8, v119
	v_fmac_f32_e32 v19, s33, v119
	v_fmac_f32_e32 v14, s34, v119
	v_fmac_f32_e32 v20, s35, v119
	v_fmac_f32_e32 v15, s46, v119
	v_fmac_f32_e32 v21, s47, v119
	s_waitcnt vmcnt(20)
	v_readlane_b32 s98, v117, 43
	v_readlane_b32 s4, v101, 43
	v_readlane_b32 s5, v103, 43
	v_readlane_b32 s8, v105, 43
	v_readlane_b32 s33, v107, 43
	v_readlane_b32 s34, v109, 43
	v_readlane_b32 s35, v111, 43
	v_readlane_b32 s46, v113, 43
	v_readlane_b32 s47, v115, 43
	v_mul_f32_e32 v119, s98, v227
	v_fmac_f32_e32 v16, s4, v119
	v_fmac_f32_e32 v18, s5, v119
	v_fmac_f32_e32 v17, s8, v119
	v_fmac_f32_e32 v19, s33, v119
	v_fmac_f32_e32 v14, s34, v119
	v_fmac_f32_e32 v20, s35, v119
	v_fmac_f32_e32 v15, s46, v119
	v_fmac_f32_e32 v21, s47, v119
	s_waitcnt vmcnt(19)
	v_readlane_b32 s98, v117, 44
	v_readlane_b32 s4, v101, 44
	v_readlane_b32 s5, v103, 44
	v_readlane_b32 s8, v105, 44
	v_readlane_b32 s33, v107, 44
	v_readlane_b32 s34, v109, 44
	v_readlane_b32 s35, v111, 44
	v_readlane_b32 s46, v113, 44
	v_readlane_b32 s47, v115, 44
	v_mul_f32_e32 v119, s98, v228
	v_fmac_f32_e32 v16, s4, v119
	v_fmac_f32_e32 v18, s5, v119
	v_fmac_f32_e32 v17, s8, v119
	v_fmac_f32_e32 v19, s33, v119
	v_fmac_f32_e32 v14, s34, v119
	v_fmac_f32_e32 v20, s35, v119
	v_fmac_f32_e32 v15, s46, v119
	v_fmac_f32_e32 v21, s47, v119
	s_waitcnt vmcnt(18)
	v_readlane_b32 s98, v117, 45
	v_readlane_b32 s4, v101, 45
	v_readlane_b32 s5, v103, 45
	v_readlane_b32 s8, v105, 45
	v_readlane_b32 s33, v107, 45
	v_readlane_b32 s34, v109, 45
	v_readlane_b32 s35, v111, 45
	v_readlane_b32 s46, v113, 45
	v_readlane_b32 s47, v115, 45
	v_mul_f32_e32 v119, s98, v229
	v_fmac_f32_e32 v16, s4, v119
	v_fmac_f32_e32 v18, s5, v119
	v_fmac_f32_e32 v17, s8, v119
	v_fmac_f32_e32 v19, s33, v119
	v_fmac_f32_e32 v14, s34, v119
	v_fmac_f32_e32 v20, s35, v119
	v_fmac_f32_e32 v15, s46, v119
	v_fmac_f32_e32 v21, s47, v119
	s_waitcnt vmcnt(17)
; __device__ __forceinline__ void p0_prologue(const Args& a, const Frame& F) {
;     ...
;             for (int d = 0; d < 128; ++d) { const float wbv = wb[(size_t)d * 1024] * ps[d];
; #pragma unroll
;                 for (int cc = 0; cc < 8; ++cc) acc[cc] += wp[cc * 128 + d] * wbv; }
	v_readlane_b32 s98, v117, 46
	v_readlane_b32 s4, v101, 46
	v_readlane_b32 s5, v103, 46
	v_readlane_b32 s8, v105, 46
	v_readlane_b32 s33, v107, 46
	v_readlane_b32 s34, v109, 46
	v_readlane_b32 s35, v111, 46
	v_readlane_b32 s46, v113, 46
	v_readlane_b32 s47, v115, 46
	v_mul_f32_e32 v119, s98, v230
	v_fmac_f32_e32 v16, s4, v119
	v_fmac_f32_e32 v18, s5, v119
	v_fmac_f32_e32 v17, s8, v119
	v_fmac_f32_e32 v19, s33, v119
	v_fmac_f32_e32 v14, s34, v119
	v_fmac_f32_e32 v20, s35, v119
	v_fmac_f32_e32 v15, s46, v119
	v_fmac_f32_e32 v21, s47, v119
	s_waitcnt vmcnt(16)
	v_readlane_b32 s98, v117, 47
	v_readlane_b32 s4, v101, 47
	v_readlane_b32 s5, v103, 47
	v_readlane_b32 s8, v105, 47
	v_readlane_b32 s33, v107, 47
	v_readlane_b32 s34, v109, 47
	v_readlane_b32 s35, v111, 47
	v_readlane_b32 s46, v113, 47
	v_readlane_b32 s47, v115, 47
	v_mul_f32_e32 v119, s98, v231
	v_fmac_f32_e32 v16, s4, v119
	v_fmac_f32_e32 v18, s5, v119
	v_fmac_f32_e32 v17, s8, v119
	v_fmac_f32_e32 v19, s33, v119
	v_fmac_f32_e32 v14, s34, v119
	v_fmac_f32_e32 v20, s35, v119
	v_fmac_f32_e32 v15, s46, v119
	v_fmac_f32_e32 v21, s47, v119
	s_waitcnt vmcnt(15)
	v_readlane_b32 s98, v117, 48
	v_readlane_b32 s4, v101, 48
	v_readlane_b32 s5, v103, 48
	v_readlane_b32 s8, v105, 48
	v_readlane_b32 s33, v107, 48
	v_readlane_b32 s34, v109, 48
	v_readlane_b32 s35, v111, 48
	v_readlane_b32 s46, v113, 48
	v_readlane_b32 s47, v115, 48
	v_mul_f32_e32 v119, s98, v232
	v_fmac_f32_e32 v16, s4, v119
	v_fmac_f32_e32 v18, s5, v119
	v_fmac_f32_e32 v17, s8, v119
	v_fmac_f32_e32 v19, s33, v119
	v_fmac_f32_e32 v14, s34, v119
	v_fmac_f32_e32 v20, s35, v119
	v_fmac_f32_e32 v15, s46, v119
	v_fmac_f32_e32 v21, s47, v119
	s_waitcnt vmcnt(14)
	v_readlane_b32 s98, v117, 49
	v_readlane_b32 s4, v101, 49
	v_readlane_b32 s5, v103, 49
	v_readlane_b32 s8, v105, 49
	v_readlane_b32 s33, v107, 49
	v_readlane_b32 s34, v109, 49
	v_readlane_b32 s35, v111, 49
	v_readlane_b32 s46, v113, 49
	v_readlane_b32 s47, v115, 49
	v_mul_f32_e32 v119, s98, v233
	v_fmac_f32_e32 v16, s4, v119
	v_fmac_f32_e32 v18, s5, v119
	v_fmac_f32_e32 v17, s8, v119
	v_fmac_f32_e32 v19, s33, v119
	v_fmac_f32_e32 v14, s34, v119
	v_fmac_f32_e32 v20, s35, v119
	v_fmac_f32_e32 v15, s46, v119
	v_fmac_f32_e32 v21, s47, v119
	s_waitcnt vmcnt(13)
	v_readlane_b32 s98, v117, 50
	v_readlane_b32 s4, v101, 50
	v_readlane_b32 s5, v103, 50
	v_readlane_b32 s8, v105, 50
	v_readlane_b32 s33, v107, 50
	v_readlane_b32 s34, v109, 50
	v_readlane_b32 s35, v111, 50
	v_readlane_b32 s46, v113, 50
	v_readlane_b32 s47, v115, 50
	v_mul_f32_e32 v119, s98, v234
	v_fmac_f32_e32 v16, s4, v119
	v_fmac_f32_e32 v18, s5, v119
	v_fmac_f32_e32 v17, s8, v119
	v_fmac_f32_e32 v19, s33, v119
	v_fmac_f32_e32 v14, s34, v119
	v_fmac_f32_e32 v20, s35, v119
	v_fmac_f32_e32 v15, s46, v119
	v_fmac_f32_e32 v21, s47, v119
	s_waitcnt vmcnt(12)
	v_readlane_b32 s98, v117, 51
	v_readlane_b32 s4, v101, 51
	v_readlane_b32 s5, v103, 51
	v_readlane_b32 s8, v105, 51
	v_readlane_b32 s33, v107, 51
	v_readlane_b32 s34, v109, 51
	v_readlane_b32 s35, v111, 51
	v_readlane_b32 s46, v113, 51
	v_readlane_b32 s47, v115, 51
	v_mul_f32_e32 v119, s98, v235
	v_fmac_f32_e32 v16, s4, v119
	v_fmac_f32_e32 v18, s5, v119
	v_fmac_f32_e32 v17, s8, v119
	v_fmac_f32_e32 v19, s33, v119
	v_fmac_f32_e32 v14, s34, v119
	v_fmac_f32_e32 v20, s35, v119
	v_fmac_f32_e32 v15, s46, v119
	v_fmac_f32_e32 v21, s47, v119
	s_waitcnt vmcnt(11)
	v_readlane_b32 s98, v117, 52
	v_readlane_b32 s4, v101, 52
	v_readlane_b32 s5, v103, 52
	v_readlane_b32 s8, v105, 52
	v_readlane_b32 s33, v107, 52
	v_readlane_b32 s34, v109, 52
	v_readlane_b32 s35, v111, 52
	v_readlane_b32 s46, v113, 52
	v_readlane_b32 s47, v115, 52
	v_mul_f32_e32 v119, s98, v236
	v_fmac_f32_e32 v16, s4, v119
	v_fmac_f32_e32 v18, s5, v119
	v_fmac_f32_e32 v17, s8, v119
	v_fmac_f32_e32 v19, s33, v119
	v_fmac_f32_e32 v14, s34, v119
	v_fmac_f32_e32 v20, s35, v119
	v_fmac_f32_e32 v15, s46, v119
	v_fmac_f32_e32 v21, s47, v119
	s_waitcnt vmcnt(10)
	v_readlane_b32 s98, v117, 53
	v_readlane_b32 s4, v101, 53
	v_readlane_b32 s5, v103, 53
	v_readlane_b32 s8, v105, 53
	v_readlane_b32 s33, v107, 53
	v_readlane_b32 s34, v109, 53
	v_readlane_b32 s35, v111, 53
	v_readlane_b32 s46, v113, 53
	v_readlane_b32 s47, v115, 53
	v_mul_f32_e32 v119, s98, v237
	v_fmac_f32_e32 v16, s4, v119
	v_fmac_f32_e32 v18, s5, v119
	v_fmac_f32_e32 v17, s8, v119
	v_fmac_f32_e32 v19, s33, v119
	v_fmac_f32_e32 v14, s34, v119
	v_fmac_f32_e32 v20, s35, v119
	v_fmac_f32_e32 v15, s46, v119
	v_fmac_f32_e32 v21, s47, v119
	s_waitcnt vmcnt(9)
	v_readlane_b32 s98, v117, 54
	v_readlane_b32 s4, v101, 54
	v_readlane_b32 s5, v103, 54
	v_readlane_b32 s8, v105, 54
	v_readlane_b32 s33, v107, 54
	v_readlane_b32 s34, v109, 54
	v_readlane_b32 s35, v111, 54
	v_readlane_b32 s46, v113, 54
	v_readlane_b32 s47, v115, 54
	v_mul_f32_e32 v119, s98, v238
	v_fmac_f32_e32 v16, s4, v119
	v_fmac_f32_e32 v18, s5, v119
	v_fmac_f32_e32 v17, s8, v119
	v_fmac_f32_e32 v19, s33, v119
	v_fmac_f32_e32 v14, s34, v119
	v_fmac_f32_e32 v20, s35, v119
	v_fmac_f32_e32 v15, s46, v119
	v_fmac_f32_e32 v21, s47, v119
	s_waitcnt vmcnt(8)
	v_readlane_b32 s98, v117, 55
	v_readlane_b32 s4, v101, 55
	v_readlane_b32 s5, v103, 55
	v_readlane_b32 s8, v105, 55
	v_readlane_b32 s33, v107, 55
	v_readlane_b32 s34, v109, 55
	v_readlane_b32 s35, v111, 55
	v_readlane_b32 s46, v113, 55
	v_readlane_b32 s47, v115, 55
	v_mul_f32_e32 v119, s98, v239
	v_fmac_f32_e32 v16, s4, v119
	v_fmac_f32_e32 v18, s5, v119
	v_fmac_f32_e32 v17, s8, v119
	v_fmac_f32_e32 v19, s33, v119
	v_fmac_f32_e32 v14, s34, v119
	v_fmac_f32_e32 v20, s35, v119
	v_fmac_f32_e32 v15, s46, v119
	v_fmac_f32_e32 v21, s47, v119
	s_waitcnt vmcnt(7)
; __device__ __forceinline__ unsigned pk2(float lo, float hi) { return f2bf(lo) | (f2bf(hi) << 16); }
; __device__ __forceinline__ void p0_prologue(const Args& a, const Frame& F) {
;     ...
;             for (int d = 0; d < 128; ++d) { const float wbv = wb[(size_t)d * 1024] * ps[d];
; #pragma unroll
;                 for (int cc = 0; cc < 8; ++cc) acc[cc] += wp[cc * 128 + d] * wbv; }
;             u32x4 o; o.x = pk2(acc[0], acc[1]); o.y = pk2(acc[2], acc[3]); o.z = pk2(acc[4], acc[5]); o.w = pk2(acc[6], acc[7]);
;             *(u32x4*)((bf16*)(ws + WS_WPA_T) + (size_t)n * 512 + k0) = o;
	v_readlane_b32 s98, v117, 56
	v_readlane_b32 s4, v101, 56
	v_readlane_b32 s5, v103, 56
	v_readlane_b32 s8, v105, 56
	v_readlane_b32 s33, v107, 56
	v_readlane_b32 s34, v109, 56
	v_readlane_b32 s35, v111, 56
	v_readlane_b32 s46, v113, 56
	v_readlane_b32 s47, v115, 56
	v_mul_f32_e32 v119, s98, v240
	v_fmac_f32_e32 v16, s4, v119
	v_fmac_f32_e32 v18, s5, v119
	v_fmac_f32_e32 v17, s8, v119
	v_fmac_f32_e32 v19, s33, v119
	v_fmac_f32_e32 v14, s34, v119
	v_fmac_f32_e32 v20, s35, v119
	v_fmac_f32_e32 v15, s46, v119
	v_fmac_f32_e32 v21, s47, v119
	s_waitcnt vmcnt(6)
	v_readlane_b32 s98, v117, 57
	v_readlane_b32 s4, v101, 57
	v_readlane_b32 s5, v103, 57
	v_readlane_b32 s8, v105, 57
	v_readlane_b32 s33, v107, 57
	v_readlane_b32 s34, v109, 57
	v_readlane_b32 s35, v111, 57
	v_readlane_b32 s46, v113, 57
	v_readlane_b32 s47, v115, 57
	v_mul_f32_e32 v119, s98, v241
	v_fmac_f32_e32 v16, s4, v119
	v_fmac_f32_e32 v18, s5, v119
	v_fmac_f32_e32 v17, s8, v119
	v_fmac_f32_e32 v19, s33, v119
	v_fmac_f32_e32 v14, s34, v119
	v_fmac_f32_e32 v20, s35, v119
	v_fmac_f32_e32 v15, s46, v119
	v_fmac_f32_e32 v21, s47, v119
	s_waitcnt vmcnt(5)
	v_readlane_b32 s98, v117, 58
	v_readlane_b32 s4, v101, 58
	v_readlane_b32 s5, v103, 58
	v_readlane_b32 s8, v105, 58
	v_readlane_b32 s33, v107, 58
	v_readlane_b32 s34, v109, 58
	v_readlane_b32 s35, v111, 58
	v_readlane_b32 s46, v113, 58
	v_readlane_b32 s47, v115, 58
	v_mul_f32_e32 v119, s98, v242
	v_fmac_f32_e32 v16, s4, v119
	v_fmac_f32_e32 v18, s5, v119
	v_fmac_f32_e32 v17, s8, v119
	v_fmac_f32_e32 v19, s33, v119
	v_fmac_f32_e32 v14, s34, v119
	v_fmac_f32_e32 v20, s35, v119
	v_fmac_f32_e32 v15, s46, v119
	v_fmac_f32_e32 v21, s47, v119
	s_waitcnt vmcnt(4)
	v_readlane_b32 s98, v117, 59
	v_readlane_b32 s4, v101, 59
	v_readlane_b32 s5, v103, 59
	v_readlane_b32 s8, v105, 59
	v_readlane_b32 s33, v107, 59
	v_readlane_b32 s34, v109, 59
	v_readlane_b32 s35, v111, 59
	v_readlane_b32 s46, v113, 59
	v_readlane_b32 s47, v115, 59
	v_mul_f32_e32 v119, s98, v243
	v_fmac_f32_e32 v16, s4, v119
	v_fmac_f32_e32 v18, s5, v119
	v_fmac_f32_e32 v17, s8, v119
	v_fmac_f32_e32 v19, s33, v119
	v_fmac_f32_e32 v14, s34, v119
	v_fmac_f32_e32 v20, s35, v119
	v_fmac_f32_e32 v15, s46, v119
	v_fmac_f32_e32 v21, s47, v119
	s_waitcnt vmcnt(3)
	v_readlane_b32 s98, v117, 60
	v_readlane_b32 s4, v101, 60
	v_readlane_b32 s5, v103, 60
	v_readlane_b32 s8, v105, 60
	v_readlane_b32 s33, v107, 60
	v_readlane_b32 s34, v109, 60
	v_readlane_b32 s35, v111, 60
	v_readlane_b32 s46, v113, 60
	v_readlane_b32 s47, v115, 60
	v_mul_f32_e32 v119, s98, v244
	v_fmac_f32_e32 v16, s4, v119
	v_fmac_f32_e32 v18, s5, v119
	v_fmac_f32_e32 v17, s8, v119
	v_fmac_f32_e32 v19, s33, v119
	v_fmac_f32_e32 v14, s34, v119
	v_fmac_f32_e32 v20, s35, v119
	v_fmac_f32_e32 v15, s46, v119
	v_fmac_f32_e32 v21, s47, v119
	s_waitcnt vmcnt(2)
	v_readlane_b32 s98, v117, 61
	v_readlane_b32 s4, v101, 61
	v_readlane_b32 s5, v103, 61
	v_readlane_b32 s8, v105, 61
	v_readlane_b32 s33, v107, 61
	v_readlane_b32 s34, v109, 61
	v_readlane_b32 s35, v111, 61
	v_readlane_b32 s46, v113, 61
	v_readlane_b32 s47, v115, 61
	v_mul_f32_e32 v119, s98, v245
	v_fmac_f32_e32 v16, s4, v119
	v_fmac_f32_e32 v18, s5, v119
	v_fmac_f32_e32 v17, s8, v119
	v_fmac_f32_e32 v19, s33, v119
	v_fmac_f32_e32 v14, s34, v119
	v_fmac_f32_e32 v20, s35, v119
	v_fmac_f32_e32 v15, s46, v119
	v_fmac_f32_e32 v21, s47, v119
	s_waitcnt vmcnt(1)
	v_readlane_b32 s98, v117, 62
	v_readlane_b32 s4, v101, 62
	v_readlane_b32 s5, v103, 62
	v_readlane_b32 s8, v105, 62
	v_readlane_b32 s33, v107, 62
	v_readlane_b32 s34, v109, 62
	v_readlane_b32 s35, v111, 62
	v_readlane_b32 s46, v113, 62
	v_readlane_b32 s47, v115, 62
	v_mul_f32_e32 v119, s98, v246
	v_fmac_f32_e32 v16, s4, v119
	v_fmac_f32_e32 v18, s5, v119
	v_fmac_f32_e32 v17, s8, v119
	v_fmac_f32_e32 v19, s33, v119
	v_fmac_f32_e32 v14, s34, v119
	v_fmac_f32_e32 v20, s35, v119
	v_fmac_f32_e32 v15, s46, v119
	v_fmac_f32_e32 v21, s47, v119
	s_waitcnt vmcnt(0)
	v_readlane_b32 s98, v117, 63
	v_readlane_b32 s4, v101, 63
	v_readlane_b32 s5, v103, 63
	v_readlane_b32 s8, v105, 63
	v_readlane_b32 s33, v107, 63
	v_readlane_b32 s34, v109, 63
	v_readlane_b32 s35, v111, 63
	v_readlane_b32 s46, v113, 63
	v_readlane_b32 s47, v115, 63
	v_mul_f32_e32 v119, s98, v247
	v_fmac_f32_e32 v16, s4, v119
	v_fmac_f32_e32 v18, s5, v119
	v_fmac_f32_e32 v17, s8, v119
	v_fmac_f32_e32 v19, s33, v119
	v_fmac_f32_e32 v14, s34, v119
	v_fmac_f32_e32 v20, s35, v119
	v_fmac_f32_e32 v15, s46, v119
	v_fmac_f32_e32 v21, s47, v119
	s_lshl_b32 s4, s77, 6
	v_bfe_u32 v12, v21, 16, 1
	v_bfe_u32 v13, v20, 16, 1
	v_bfe_u32 v22, v19, 16, 1
	v_bfe_u32 v23, v18, 16, 1
	s_and_b32 s4, s4, 0x3c0
	v_add3_u32 v18, v18, v23, s90
	v_add3_u32 v19, v19, v22, s90
	v_add3_u32 v13, v20, v13, s90
	v_add3_u32 v12, v21, v12, s90
	v_bfe_u32 v20, v16, 16, 1
	v_bfe_u32 v21, v17, 16, 1
	v_bfe_u32 v22, v14, 16, 1
	v_bfe_u32 v23, v15, 16, 1
	v_or_b32_e32 v2, s4, v252
	v_add3_u32 v15, v15, v23, s90
	v_add3_u32 v14, v14, v22, s90
	v_add3_u32 v17, v17, v21, s90
	v_add3_u32 v16, v16, v20, s90
	v_lshrrev_b32_e32 v16, 16, v16
	v_lshrrev_b32_e32 v17, 16, v17
	v_lshrrev_b32_e32 v14, 16, v14
	v_lshrrev_b32_e32 v15, 16, v15
	v_lshlrev_b32_e32 v2, 10, v2
	v_and_or_b32 v15, v12, s91, v15
	v_and_or_b32 v14, v13, s91, v14
	v_and_or_b32 v13, v19, s91, v17
	v_and_or_b32 v12, v18, s91, v16
	v_lshl_add_u64 v[16:17], s[10:11], 0, v[2:3]
	v_lshl_add_u64 v[16:17], s[0:1], 1, v[16:17]
	global_store_dwordx4 v[16:17], v[12:15], off
	s_branch .LBB0_24
